# LDS-DMA address form: SGPR base + 32-bit VGPR offset (saddr) at 138 global_load_lds sites instead of a 64-bit v_lshl_add_u64 per DMA (98 adds removed)
# speedup vs baseline: 1.0039x; 1.0010x over previous
; #define PG8_STAGE(bufoff, gbase, voff) do { _Pragma("unroll") for (int _i = 0; _i < 2; ++_i) \
;         __builtin_amdgcn_global_load_lds((const unsigned*)((const char*)(gbase) + (voff)[_i]), (PG8_LAS unsigned*)(lds + (bufoff) + ldsw + _i * 8192), 16, 0, 0); } while (0)
; #define PG8_WAIT_V(n) asm volatile("s_waitcnt vmcnt(" #n ")" ::: "memory")
; #define PG8_BAR __builtin_amdgcn_s_barrier()
; template <class Epi, class Sched, bool ALIGN_EPI = false, bool SP2 = false, bool FP8 = false, bool ABLK = false>
; __device__ __forceinline__ void gemm_phase(PG8_LAS unsigned char* lds, const Gemm g, const Sched& S, const Epi& E) {
;     ...
;     for (int i = 0; i < 2; ++i) { int R, C; stage_rc(tid * 16 + i * 8192, R, C); const int Rb = Epi::PERM ? ((R & ~31) + perm32(R & 31)) : R;
;         voffA[i] = ABLK ? (unsigned)(((((R >> 6) * 4 + (C >> 4)) * 8 + ((R >> 4) & 3)) * 64 + ((C >> 3) & 1) * 32 + (R & 15) * 2) * 8) : (unsigned)(R * K + C) * 2u; voffB[i] = (unsigned)(Rb * K + C) * 2u; }
;     const size_t kstep = (size_t)(BK * 2);
;     const size_t hstep = (size_t)HALF * K * 2;
;     const size_t kstepA = ABLK ? (size_t)32768 : kstep, hstepA = ABLK ? (size_t)2048 : hstep;
;     const size_t tstep = 2 * hstep;
;     const unsigned ldsw = (unsigned)wid * 1024u;
;     const int aoff = lds_byte(wr * 64 + fr, fq * 8), boff = lds_byte(wc * 32 + fr, fq * 8);
;     ...
;         PG8_STAGE(PG8_SB(0, 0), cB, voffB); PG8_STAGE(PG8_SB(0, 1), cB + hstep, voffB); PG8_STAGE(PG8_SA(0, 0), cA, voffA); PG8_STAGE(PG8_SA(0, 1), cA + hstepA, voffA);
;         if (wr == 1) PG8_BAR;
;         PG8_WAIT_V(2); PG8_BAR;
;         PG8_STAGE(PG8_SB(1, 0), cB + kstep, voffB); PG8_STAGE(PG8_SA(1, 0), cA + kstepA, voffA); PG8_STAGE(PG8_SB(1, 1), cB + hstep + kstep, voffB);
;         PG8_WAIT_V(0); PG8_BAR;
.LBB0_425:
	s_add_u32 s22, s38, 0xba00000
	s_addc_u32 s23, s39, 0
	s_add_u32 s48, s38, 0x1c000000
	s_addc_u32 s49, s39, 0
	s_and_b32 s5, s5, 3
	s_add_i32 m0, s18, 0x18000
	v_lshl_add_u64 v[10:11], v[10:11], 0, s[34:35]
	s_lshl_b32 s47, s4, 6
	s_lshl_b32 s51, s4, 13
	s_lshl_b32 s52, s5, 12
	s_waitcnt vmcnt(2)
	s_barrier
	global_load_lds_dwordx4 v[10:11], off
	v_lshl_add_u64 v[8:9], v[8:9], 0, s[34:35]
	s_add_i32 m0, s18, 0x1a000
	s_add_i32 s66, s18, 0x8000
	s_add_i32 s67, s18, 0xa000
	global_load_lds_dwordx4 v[8:9], off
	v_lshl_add_u64 v[4:5], v[4:5], 0, s[34:35]
	s_mov_b32 m0, s66
	s_add_u32 s38, s62, 0x40080
	global_load_lds_dwordx4 v[4:5], off
	v_lshl_add_u64 v[4:5], v[6:7], 0, s[34:35]
	s_mov_b32 m0, s67
	s_addc_u32 s39, s63, 0
	global_load_lds_dwordx4 v[4:5], off
	s_add_i32 m0, s18, 0x1c000
	s_nop 0
	global_load_lds_dwordx4 v2, s[38:39]
	s_add_i32 m0, s18, 0x1e000
	v_bfe_u32 v164, v12, 4, 2
	global_load_lds_dwordx4 v152, s[38:39]
	v_and_b32_e32 v1, 15, v12
	v_lshlrev_b32_e32 v4, 4, v164
	v_lshlrev_b32_e32 v5, 2, v12
	v_lshl_or_b32 v4, v1, 6, v4
	v_and_b32_e32 v5, 32, v5
	v_bitop3_b32 v6, v4, s51, v5 bitop3:0xde
	v_bitop3_b32 v165, v4, s52, v5 bitop3:0xde
	v_lshlrev_b32_e32 v4, 14, v17
	v_and_b32_e32 v4, 0xffff8000, v4
	v_lshl_add_u32 v4, v16, 11, v4
	v_and_b32_e32 v5, 1, v17
	v_lshl_or_b32 v4, v5, 6, v4
	v_lshl_add_u32 v158, v18, 1, v4
	v_lshlrev_b32_e32 v4, 14, v13
	s_cmpk_lt_u32 s50, 0x100
	v_and_b32_e32 v4, 0xffff8000, v4
	s_waitcnt vmcnt(0)
	s_cselect_b64 s[50:51], -1, 0
	s_lshl_b32 s4, s4, 11
	s_lshl_b32 s5, s5, 9
	v_lshl_add_u32 v4, v14, 11, v4
	v_and_b32_e32 v5, 1, v13
	s_or_b32 s68, s5, s4
	v_lshl_or_b32 v4, v5, 6, v4
	v_readlane_b32 s4, v252, 12
	v_mov_b32_e32 v159, v3
	v_lshl_add_u32 v160, v15, 1, v4
	v_mov_b32_e32 v161, v3
	s_mov_b32 s69, 0
	v_add_u32_e32 v166, 0, v6
	v_readlane_b32 s70, v254, 34
	s_mov_b32 s71, s4
	s_barrier
	v_readlane_b32 s5, v252, 13
	s_branch .LBB0_428

; #define PG8_STAGE(bufoff, gbase, voff) do { _Pragma("unroll") for (int _i = 0; _i < 2; ++_i) \
;         __builtin_amdgcn_global_load_lds((const unsigned*)((const char*)(gbase) + (voff)[_i]), (PG8_LAS unsigned*)(lds + (bufoff) + ldsw + _i * 8192), 16, 0, 0); } while (0)
; #define PG8_LDA(dst, b, h) do { _Pragma("unroll") for (int m = 0; m < 4; ++m) _Pragma("unroll") for (int k = 0; k < 2; ++k) dst[m][k] = *(const PG8_LAS bf16x8*)(lds + PG8_SA(b, h) + aoff + m * 2048 + k * 1024); } while (0)
; #define PG8_LDB(dst, b, h) do { _Pragma("unroll") for (int n = 0; n < 2; ++n) _Pragma("unroll") for (int k = 0; k < 2; ++k) dst[n][k] = *(const PG8_LAS bf16x8*)(lds + PG8_SB(b, h) + boff + n * 2048 + k * 1024); } while (0)
; #define PG8_WAIT_V8_UNLESS_FIRST(t) asm volatile("s_cmp_eq_u32 %0, 0\n\ts_cbranch_scc1 .Lpg8skip%=\n\ts_waitcnt vmcnt(8)\n.Lpg8skip%=:" :: "s"(t) : "scc", "memory")
; #define PG8_BAR __builtin_amdgcn_s_barrier()
; template <class Epi, class Sched, bool ALIGN_EPI = false, bool SP2 = false, bool FP8 = false, bool ABLK = false>
; __device__ __forceinline__ void gemm_phase(PG8_LAS unsigned char* lds, const Gemm g, const Sched& S, const Epi& E) {
;     ...
;         const bool has_next = S.next(ui + 1, nxt);
;         const char* nA = has_next ? (const char*)g.A + (size_t)nxt.pm * tstep : cA; const char* nB = has_next ? (const char*)g.Bt + (size_t)nxt.pn * tstep : cB;
;         for (int t = 0; t < nt; t += 2) {
;             const bool last = (t == nt - 2);
;             const char* a1 = cA + (size_t)(t + 1) * kstepA;
;             const char* a2 = last ? nA : cA + (size_t)(t + 2) * kstepA; const char* b2 = last ? nB : cB + (size_t)(t + 2) * kstep;
;             const char* a3 = a2 + kstepA; const char* b3 = b2 + kstep;
;             if (last && has_next) S.a_ready(nxt);
;             if constexpr (SP2) {
;             PG8_LDB(B0, 0, 0); PG8_LDB(B1, 0, 1); PG8_SCHED; PG8_LDA(At, 0, 0); PG8_STAGE(PG8_SA(1, 1), a1 + hstepA, voffA);
;             PG8_WAIT_V8_UNLESS_FIRST(t); PG8_WAIT_L(0); PG8_BAR; PG8_MMA(0, 0, At, B0); PG8_MMA(0, 1, At, B1); PG8_BAR; PG8_SCHED;
;             PG8_LDA(At, 0, 1); PG8_STAGE(PG8_SB(0, 0), b2, voffB); PG8_STAGE(PG8_SB(0, 1), b2 + hstep, voffB); PG8_STAGE(PG8_SA(0, 0), a2, voffA);
;             PG8_WAIT_V8_UNLESS_FIRST(t); PG8_WAIT_L(0); PG8_BAR; PG8_MMA(1, 0, At, B0); PG8_MMA(1, 1, At, B1); PG8_BAR; PG8_SCHED;
.LBB0_431:
	s_add_i32 s74, s62, 2
	s_add_u32 s63, s60, 0xfffc0080
	s_addc_u32 s64, s61, -1
	s_add_i32 s75, 0, 0x10000
	s_cmp_eq_u32 s62, 12
	s_cselect_b32 s65, s4, s64
	s_cselect_b32 s64, s5, s63
	s_cselect_b32 s63, s53, s73
	s_cselect_b32 s62, s55, s72
	s_add_i32 s81, 0, 0x14000
	v_add_u32_e32 v144, s75, v165
	v_add_u32_e32 v162, s81, v165
	ds_read_b128 v[132:135], v144
	ds_read_b128 v[136:139], v144 offset:1024
	ds_read_b128 v[140:143], v144 offset:2048
	ds_read_b128 v[144:147], v144 offset:3072
	ds_read_b128 v[148:151], v162
	ds_read_b128 v[168:171], v162 offset:1024
	ds_read_b128 v[172:175], v162 offset:2048
	ds_read_b128 v[176:179], v162 offset:3072
	s_add_i32 m0, s18, 0xc000
	ds_read_b128 v[180:183], v166
	ds_read_b128 v[184:187], v166 offset:1024
	ds_read_b128 v[188:191], v166 offset:2048
	ds_read_b128 v[192:195], v166 offset:3072
	ds_read_b128 v[208:211], v166 offset:4096
	ds_read_b128 v[212:215], v166 offset:5120
	ds_read_b128 v[216:219], v166 offset:6144
	ds_read_b128 v[220:223], v166 offset:7168
	global_load_lds_dwordx4 v158, s[60:61]
	s_add_i32 m0, s18, 0xe000
	s_nop 0
	global_load_lds_dwordx4 v160, s[60:61]
	s_cmp_eq_u32 s74, 0
	s_cbranch_scc1 .Lpg8skip0
	s_waitcnt vmcnt(8)
.Lpg8skip0:
	s_waitcnt lgkmcnt(0)
	s_barrier
	s_setprio 1
	s_waitcnt lgkmcnt(0)
	v_mfma_f32_16x16x32_bf16 v[128:131], v[132:135], v[180:183], v[128:131]
	v_mfma_f32_16x16x32_bf16 v[124:127], v[140:143], v[180:183], v[124:127]
	v_mfma_f32_16x16x32_bf16 v[112:115], v[132:135], v[188:191], v[112:115]
	v_mfma_f32_16x16x32_bf16 v[108:111], v[140:143], v[188:191], v[108:111]
	v_mfma_f32_16x16x32_bf16 v[96:99], v[132:135], v[208:211], v[96:99]
	v_mfma_f32_16x16x32_bf16 v[92:95], v[140:143], v[208:211], v[92:95]
	v_mfma_f32_16x16x32_bf16 v[80:83], v[132:135], v[216:219], v[80:83]
	v_mfma_f32_16x16x32_bf16 v[76:79], v[140:143], v[216:219], v[76:79]
	v_mfma_f32_16x16x32_bf16 v[128:131], v[136:139], v[184:187], v[128:131]
	v_mfma_f32_16x16x32_bf16 v[124:127], v[144:147], v[184:187], v[124:127]
	v_mfma_f32_16x16x32_bf16 v[112:115], v[136:139], v[192:195], v[112:115]
	v_mfma_f32_16x16x32_bf16 v[108:111], v[144:147], v[192:195], v[108:111]
	v_mfma_f32_16x16x32_bf16 v[96:99], v[136:139], v[212:215], v[96:99]
	v_mfma_f32_16x16x32_bf16 v[92:95], v[144:147], v[212:215], v[92:95]
	v_mfma_f32_16x16x32_bf16 v[80:83], v[136:139], v[220:223], v[80:83]
	v_mfma_f32_16x16x32_bf16 v[76:79], v[144:147], v[220:223], v[76:79]
	s_setprio 0
	s_setprio 1
	v_mfma_f32_16x16x32_bf16 v[120:123], v[148:151], v[180:183], v[120:123]
	v_mfma_f32_16x16x32_bf16 v[116:119], v[172:175], v[180:183], v[116:119]
	v_mfma_f32_16x16x32_bf16 v[104:107], v[148:151], v[188:191], v[104:107]
	v_mfma_f32_16x16x32_bf16 v[100:103], v[172:175], v[188:191], v[100:103]
	v_mfma_f32_16x16x32_bf16 v[88:91], v[148:151], v[208:211], v[88:91]
	v_mfma_f32_16x16x32_bf16 v[84:87], v[172:175], v[208:211], v[84:87]
	v_mfma_f32_16x16x32_bf16 v[72:75], v[148:151], v[216:219], v[72:75]
	v_mfma_f32_16x16x32_bf16 v[68:71], v[172:175], v[216:219], v[68:71]
	v_mfma_f32_16x16x32_bf16 v[120:123], v[168:171], v[184:187], v[120:123]
	v_mfma_f32_16x16x32_bf16 v[116:119], v[176:179], v[184:187], v[116:119]
	v_mfma_f32_16x16x32_bf16 v[104:107], v[168:171], v[192:195], v[104:107]
	v_mfma_f32_16x16x32_bf16 v[100:103], v[176:179], v[192:195], v[100:103]
	v_mfma_f32_16x16x32_bf16 v[88:91], v[168:171], v[212:215], v[88:91]
	v_mfma_f32_16x16x32_bf16 v[84:87], v[176:179], v[212:215], v[84:87]
	v_mfma_f32_16x16x32_bf16 v[72:75], v[168:171], v[220:223], v[72:75]
	v_mfma_f32_16x16x32_bf16 v[68:71], v[176:179], v[220:223], v[68:71]
	s_setprio 0
	s_barrier
	s_add_i32 s75, s75, s17
	v_lshl_add_u64 v[162:163], s[62:63], 0, v[2:3]
	s_mov_b32 m0, s75
	ds_read_b128 v[180:183], v166 offset:16384
	ds_read_b128 v[184:187], v166 offset:17408
	ds_read_b128 v[188:191], v166 offset:18432
	ds_read_b128 v[192:195], v166 offset:19456
	ds_read_b128 v[208:211], v166 offset:20480
	ds_read_b128 v[212:215], v166 offset:21504
	ds_read_b128 v[216:219], v166 offset:22528
	ds_read_b128 v[220:223], v166 offset:23552
	global_load_lds_dwordx4 v2, s[62:63]
	s_add_i32 m0, s75, 0x2000
	s_add_u32 s76, s62, 0x40000
	v_lshl_add_u64 v[224:225], s[62:63], 0, v[152:153]
	s_addc_u32 s77, s63, 0
	s_add_i32 s75, s81, s17
	global_load_lds_dwordx4 v152, s[62:63]
	s_mov_b32 m0, s75
	v_lshl_add_u64 v[230:231], s[64:65], 0, v[154:155]
	global_load_lds_dwordx4 v2, s[76:77]
	s_add_i32 m0, s75, 0x2000
	s_nop 0
	global_load_lds_dwordx4 v152, s[76:77]
	v_lshl_add_u64 v[228:229], s[64:65], 0, v[156:157]
	s_mov_b32 m0, s18
	s_nop 0
	global_load_lds_dwordx4 v156, s[64:65]
	s_mov_b32 m0, s19
	s_nop 0
	global_load_lds_dwordx4 v154, s[64:65]
	s_cmp_eq_u32 s74, 0
	s_cbranch_scc1 .Lpg8skip1
	s_waitcnt vmcnt(8)
; #define PG8_STAGE(bufoff, gbase, voff) do { _Pragma("unroll") for (int _i = 0; _i < 2; ++_i) \
;         __builtin_amdgcn_global_load_lds((const unsigned*)((const char*)(gbase) + (voff)[_i]), (PG8_LAS unsigned*)(lds + (bufoff) + ldsw + _i * 8192), 16, 0, 0); } while (0)
; #define PG8_LDA(dst, b, h) do { _Pragma("unroll") for (int m = 0; m < 4; ++m) _Pragma("unroll") for (int k = 0; k < 2; ++k) dst[m][k] = *(const PG8_LAS bf16x8*)(lds + PG8_SA(b, h) + aoff + m * 2048 + k * 1024); } while (0)
; #define PG8_LDB(dst, b, h) do { _Pragma("unroll") for (int n = 0; n < 2; ++n) _Pragma("unroll") for (int k = 0; k < 2; ++k) dst[n][k] = *(const PG8_LAS bf16x8*)(lds + PG8_SB(b, h) + boff + n * 2048 + k * 1024); } while (0)
; #define PG8_WAIT_V(n) asm volatile("s_waitcnt vmcnt(" #n ")" ::: "memory")
; #define PG8_WAIT_V8_UNLESS_FIRST(t) asm volatile("s_cmp_eq_u32 %0, 0\n\ts_cbranch_scc1 .Lpg8skip%=\n\ts_waitcnt vmcnt(8)\n.Lpg8skip%=:" :: "s"(t) : "scc", "memory")
; #define PG8_WAIT_L(n) asm volatile("s_waitcnt lgkmcnt(" #n ")" ::: "memory")
; #define PG8_BAR __builtin_amdgcn_s_barrier()
; template <class Epi, class Sched, bool ALIGN_EPI = false, bool SP2 = false, bool FP8 = false, bool ABLK = false>
; __device__ __forceinline__ void gemm_phase(PG8_LAS unsigned char* lds, const Gemm g, const Sched& S, const Epi& E) {
;     ...
;             PG8_LDB(B0, 0, 0); PG8_LDB(B1, 0, 1); PG8_SCHED; PG8_LDA(At, 0, 0); PG8_STAGE(PG8_SA(1, 1), a1 + hstepA, voffA);
;             PG8_WAIT_V8_UNLESS_FIRST(t); PG8_WAIT_L(0); PG8_BAR; PG8_MMA(0, 0, At, B0); PG8_MMA(0, 1, At, B1); PG8_BAR; PG8_SCHED;
;             PG8_LDA(At, 0, 1); PG8_STAGE(PG8_SB(0, 0), b2, voffB); PG8_STAGE(PG8_SB(0, 1), b2 + hstep, voffB); PG8_STAGE(PG8_SA(0, 0), a2, voffA);
;             PG8_WAIT_V8_UNLESS_FIRST(t); PG8_WAIT_L(0); PG8_BAR; PG8_MMA(1, 0, At, B0); PG8_MMA(1, 1, At, B1); PG8_BAR; PG8_SCHED;
;             PG8_LDB(B0, 1, 0); PG8_LDB(B1, 1, 1); PG8_SCHED; PG8_LDA(At, 1, 0); PG8_STAGE(PG8_SA(0, 1), a2 + hstepA, voffA);
;             PG8_WAIT_V(8); PG8_WAIT_L(0); PG8_BAR; PG8_MMA(0, 0, At, B0); PG8_MMA(0, 1, At, B1); PG8_BAR; PG8_SCHED;
;             PG8_LDA(At, 1, 1); PG8_STAGE(PG8_SB(1, 0), b3, voffB); PG8_STAGE(PG8_SB(1, 1), b3 + hstep, voffB); PG8_STAGE(PG8_SA(1, 0), a3, voffA);
;             PG8_WAIT_V(8); PG8_WAIT_L(0); PG8_BAR; PG8_MMA(1, 0, At, B0); PG8_MMA(1, 1, At, B1); PG8_BAR; PG8_SCHED;
.Lpg8skip1:
	s_waitcnt lgkmcnt(0)
	s_barrier
	s_setprio 1
	s_waitcnt lgkmcnt(0)
	v_mfma_f32_16x16x32_bf16 v[64:67], v[132:135], v[180:183], v[64:67]
	v_mfma_f32_16x16x32_bf16 v[60:63], v[140:143], v[180:183], v[60:63]
	v_mfma_f32_16x16x32_bf16 v[48:51], v[132:135], v[188:191], v[48:51]
	v_mfma_f32_16x16x32_bf16 v[44:47], v[140:143], v[188:191], v[44:47]
	v_mfma_f32_16x16x32_bf16 v[32:35], v[132:135], v[208:211], v[32:35]
	v_mfma_f32_16x16x32_bf16 v[28:31], v[140:143], v[208:211], v[28:31]
	v_mfma_f32_16x16x32_bf16 v[16:19], v[132:135], v[216:219], v[16:19]
	v_mfma_f32_16x16x32_bf16 v[12:15], v[140:143], v[216:219], v[12:15]
	v_mfma_f32_16x16x32_bf16 v[64:67], v[136:139], v[184:187], v[64:67]
	v_mfma_f32_16x16x32_bf16 v[60:63], v[144:147], v[184:187], v[60:63]
	v_mfma_f32_16x16x32_bf16 v[48:51], v[136:139], v[192:195], v[48:51]
	v_mfma_f32_16x16x32_bf16 v[44:47], v[144:147], v[192:195], v[44:47]
	v_mfma_f32_16x16x32_bf16 v[32:35], v[136:139], v[212:215], v[32:35]
	v_mfma_f32_16x16x32_bf16 v[28:31], v[144:147], v[212:215], v[28:31]
	v_mfma_f32_16x16x32_bf16 v[16:19], v[136:139], v[220:223], v[16:19]
	v_mfma_f32_16x16x32_bf16 v[12:15], v[144:147], v[220:223], v[12:15]
	s_setprio 0
	s_setprio 1
	v_mfma_f32_16x16x32_bf16 v[56:59], v[148:151], v[180:183], v[56:59]
	v_mfma_f32_16x16x32_bf16 v[52:55], v[172:175], v[180:183], v[52:55]
	v_mfma_f32_16x16x32_bf16 v[40:43], v[148:151], v[188:191], v[40:43]
	v_mfma_f32_16x16x32_bf16 v[36:39], v[172:175], v[188:191], v[36:39]
	v_mfma_f32_16x16x32_bf16 v[24:27], v[148:151], v[208:211], v[24:27]
	v_mfma_f32_16x16x32_bf16 v[20:23], v[172:175], v[208:211], v[20:23]
	v_mfma_f32_16x16x32_bf16 v[8:11], v[148:151], v[216:219], v[8:11]
	v_mfma_f32_16x16x32_bf16 v[4:7], v[172:175], v[216:219], v[4:7]
	v_mfma_f32_16x16x32_bf16 v[56:59], v[168:171], v[184:187], v[56:59]
	v_mfma_f32_16x16x32_bf16 v[52:55], v[176:179], v[184:187], v[52:55]
	v_mfma_f32_16x16x32_bf16 v[40:43], v[168:171], v[192:195], v[40:43]
	v_mfma_f32_16x16x32_bf16 v[36:39], v[176:179], v[192:195], v[36:39]
	v_mfma_f32_16x16x32_bf16 v[24:27], v[168:171], v[212:215], v[24:27]
	v_mfma_f32_16x16x32_bf16 v[20:23], v[176:179], v[212:215], v[20:23]
	v_mfma_f32_16x16x32_bf16 v[8:11], v[168:171], v[220:223], v[8:11]
	v_mfma_f32_16x16x32_bf16 v[4:7], v[176:179], v[220:223], v[4:7]
	s_setprio 0
	s_barrier
	s_add_i32 s75, 0, 0x18000
	s_add_i32 s76, 0, 0x1c000
	v_add_u32_e32 v144, s75, v165
	v_add_u32_e32 v167, s76, v165
	ds_read_b128 v[132:135], v144
	ds_read_b128 v[136:139], v144 offset:1024
	ds_read_b128 v[140:143], v144 offset:2048
	ds_read_b128 v[144:147], v144 offset:3072
	ds_read_b128 v[148:151], v167
	ds_read_b128 v[168:171], v167 offset:1024
	ds_read_b128 v[172:175], v167 offset:2048
	ds_read_b128 v[176:179], v167 offset:3072
	s_add_u32 s64, s64, 0x40000
	s_addc_u32 s65, s65, 0
	s_mov_b32 m0, s20
	ds_read_b128 v[180:183], v166 offset:32768
	ds_read_b128 v[184:187], v166 offset:33792
	ds_read_b128 v[188:191], v166 offset:34816
	ds_read_b128 v[192:195], v166 offset:35840
	ds_read_b128 v[208:211], v166 offset:36864
	ds_read_b128 v[212:215], v166 offset:37888
	ds_read_b128 v[216:219], v166 offset:38912
	ds_read_b128 v[220:223], v166 offset:39936
	global_load_lds_dwordx4 v156, s[64:65]
	s_mov_b32 m0, s21
	s_nop 0
	global_load_lds_dwordx4 v154, s[64:65]
	s_waitcnt vmcnt(8)
	s_waitcnt lgkmcnt(0)
	s_barrier
	s_setprio 1
	s_waitcnt lgkmcnt(0)
	v_mfma_f32_16x16x32_bf16 v[128:131], v[132:135], v[180:183], v[128:131]
	v_mfma_f32_16x16x32_bf16 v[124:127], v[140:143], v[180:183], v[124:127]
	v_mfma_f32_16x16x32_bf16 v[112:115], v[132:135], v[188:191], v[112:115]
	v_mfma_f32_16x16x32_bf16 v[108:111], v[140:143], v[188:191], v[108:111]
	v_mfma_f32_16x16x32_bf16 v[96:99], v[132:135], v[208:211], v[96:99]
	v_mfma_f32_16x16x32_bf16 v[92:95], v[140:143], v[208:211], v[92:95]
	v_mfma_f32_16x16x32_bf16 v[80:83], v[132:135], v[216:219], v[80:83]
	v_mfma_f32_16x16x32_bf16 v[76:79], v[140:143], v[216:219], v[76:79]
	v_mfma_f32_16x16x32_bf16 v[128:131], v[136:139], v[184:187], v[128:131]
	v_mfma_f32_16x16x32_bf16 v[124:127], v[144:147], v[184:187], v[124:127]
	v_mfma_f32_16x16x32_bf16 v[112:115], v[136:139], v[192:195], v[112:115]
	v_mfma_f32_16x16x32_bf16 v[108:111], v[144:147], v[192:195], v[108:111]
	v_mfma_f32_16x16x32_bf16 v[96:99], v[136:139], v[212:215], v[96:99]
	v_mfma_f32_16x16x32_bf16 v[92:95], v[144:147], v[212:215], v[92:95]
	v_mfma_f32_16x16x32_bf16 v[80:83], v[136:139], v[220:223], v[80:83]
	v_mfma_f32_16x16x32_bf16 v[76:79], v[144:147], v[220:223], v[76:79]
	s_setprio 0
	s_setprio 1
	v_mfma_f32_16x16x32_bf16 v[120:123], v[148:151], v[180:183], v[120:123]
	v_mfma_f32_16x16x32_bf16 v[116:119], v[172:175], v[180:183], v[116:119]
	v_mfma_f32_16x16x32_bf16 v[104:107], v[148:151], v[188:191], v[104:107]
	v_mfma_f32_16x16x32_bf16 v[100:103], v[172:175], v[188:191], v[100:103]
	v_mfma_f32_16x16x32_bf16 v[88:91], v[148:151], v[208:211], v[88:91]
	v_mfma_f32_16x16x32_bf16 v[84:87], v[172:175], v[208:211], v[84:87]
	v_mfma_f32_16x16x32_bf16 v[72:75], v[148:151], v[216:219], v[72:75]
	v_mfma_f32_16x16x32_bf16 v[68:71], v[172:175], v[216:219], v[68:71]
	v_mfma_f32_16x16x32_bf16 v[120:123], v[168:171], v[184:187], v[120:123]
	v_mfma_f32_16x16x32_bf16 v[116:119], v[176:179], v[184:187], v[116:119]
	v_mfma_f32_16x16x32_bf16 v[104:107], v[168:171], v[192:195], v[104:107]
	v_mfma_f32_16x16x32_bf16 v[100:103], v[176:179], v[192:195], v[100:103]
	v_mfma_f32_16x16x32_bf16 v[88:91], v[168:171], v[212:215], v[88:91]
	v_mfma_f32_16x16x32_bf16 v[84:87], v[176:179], v[212:215], v[84:87]
	v_mfma_f32_16x16x32_bf16 v[72:75], v[168:171], v[220:223], v[72:75]
	v_mfma_f32_16x16x32_bf16 v[68:71], v[176:179], v[220:223], v[68:71]
	s_setprio 0
	s_barrier
; #define PG8_WAIT_V(n) asm volatile("s_waitcnt vmcnt(" #n ")" ::: "memory")
; #define PG8_WAIT_L(n) asm volatile("s_waitcnt lgkmcnt(" #n ")" ::: "memory")
; template <class Epi, class Sched, bool ALIGN_EPI = false, bool SP2 = false, bool FP8 = false, bool ABLK = false>
; __device__ __forceinline__ void gemm_phase(PG8_LAS unsigned char* lds, const Gemm g, const Sched& S, const Epi& E) {
;     ...
;             PG8_LDB(B0, 1, 0); PG8_LDB(B1, 1, 1); PG8_SCHED; PG8_LDA(At, 1, 0); PG8_STAGE(PG8_SA(0, 1), a2 + hstepA, voffA);
;             PG8_WAIT_V(8); PG8_WAIT_L(0); PG8_BAR; PG8_MMA(0, 0, At, B0); PG8_MMA(0, 1, At, B1); PG8_BAR; PG8_SCHED;
;             PG8_LDA(At, 1, 1); PG8_STAGE(PG8_SB(1, 0), b3, voffB); PG8_STAGE(PG8_SB(1, 1), b3 + hstep, voffB); PG8_STAGE(PG8_SA(1, 0), a3, voffA);
;             PG8_WAIT_V(8); PG8_WAIT_L(0); PG8_BAR; PG8_MMA(1, 0, At, B0); PG8_MMA(1, 1, At, B1); PG8_BAR; PG8_SCHED;
;             } else {
;             PG8_LDB(B0, 0, 0); PG8_SCHED; PG8_LDA(At, 0, 0); PG8_STAGE(PG8_SA(1, 1), a1 + hstepA, voffA);
;             PG8_WAIT_L(8); PG8_BAR; PG8_WAIT_L(0); PG8_MMA(0, 0, At, B0); PG8_BAR; PG8_SCHED;
;             PG8_LDB(B1, 0, 1); PG8_STAGE(PG8_SB(0, 0), b2, voffB);
;             PG8_BAR; PG8_WAIT_L(0); PG8_MMA(0, 1, At, B1); PG8_BAR;
;             PG8_LDA(At, 0, 1); PG8_STAGE(PG8_SA(0, 0), a2, voffA);
;             PG8_BAR; PG8_WAIT_L(0); PG8_MMA(1, 0, At, B0); PG8_BAR; PG8_SCHED;
;             PG8_STAGE(PG8_SB(0, 1), b2 + hstep, voffB);
;             PG8_WAIT_V(6); PG8_BAR; PG8_MMA(1, 1, At, B1); PG8_BAR;
;             PG8_LDB(B0, 1, 0); PG8_SCHED; PG8_LDA(At, 1, 0); PG8_STAGE(PG8_SA(0, 1), a2 + hstepA, voffA);
;             PG8_WAIT_L(8); PG8_BAR; PG8_WAIT_L(0); PG8_MMA(0, 0, At, B0); PG8_BAR; PG8_SCHED;
;             PG8_LDB(B1, 1, 1); PG8_STAGE(PG8_SB(1, 0), b3, voffB);
;             PG8_BAR; PG8_WAIT_L(0); PG8_MMA(0, 1, At, B1); PG8_BAR;
;             PG8_LDA(At, 1, 1); PG8_STAGE(PG8_SA(1, 0), a3, voffA);
;             PG8_BAR; PG8_WAIT_L(0); PG8_MMA(1, 0, At, B0); PG8_BAR; PG8_SCHED;
;             PG8_STAGE(PG8_SB(1, 1), b3 + hstep, voffB);
;             PG8_WAIT_V(6); PG8_BAR; PG8_MMA(1, 1, At, B1); PG8_BAR;
;             }
;         }
;         if constexpr (SP2) PG8_WAIT_V(0);
;         if constexpr (FP8) asm volatile("s_nop 15\n\ts_nop 15" ::: "memory");
;         if constexpr (ALIGN_EPI) { if (wr == 0) PG8_BAR; }
	s_add_i32 s64, s75, s17
	v_lshl_add_u64 v[162:163], v[162:163], 0, s[34:35]
	s_mov_b32 m0, s64
	ds_read_b128 v[180:183], v166 offset:49152
	ds_read_b128 v[184:187], v166 offset:50176
	ds_read_b128 v[188:191], v166 offset:51200
	ds_read_b128 v[192:195], v166 offset:52224
	ds_read_b128 v[208:211], v166 offset:53248
	ds_read_b128 v[212:215], v166 offset:54272
	ds_read_b128 v[216:219], v166 offset:55296
	ds_read_b128 v[220:223], v166 offset:56320
	global_load_lds_dwordx4 v[162:163], off
	s_add_i32 m0, s64, 0x2000
	s_add_u32 s62, s62, 0x40080
	v_lshl_add_u64 v[162:163], v[224:225], 0, s[34:35]
	s_addc_u32 s63, s63, 0
	s_add_i32 s64, s76, s17
	global_load_lds_dwordx4 v[162:163], off
	s_mov_b32 m0, s64
	s_nop 0
	global_load_lds_dwordx4 v2, s[62:63]
	s_add_i32 m0, s64, 0x2000
	s_nop 0
	global_load_lds_dwordx4 v152, s[62:63]
	v_lshl_add_u64 v[162:163], v[228:229], 0, s[34:35]
	s_mov_b32 m0, s66
	s_nop 0
	global_load_lds_dwordx4 v[162:163], off
	v_lshl_add_u64 v[162:163], v[230:231], 0, s[34:35]
	s_mov_b32 m0, s67
	s_nop 0
	global_load_lds_dwordx4 v[162:163], off
	s_waitcnt vmcnt(8)
	s_waitcnt lgkmcnt(0)
	s_barrier
	s_setprio 1
	s_waitcnt lgkmcnt(0)
	v_mfma_f32_16x16x32_bf16 v[64:67], v[132:135], v[180:183], v[64:67]
	v_mfma_f32_16x16x32_bf16 v[60:63], v[140:143], v[180:183], v[60:63]
	v_mfma_f32_16x16x32_bf16 v[48:51], v[132:135], v[188:191], v[48:51]
	v_mfma_f32_16x16x32_bf16 v[44:47], v[140:143], v[188:191], v[44:47]
	v_mfma_f32_16x16x32_bf16 v[32:35], v[132:135], v[208:211], v[32:35]
	v_mfma_f32_16x16x32_bf16 v[28:31], v[140:143], v[208:211], v[28:31]
	v_mfma_f32_16x16x32_bf16 v[16:19], v[132:135], v[216:219], v[16:19]
	v_mfma_f32_16x16x32_bf16 v[12:15], v[140:143], v[216:219], v[12:15]
	v_mfma_f32_16x16x32_bf16 v[64:67], v[136:139], v[184:187], v[64:67]
	v_mfma_f32_16x16x32_bf16 v[60:63], v[144:147], v[184:187], v[60:63]
	v_mfma_f32_16x16x32_bf16 v[48:51], v[136:139], v[192:195], v[48:51]
	v_mfma_f32_16x16x32_bf16 v[44:47], v[144:147], v[192:195], v[44:47]
	v_mfma_f32_16x16x32_bf16 v[32:35], v[136:139], v[212:215], v[32:35]
	v_mfma_f32_16x16x32_bf16 v[28:31], v[144:147], v[212:215], v[28:31]
	v_mfma_f32_16x16x32_bf16 v[16:19], v[136:139], v[220:223], v[16:19]
	v_mfma_f32_16x16x32_bf16 v[12:15], v[144:147], v[220:223], v[12:15]
	s_setprio 0
	s_setprio 1
	v_mfma_f32_16x16x32_bf16 v[56:59], v[148:151], v[180:183], v[56:59]
	v_mfma_f32_16x16x32_bf16 v[52:55], v[172:175], v[180:183], v[52:55]
	v_mfma_f32_16x16x32_bf16 v[40:43], v[148:151], v[188:191], v[40:43]
	v_mfma_f32_16x16x32_bf16 v[36:39], v[172:175], v[188:191], v[36:39]
	v_mfma_f32_16x16x32_bf16 v[24:27], v[148:151], v[208:211], v[24:27]
	v_mfma_f32_16x16x32_bf16 v[20:23], v[172:175], v[208:211], v[20:23]
	v_mfma_f32_16x16x32_bf16 v[8:11], v[148:151], v[216:219], v[8:11]
	v_mfma_f32_16x16x32_bf16 v[4:7], v[172:175], v[216:219], v[4:7]
	v_mfma_f32_16x16x32_bf16 v[56:59], v[168:171], v[184:187], v[56:59]
	v_mfma_f32_16x16x32_bf16 v[52:55], v[176:179], v[184:187], v[52:55]
	v_mfma_f32_16x16x32_bf16 v[40:43], v[168:171], v[192:195], v[40:43]
	v_mfma_f32_16x16x32_bf16 v[36:39], v[176:179], v[192:195], v[36:39]
	v_mfma_f32_16x16x32_bf16 v[24:27], v[168:171], v[212:215], v[24:27]
	v_mfma_f32_16x16x32_bf16 v[20:23], v[176:179], v[212:215], v[20:23]
	v_mfma_f32_16x16x32_bf16 v[8:11], v[168:171], v[220:223], v[8:11]
	v_mfma_f32_16x16x32_bf16 v[4:7], v[176:179], v[220:223], v[4:7]
	s_setprio 0
	s_barrier
	s_add_u32 s60, s60, 0x100
	s_addc_u32 s61, s61, 0
	s_add_u32 s72, s72, 0x100
	s_addc_u32 s73, s73, 0
	s_cmp_gt_u32 s74, 13
	s_mov_b32 s62, s74
	s_cbranch_scc0 .LBB0_431
	s_waitcnt vmcnt(0)
	s_and_b64 vcc, exec, s[50:51]
	s_cbranch_vccz .LBB0_434
	s_barrier

; #define PG8_STAGE(bufoff, gbase, voff) do { _Pragma("unroll") for (int _i = 0; _i < 2; ++_i) \
;         __builtin_amdgcn_global_load_lds((const unsigned*)((const char*)(gbase) + (voff)[_i]), (PG8_LAS unsigned*)(lds + (bufoff) + ldsw + _i * 8192), 16, 0, 0); } while (0)
; #define PG8_WAIT_V(n) asm volatile("s_waitcnt vmcnt(" #n ")" ::: "memory")
; #define PG8_BAR __builtin_amdgcn_s_barrier()
;   __device__ __forceinline__ bool next(int i,AttnUnit&u)const{ const int v=vcu+(i>>2)*grid; if(v>=256)return false; const int k=i&3,s=v&7; u.bh=v>>3; u.qb=(k==0)?s:(k==1)?15-s:(k==2)?16+s:31-s; return true; }
; template <class Epi, class Sched, bool ALIGN_EPI = false, bool SP2 = false, bool FP8 = false, bool ABLK = false>
; __device__ __forceinline__ void gemm_phase(PG8_LAS unsigned char* lds, const Gemm g, const Sched& S, const Epi& E) {
;     ...
;         PG8_STAGE(PG8_SB(0, 0), cB, voffB); PG8_STAGE(PG8_SB(0, 1), cB + hstep, voffB); PG8_STAGE(PG8_SA(0, 0), cA, voffA); PG8_STAGE(PG8_SA(0, 1), cA + hstepA, voffA);
;         if (wr == 1) PG8_BAR;
;         PG8_WAIT_V(2); PG8_BAR;
;         PG8_STAGE(PG8_SB(1, 0), cB + kstep, voffB); PG8_STAGE(PG8_SA(1, 0), cA + kstepA, voffA); PG8_STAGE(PG8_SB(1, 1), cB + hstep + kstep, voffB);
;         PG8_WAIT_V(0); PG8_BAR;
;     } else {
;         PG8_STAGE(PG8_SB(0, 0), cB, voffB); PG8_STAGE(PG8_SA(0, 0), cA, voffA); PG8_STAGE(PG8_SB(0, 1), cB + hstep, voffB); PG8_STAGE(PG8_SA(0, 1), cA + hstepA, voffA);
;         if (wr == 1) PG8_BAR;
;         PG8_WAIT_V(4); PG8_BAR;
;         PG8_STAGE(PG8_SB(1, 0), cB + kstep, voffB); PG8_STAGE(PG8_SA(1, 0), cA + kstepA, voffA); PG8_STAGE(PG8_SB(1, 1), cB + hstep + kstep, voffB);
;         PG8_WAIT_V(6); PG8_BAR;
;     }
;     for (;;) {
;         const bool has_next = S.next(ui + 1, nxt);
;         const char* nA = has_next ? (const char*)g.A + (size_t)nxt.pm * tstep : cA; const char* nB = has_next ? (const char*)g.Bt + (size_t)nxt.pn * tstep : cB;
.LBB0_494:
	s_add_u32 s44, s40, 0x7a00000
	s_addc_u32 s45, s41, 0
	v_bfe_u32 v182, v13, 4, 2
	s_add_u32 s48, s40, 0x1c200000
	v_and_b32_e32 v1, 15, v13
	v_lshlrev_b32_e32 v19, 4, v182
	v_lshlrev_b32_e32 v13, 2, v13
	s_addc_u32 s49, s41, 0
	s_and_b32 s22, s5, 3
	s_lshl_b32 s23, s4, 6
	v_lshl_or_b32 v19, v1, 6, v19
	s_lshl_b32 s4, s4, 13
	v_and_b32_e32 v13, 32, v13
	s_add_i32 m0, s18, 0x18000
	v_lshl_add_u64 v[4:5], v[4:5], 0, s[34:35]
	v_bitop3_b32 v20, v19, s4, v13 bitop3:0xde
	s_lshl_b32 s47, s22, 5
	s_lshl_b32 s4, s22, 12
	s_waitcnt vmcnt(2)
	s_barrier
	global_load_lds_dwordx4 v[4:5], off
	s_add_i32 m0, s18, 0x1a000
	v_bitop3_b32 v183, v19, s4, v13 bitop3:0xde
	s_add_u32 s4, s54, 0x8000
	v_lshl_add_u64 v[4:5], v[6:7], 0, s[34:35]
	s_addc_u32 s5, s55, 0
	s_add_i32 s64, s18, 0x8000
	global_load_lds_dwordx4 v[4:5], off
	s_mov_b32 m0, s64
	s_add_i32 s65, s18, 0xa000
	global_load_lds_dwordx4 v168, s[4:5]
	v_lshl_add_u64 v[4:5], s[4:5], 0, v[166:167]
	s_add_u32 s4, s56, 0x58080
	s_mov_b32 m0, s65
	s_addc_u32 s5, s57, 0
	global_load_lds_dwordx4 v[4:5], off
	s_add_i32 m0, s18, 0x1c000
	s_nop 0
	global_load_lds_dwordx4 v2, s[4:5]
	s_add_i32 m0, s18, 0x1e000
	s_cmpk_lt_u32 s42, 0x100
	global_load_lds_dwordx4 v164, s[4:5]
	v_lshlrev_b32_e32 v4, 8, v14
	v_and_b32_e32 v4, 0xffffc000, v4
	v_lshl_add_u32 v4, v15, 12, v4
	v_or_b32_e32 v4, v4, v16
	v_add3_u32 v170, v4, v17, v18
	v_lshlrev_b32_e32 v4, 8, v8
	v_and_b32_e32 v4, 0xffffc000, v4
	s_waitcnt vmcnt(0)
	v_lshl_add_u32 v4, v9, 12, v4
	v_or_b32_e32 v4, v4, v10
	v_readlane_b32 s4, v252, 8
	s_cselect_b64 s[50:51], -1, 0
	v_mov_b32_e32 v171, v3
	v_add3_u32 v172, v4, v11, v12
	v_mov_b32_e32 v173, v3
	s_mov_b32 s66, 0
	v_add_u32_e32 v184, 0, v20
	v_readlane_b32 s69, v254, 58
	s_mov_b32 s70, s4
	s_barrier
	v_readlane_b32 s5, v252, 9
	s_branch .LBB0_497

; #define PG8_STAGE(bufoff, gbase, voff) do { _Pragma("unroll") for (int _i = 0; _i < 2; ++_i) \
;         __builtin_amdgcn_global_load_lds((const unsigned*)((const char*)(gbase) + (voff)[_i]), (PG8_LAS unsigned*)(lds + (bufoff) + ldsw + _i * 8192), 16, 0, 0); } while (0)
; #define PG8_LDA(dst, b, h) do { _Pragma("unroll") for (int m = 0; m < 4; ++m) _Pragma("unroll") for (int k = 0; k < 2; ++k) dst[m][k] = *(const PG8_LAS bf16x8*)(lds + PG8_SA(b, h) + aoff + m * 2048 + k * 1024); } while (0)
; #define PG8_LDB(dst, b, h) do { _Pragma("unroll") for (int n = 0; n < 2; ++n) _Pragma("unroll") for (int k = 0; k < 2; ++k) dst[n][k] = *(const PG8_LAS bf16x8*)(lds + PG8_SB(b, h) + boff + n * 2048 + k * 1024); } while (0)
; #define PG8_WAIT_V(n) asm volatile("s_waitcnt vmcnt(" #n ")" ::: "memory")
; #define PG8_WAIT_V8_UNLESS_FIRST(t) asm volatile("s_cmp_eq_u32 %0, 0\n\ts_cbranch_scc1 .Lpg8skip%=\n\ts_waitcnt vmcnt(8)\n.Lpg8skip%=:" :: "s"(t) : "scc", "memory")
; #define PG8_WAIT_L(n) asm volatile("s_waitcnt lgkmcnt(" #n ")" ::: "memory")
; #define PG8_BAR __builtin_amdgcn_s_barrier()
; template <class Epi, class Sched, bool ALIGN_EPI = false, bool SP2 = false, bool FP8 = false, bool ABLK = false>
; __device__ __forceinline__ void gemm_phase(PG8_LAS unsigned char* lds, const Gemm g, const Sched& S, const Epi& E) {
;     ...
;             PG8_LDB(B0, 0, 0); PG8_LDB(B1, 0, 1); PG8_SCHED; PG8_LDA(At, 0, 0); PG8_STAGE(PG8_SA(1, 1), a1 + hstepA, voffA);
;             PG8_WAIT_V8_UNLESS_FIRST(t); PG8_WAIT_L(0); PG8_BAR; PG8_MMA(0, 0, At, B0); PG8_MMA(0, 1, At, B1); PG8_BAR; PG8_SCHED;
;             PG8_LDA(At, 0, 1); PG8_STAGE(PG8_SB(0, 0), b2, voffB); PG8_STAGE(PG8_SB(0, 1), b2 + hstep, voffB); PG8_STAGE(PG8_SA(0, 0), a2, voffA);
;             PG8_WAIT_V8_UNLESS_FIRST(t); PG8_WAIT_L(0); PG8_BAR; PG8_MMA(1, 0, At, B0); PG8_MMA(1, 1, At, B1); PG8_BAR; PG8_SCHED;
;             PG8_LDB(B0, 1, 0); PG8_LDB(B1, 1, 1); PG8_SCHED; PG8_LDA(At, 1, 0); PG8_STAGE(PG8_SA(0, 1), a2 + hstepA, voffA);
;             PG8_WAIT_V(8); PG8_WAIT_L(0); PG8_BAR; PG8_MMA(0, 0, At, B0); PG8_MMA(0, 1, At, B1); PG8_BAR; PG8_SCHED;
;             PG8_LDA(At, 1, 1); PG8_STAGE(PG8_SB(1, 0), b3, voffB); PG8_STAGE(PG8_SB(1, 1), b3 + hstep, voffB); PG8_STAGE(PG8_SA(1, 0), a3, voffA);
;             PG8_WAIT_V(8); PG8_WAIT_L(0); PG8_BAR; PG8_MMA(1, 0, At, B0); PG8_MMA(1, 1, At, B1); PG8_BAR; PG8_SCHED;
.Lpg8skip2:
	s_waitcnt lgkmcnt(0)
	s_barrier
	s_setprio 1
	s_waitcnt lgkmcnt(0)
	v_mfma_scale_f32_16x16x128_f8f6f4 v[160:163], v[28:35], v[186:193], v[160:163], v245, v245 op_sel_hi:[0,0,0]
	v_mfma_scale_f32_16x16x128_f8f6f4 v[156:159], v[20:27], v[186:193], v[156:159], v245, v245 op_sel_hi:[0,0,0]
	v_mfma_scale_f32_16x16x128_f8f6f4 v[144:147], v[28:35], v[208:215], v[144:147], v245, v245 op_sel_hi:[0,0,0]
	v_mfma_scale_f32_16x16x128_f8f6f4 v[140:143], v[20:27], v[208:215], v[140:143], v245, v245 op_sel_hi:[0,0,0]
	v_mfma_scale_f32_16x16x128_f8f6f4 v[128:131], v[28:35], v[216:223], v[128:131], v245, v245 op_sel_hi:[0,0,0]
	v_mfma_scale_f32_16x16x128_f8f6f4 v[124:127], v[20:27], v[216:223], v[124:127], v245, v245 op_sel_hi:[0,0,0]
	v_mfma_scale_f32_16x16x128_f8f6f4 v[112:115], v[28:35], v[228:235], v[112:115], v245, v245 op_sel_hi:[0,0,0]
	v_mfma_scale_f32_16x16x128_f8f6f4 v[108:111], v[20:27], v[228:235], v[108:111], v245, v245 op_sel_hi:[0,0,0]
	s_setprio 0
	s_setprio 1
	v_mfma_scale_f32_16x16x128_f8f6f4 v[152:155], v[12:19], v[186:193], v[152:155], v245, v245 op_sel_hi:[0,0,0]
	v_mfma_scale_f32_16x16x128_f8f6f4 v[148:151], v[4:11], v[186:193], v[148:151], v245, v245 op_sel_hi:[0,0,0]
	v_mfma_scale_f32_16x16x128_f8f6f4 v[136:139], v[12:19], v[208:215], v[136:139], v245, v245 op_sel_hi:[0,0,0]
	v_mfma_scale_f32_16x16x128_f8f6f4 v[132:135], v[4:11], v[208:215], v[132:135], v245, v245 op_sel_hi:[0,0,0]
	v_mfma_scale_f32_16x16x128_f8f6f4 v[120:123], v[12:19], v[216:223], v[120:123], v245, v245 op_sel_hi:[0,0,0]
	v_mfma_scale_f32_16x16x128_f8f6f4 v[116:119], v[4:11], v[216:223], v[116:119], v245, v245 op_sel_hi:[0,0,0]
	v_mfma_scale_f32_16x16x128_f8f6f4 v[104:107], v[12:19], v[228:235], v[104:107], v245, v245 op_sel_hi:[0,0,0]
	v_mfma_scale_f32_16x16x128_f8f6f4 v[100:103], v[4:11], v[228:235], v[100:103], v245, v245 op_sel_hi:[0,0,0]
	s_setprio 0
	s_barrier
	s_add_i32 s73, s73, s17
	v_lshl_add_u64 v[178:179], s[60:61], 0, v[2:3]
	s_mov_b32 m0, s73
	ds_read_b128 v[186:189], v184 offset:16384
	ds_read_b128 v[190:193], v184 offset:17408
	ds_read_b128 v[208:211], v184 offset:18432
	ds_read_b128 v[212:215], v184 offset:19456
	ds_read_b128 v[216:219], v184 offset:20480
	ds_read_b128 v[220:223], v184 offset:21504
	ds_read_b128 v[228:231], v184 offset:22528
	ds_read_b128 v[232:235], v184 offset:23552
	global_load_lds_dwordx4 v2, s[60:61]
	s_add_i32 m0, s73, 0x2000
	s_add_u32 s74, s60, 0x58000
	v_lshl_add_u64 v[180:181], s[60:61], 0, v[164:165]
	s_addc_u32 s75, s61, 0
	s_add_i32 s72, s72, s17
	global_load_lds_dwordx4 v164, s[60:61]
	s_mov_b32 m0, s72
	v_lshl_add_u64 v[224:225], s[62:63], 0, v[166:167]
	global_load_lds_dwordx4 v2, s[74:75]
	s_add_i32 m0, s72, 0x2000
	s_nop 0
	global_load_lds_dwordx4 v164, s[74:75]
	v_lshl_add_u64 v[194:195], s[62:63], 0, v[168:169]
	s_mov_b32 m0, s18
	s_nop 0
	global_load_lds_dwordx4 v168, s[62:63]
	s_mov_b32 m0, s19
	s_nop 0
	global_load_lds_dwordx4 v166, s[62:63]
	s_cmp_eq_u32 s71, 0
	s_cbranch_scc1 .Lpg8skip3
	s_waitcnt vmcnt(8)
.Lpg8skip3:
	s_waitcnt lgkmcnt(0)
	s_barrier
	s_setprio 1
	s_waitcnt lgkmcnt(0)
	v_mfma_scale_f32_16x16x128_f8f6f4 v[96:99], v[28:35], v[186:193], v[96:99], v245, v245 op_sel_hi:[0,0,0]
	v_mfma_scale_f32_16x16x128_f8f6f4 v[92:95], v[20:27], v[186:193], v[92:95], v245, v245 op_sel_hi:[0,0,0]
	v_mfma_scale_f32_16x16x128_f8f6f4 v[80:83], v[28:35], v[208:215], v[80:83], v245, v245 op_sel_hi:[0,0,0]
	v_mfma_scale_f32_16x16x128_f8f6f4 v[76:79], v[20:27], v[208:215], v[76:79], v245, v245 op_sel_hi:[0,0,0]
	v_mfma_scale_f32_16x16x128_f8f6f4 v[64:67], v[28:35], v[216:223], v[64:67], v245, v245 op_sel_hi:[0,0,0]
	v_mfma_scale_f32_16x16x128_f8f6f4 v[60:63], v[20:27], v[216:223], v[60:63], v245, v245 op_sel_hi:[0,0,0]
	v_mfma_scale_f32_16x16x128_f8f6f4 v[48:51], v[28:35], v[228:235], v[48:51], v245, v245 op_sel_hi:[0,0,0]
	v_mfma_scale_f32_16x16x128_f8f6f4 v[44:47], v[20:27], v[228:235], v[44:47], v245, v245 op_sel_hi:[0,0,0]
	s_setprio 0
	s_setprio 1
	v_mfma_scale_f32_16x16x128_f8f6f4 v[88:91], v[12:19], v[186:193], v[88:91], v245, v245 op_sel_hi:[0,0,0]
	v_mfma_scale_f32_16x16x128_f8f6f4 v[84:87], v[4:11], v[186:193], v[84:87], v245, v245 op_sel_hi:[0,0,0]
	v_mfma_scale_f32_16x16x128_f8f6f4 v[72:75], v[12:19], v[208:215], v[72:75], v245, v245 op_sel_hi:[0,0,0]
	v_mfma_scale_f32_16x16x128_f8f6f4 v[68:71], v[4:11], v[208:215], v[68:71], v245, v245 op_sel_hi:[0,0,0]
	v_mfma_scale_f32_16x16x128_f8f6f4 v[56:59], v[12:19], v[216:223], v[56:59], v245, v245 op_sel_hi:[0,0,0]
	v_mfma_scale_f32_16x16x128_f8f6f4 v[52:55], v[4:11], v[216:223], v[52:55], v245, v245 op_sel_hi:[0,0,0]
	v_mfma_scale_f32_16x16x128_f8f6f4 v[40:43], v[12:19], v[228:235], v[40:43], v245, v245 op_sel_hi:[0,0,0]
	v_mfma_scale_f32_16x16x128_f8f6f4 v[36:39], v[4:11], v[228:235], v[36:39], v245, v245 op_sel_hi:[0,0,0]
	s_setprio 0
	s_barrier
	s_add_i32 s62, 0, 0x18000
	s_add_i32 s63, 0, 0x1c000
	v_add_u32_e32 v16, s62, v183
	v_add_u32_e32 v32, s63, v183
	ds_read_b128 v[4:7], v16
	ds_read_b128 v[8:11], v16 offset:1024
	ds_read_b128 v[12:15], v16 offset:2048
	ds_read_b128 v[16:19], v16 offset:3072
	ds_read_b128 v[20:23], v32
	ds_read_b128 v[24:27], v32 offset:1024
	ds_read_b128 v[28:31], v32 offset:2048
	ds_read_b128 v[32:35], v32 offset:3072
	s_mov_b32 m0, s20
	v_lshl_add_u64 v[194:195], v[194:195], 0, s[24:25]
	ds_read_b128 v[186:189], v184 offset:32768
	ds_read_b128 v[190:193], v184 offset:33792
	ds_read_b128 v[208:211], v184 offset:34816
	ds_read_b128 v[212:215], v184 offset:35840
	ds_read_b128 v[216:219], v184 offset:36864
	ds_read_b128 v[220:223], v184 offset:37888
	ds_read_b128 v[228:231], v184 offset:38912
	ds_read_b128 v[232:235], v184 offset:39936
	global_load_lds_dwordx4 v[194:195], off
	v_lshl_add_u64 v[194:195], v[224:225], 0, s[24:25]
	s_mov_b32 m0, s21
	s_nop 0
	global_load_lds_dwordx4 v[194:195], off
	s_waitcnt vmcnt(8)
	s_waitcnt lgkmcnt(0)
	s_barrier
; #define PG8_WAIT_V(n) asm volatile("s_waitcnt vmcnt(" #n ")" ::: "memory")
; #define PG8_WAIT_L(n) asm volatile("s_waitcnt lgkmcnt(" #n ")" ::: "memory")
; template <class Epi, class Sched, bool ALIGN_EPI = false, bool SP2 = false, bool FP8 = false, bool ABLK = false>
; __device__ __forceinline__ void gemm_phase(PG8_LAS unsigned char* lds, const Gemm g, const Sched& S, const Epi& E) {
;     ...
;             PG8_LDB(B0, 1, 0); PG8_LDB(B1, 1, 1); PG8_SCHED; PG8_LDA(At, 1, 0); PG8_STAGE(PG8_SA(0, 1), a2 + hstepA, voffA);
;             PG8_WAIT_V(8); PG8_WAIT_L(0); PG8_BAR; PG8_MMA(0, 0, At, B0); PG8_MMA(0, 1, At, B1); PG8_BAR; PG8_SCHED;
;             PG8_LDA(At, 1, 1); PG8_STAGE(PG8_SB(1, 0), b3, voffB); PG8_STAGE(PG8_SB(1, 1), b3 + hstep, voffB); PG8_STAGE(PG8_SA(1, 0), a3, voffA);
;             PG8_WAIT_V(8); PG8_WAIT_L(0); PG8_BAR; PG8_MMA(1, 0, At, B0); PG8_MMA(1, 1, At, B1); PG8_BAR; PG8_SCHED;
;             } else {
;             PG8_LDB(B0, 0, 0); PG8_SCHED; PG8_LDA(At, 0, 0); PG8_STAGE(PG8_SA(1, 1), a1 + hstepA, voffA);
;             PG8_WAIT_L(8); PG8_BAR; PG8_WAIT_L(0); PG8_MMA(0, 0, At, B0); PG8_BAR; PG8_SCHED;
;             PG8_LDB(B1, 0, 1); PG8_STAGE(PG8_SB(0, 0), b2, voffB);
;             PG8_BAR; PG8_WAIT_L(0); PG8_MMA(0, 1, At, B1); PG8_BAR;
;             PG8_LDA(At, 0, 1); PG8_STAGE(PG8_SA(0, 0), a2, voffA);
;             PG8_BAR; PG8_WAIT_L(0); PG8_MMA(1, 0, At, B0); PG8_BAR; PG8_SCHED;
;             PG8_STAGE(PG8_SB(0, 1), b2 + hstep, voffB);
;             PG8_WAIT_V(6); PG8_BAR; PG8_MMA(1, 1, At, B1); PG8_BAR;
;             PG8_LDB(B0, 1, 0); PG8_SCHED; PG8_LDA(At, 1, 0); PG8_STAGE(PG8_SA(0, 1), a2 + hstepA, voffA);
;             PG8_WAIT_L(8); PG8_BAR; PG8_WAIT_L(0); PG8_MMA(0, 0, At, B0); PG8_BAR; PG8_SCHED;
;             PG8_LDB(B1, 1, 1); PG8_STAGE(PG8_SB(1, 0), b3, voffB);
;             PG8_BAR; PG8_WAIT_L(0); PG8_MMA(0, 1, At, B1); PG8_BAR;
;             PG8_LDA(At, 1, 1); PG8_STAGE(PG8_SA(1, 0), a3, voffA);
;             PG8_BAR; PG8_WAIT_L(0); PG8_MMA(1, 0, At, B0); PG8_BAR; PG8_SCHED;
;             PG8_STAGE(PG8_SB(1, 1), b3 + hstep, voffB);
;             PG8_WAIT_V(6); PG8_BAR; PG8_MMA(1, 1, At, B1); PG8_BAR;
;             }
;         }
;         if constexpr (SP2) PG8_WAIT_V(0);
;         if constexpr (FP8) asm volatile("s_nop 15\n\ts_nop 15" ::: "memory");
;         if constexpr (ALIGN_EPI) { if (wr == 0) PG8_BAR; }
	s_setprio 1
	s_waitcnt lgkmcnt(0)
	v_mfma_scale_f32_16x16x128_f8f6f4 v[160:163], v[4:11], v[186:193], v[160:163], v245, v245 op_sel_hi:[0,0,0]
	v_mfma_scale_f32_16x16x128_f8f6f4 v[156:159], v[12:19], v[186:193], v[156:159], v245, v245 op_sel_hi:[0,0,0]
	v_mfma_scale_f32_16x16x128_f8f6f4 v[144:147], v[4:11], v[208:215], v[144:147], v245, v245 op_sel_hi:[0,0,0]
	v_mfma_scale_f32_16x16x128_f8f6f4 v[140:143], v[12:19], v[208:215], v[140:143], v245, v245 op_sel_hi:[0,0,0]
	v_mfma_scale_f32_16x16x128_f8f6f4 v[128:131], v[4:11], v[216:223], v[128:131], v245, v245 op_sel_hi:[0,0,0]
	v_mfma_scale_f32_16x16x128_f8f6f4 v[124:127], v[12:19], v[216:223], v[124:127], v245, v245 op_sel_hi:[0,0,0]
	v_mfma_scale_f32_16x16x128_f8f6f4 v[112:115], v[4:11], v[228:235], v[112:115], v245, v245 op_sel_hi:[0,0,0]
	v_mfma_scale_f32_16x16x128_f8f6f4 v[108:111], v[12:19], v[228:235], v[108:111], v245, v245 op_sel_hi:[0,0,0]
	s_setprio 0
	s_setprio 1
	v_mfma_scale_f32_16x16x128_f8f6f4 v[152:155], v[20:27], v[186:193], v[152:155], v245, v245 op_sel_hi:[0,0,0]
	v_mfma_scale_f32_16x16x128_f8f6f4 v[148:151], v[28:35], v[186:193], v[148:151], v245, v245 op_sel_hi:[0,0,0]
	v_mfma_scale_f32_16x16x128_f8f6f4 v[136:139], v[20:27], v[208:215], v[136:139], v245, v245 op_sel_hi:[0,0,0]
	v_mfma_scale_f32_16x16x128_f8f6f4 v[132:135], v[28:35], v[208:215], v[132:135], v245, v245 op_sel_hi:[0,0,0]
	v_mfma_scale_f32_16x16x128_f8f6f4 v[120:123], v[20:27], v[216:223], v[120:123], v245, v245 op_sel_hi:[0,0,0]
	v_mfma_scale_f32_16x16x128_f8f6f4 v[116:119], v[28:35], v[216:223], v[116:119], v245, v245 op_sel_hi:[0,0,0]
	v_mfma_scale_f32_16x16x128_f8f6f4 v[104:107], v[20:27], v[228:235], v[104:107], v245, v245 op_sel_hi:[0,0,0]
	v_mfma_scale_f32_16x16x128_f8f6f4 v[100:103], v[28:35], v[228:235], v[100:103], v245, v245 op_sel_hi:[0,0,0]
	s_setprio 0
	s_barrier
	s_add_i32 s62, s62, s17
	v_lshl_add_u64 v[178:179], v[178:179], 0, s[34:35]
	s_mov_b32 m0, s62
	ds_read_b128 v[186:189], v184 offset:49152
	ds_read_b128 v[190:193], v184 offset:50176
	ds_read_b128 v[208:211], v184 offset:51200
	ds_read_b128 v[212:215], v184 offset:52224
	ds_read_b128 v[216:219], v184 offset:53248
	ds_read_b128 v[220:223], v184 offset:54272
	ds_read_b128 v[228:231], v184 offset:55296
	ds_read_b128 v[232:235], v184 offset:56320
	global_load_lds_dwordx4 v[178:179], off
	s_add_i32 m0, s62, 0x2000
	s_add_u32 s60, s60, 0x58080
	v_lshl_add_u64 v[178:179], v[180:181], 0, s[34:35]
	s_addc_u32 s61, s61, 0
	s_add_i32 s62, s63, s17
	global_load_lds_dwordx4 v[178:179], off
	s_mov_b32 m0, s62
	s_nop 0
	global_load_lds_dwordx4 v2, s[60:61]
	s_add_i32 m0, s62, 0x2000
	s_nop 0
	global_load_lds_dwordx4 v164, s[60:61]
	s_mov_b32 m0, s64
	s_nop 0
	global_load_lds_dwordx4 v168, s[58:59]
	s_mov_b32 m0, s65
	s_nop 0
	global_load_lds_dwordx4 v166, s[58:59]
	s_waitcnt vmcnt(8)
	s_waitcnt lgkmcnt(0)
	s_barrier
	s_setprio 1
	s_waitcnt lgkmcnt(0)
	v_mfma_scale_f32_16x16x128_f8f6f4 v[96:99], v[4:11], v[186:193], v[96:99], v245, v245 op_sel_hi:[0,0,0]
	v_mfma_scale_f32_16x16x128_f8f6f4 v[92:95], v[12:19], v[186:193], v[92:95], v245, v245 op_sel_hi:[0,0,0]
	v_mfma_scale_f32_16x16x128_f8f6f4 v[80:83], v[4:11], v[208:215], v[80:83], v245, v245 op_sel_hi:[0,0,0]
	v_mfma_scale_f32_16x16x128_f8f6f4 v[76:79], v[12:19], v[208:215], v[76:79], v245, v245 op_sel_hi:[0,0,0]
	v_mfma_scale_f32_16x16x128_f8f6f4 v[64:67], v[4:11], v[216:223], v[64:67], v245, v245 op_sel_hi:[0,0,0]
	v_mfma_scale_f32_16x16x128_f8f6f4 v[60:63], v[12:19], v[216:223], v[60:63], v245, v245 op_sel_hi:[0,0,0]
	v_mfma_scale_f32_16x16x128_f8f6f4 v[48:51], v[4:11], v[228:235], v[48:51], v245, v245 op_sel_hi:[0,0,0]
	v_mfma_scale_f32_16x16x128_f8f6f4 v[44:47], v[12:19], v[228:235], v[44:47], v245, v245 op_sel_hi:[0,0,0]
	s_setprio 0
	s_setprio 1
	v_mfma_scale_f32_16x16x128_f8f6f4 v[88:91], v[20:27], v[186:193], v[88:91], v245, v245 op_sel_hi:[0,0,0]
	v_mfma_scale_f32_16x16x128_f8f6f4 v[84:87], v[28:35], v[186:193], v[84:87], v245, v245 op_sel_hi:[0,0,0]
	v_mfma_scale_f32_16x16x128_f8f6f4 v[72:75], v[20:27], v[208:215], v[72:75], v245, v245 op_sel_hi:[0,0,0]
	v_mfma_scale_f32_16x16x128_f8f6f4 v[68:71], v[28:35], v[208:215], v[68:71], v245, v245 op_sel_hi:[0,0,0]
	v_mfma_scale_f32_16x16x128_f8f6f4 v[56:59], v[20:27], v[216:223], v[56:59], v245, v245 op_sel_hi:[0,0,0]
	v_mfma_scale_f32_16x16x128_f8f6f4 v[52:55], v[28:35], v[216:223], v[52:55], v245, v245 op_sel_hi:[0,0,0]
	v_mfma_scale_f32_16x16x128_f8f6f4 v[40:43], v[20:27], v[228:235], v[40:43], v245, v245 op_sel_hi:[0,0,0]
	v_mfma_scale_f32_16x16x128_f8f6f4 v[36:39], v[28:35], v[228:235], v[36:39], v245, v245 op_sel_hi:[0,0,0]
	s_setprio 0
	s_barrier
	s_add_u32 s4, s4, 0x100
	s_addc_u32 s5, s5, 0
	s_add_u32 s56, s56, 0x10000
	s_addc_u32 s57, s57, 0
	s_cmp_gt_u32 s71, 19
	s_cbranch_scc0 .LBB0_508
	s_waitcnt vmcnt(0)
	s_nop 15
	s_nop 15
	s_and_b64 vcc, exec, s[50:51]
	s_cbranch_vccz .LBB0_511
	s_barrier

; #define PG8_STAGE(bufoff, gbase, voff) do { _Pragma("unroll") for (int _i = 0; _i < 2; ++_i) \
;         __builtin_amdgcn_global_load_lds((const unsigned*)((const char*)(gbase) + (voff)[_i]), (PG8_LAS unsigned*)(lds + (bufoff) + ldsw + _i * 8192), 16, 0, 0); } while (0)
; #define PG8_WAIT_V(n) asm volatile("s_waitcnt vmcnt(" #n ")" ::: "memory")
; #define PG8_BAR __builtin_amdgcn_s_barrier()
;     __device__ __forceinline__ void operator()(const f32x4 (&acc)[2][2][4][2], const Unit& u, int wr, int wc, int fr, int fq) const {
;         if (u.pm >= TILE_X) { const EpiWin W{ws, ss, qscale}; const Unit v{u.pm - TILE_X, u.pn - tin}; W(acc, v, wr, wc, fr, fq); }
;         else { const EpiMemKV KV{(bf16_t*)(ws + WS_MEMK), (bf16_t*)(ws + WS_MEMVT), (const float*)(ws + WS_MSS)}; const Unit v{u.pm - TILE_MK, u.pn - TILE_MK}; KV(acc, v, wr, wc, fr, fq); }
; template <class Epi, class Sched, bool ALIGN_EPI = false, bool SP2 = false, bool FP8 = false, bool ABLK = false>
; __device__ __forceinline__ void gemm_phase(PG8_LAS unsigned char* lds, const Gemm g, const Sched& S, const Epi& E) {
;     ...
;     const char* cA = (const char*)g.A + (size_t)cur.pm * tstep; const char* cB = (const char*)g.Bt + (size_t)cur.pn * tstep;
;     S.a_ready(cur);
;     if constexpr (SP2) {
;         PG8_STAGE(PG8_SB(0, 0), cB, voffB); PG8_STAGE(PG8_SB(0, 1), cB + hstep, voffB); PG8_STAGE(PG8_SA(0, 0), cA, voffA); PG8_STAGE(PG8_SA(0, 1), cA + hstepA, voffA);
;         if (wr == 1) PG8_BAR;
;         PG8_WAIT_V(2); PG8_BAR;
;         PG8_STAGE(PG8_SB(1, 0), cB + kstep, voffB); PG8_STAGE(PG8_SA(1, 0), cA + kstepA, voffA); PG8_STAGE(PG8_SB(1, 1), cB + hstep + kstep, voffB);
;         PG8_WAIT_V(0); PG8_BAR;
;     } else {
;         PG8_STAGE(PG8_SB(0, 0), cB, voffB); PG8_STAGE(PG8_SA(0, 0), cA, voffA); PG8_STAGE(PG8_SB(0, 1), cB + hstep, voffB); PG8_STAGE(PG8_SA(0, 1), cA + hstepA, voffA);
;         if (wr == 1) PG8_BAR;
;         PG8_WAIT_V(4); PG8_BAR;
;         PG8_STAGE(PG8_SB(1, 0), cB + kstep, voffB); PG8_STAGE(PG8_SA(1, 0), cA + kstepA, voffA); PG8_STAGE(PG8_SB(1, 1), cB + hstep + kstep, voffB);
;         PG8_WAIT_V(6); PG8_BAR;
;     }
;     for (;;) {
;         const bool has_next = S.next(ui + 1, nxt);
;         const char* nA = has_next ? (const char*)g.A + (size_t)nxt.pm * tstep : cA; const char* nB = has_next ? (const char*)g.Bt + (size_t)nxt.pn * tstep : cB;
.LBB0_587:
	s_add_u32 s50, s38, 0x1c200000
	s_addc_u32 s51, s39, 0
	s_add_u32 s52, s38, 0x300000
	s_addc_u32 s53, s39, 0
	s_add_u32 s22, s38, 0x15a00000
	s_addc_u32 s23, s39, 0
	s_add_u32 s56, s38, 0x400000
	v_writelane_b32 v252, s22, 28
	s_addc_u32 s57, s39, 0
	v_bfe_u32 v187, v18, 4, 2
	v_writelane_b32 v252, s23, 29
	s_add_u32 s22, s38, 0x15e00000
	s_addc_u32 s23, s39, 0
	s_add_u32 s60, s38, 0xda00000
	s_addc_u32 s61, s39, 0
	s_add_u32 s62, s38, 0x800000
	v_writelane_b32 v252, s22, 30
	s_addc_u32 s63, s39, 0
	s_add_u32 s19, s38, 0x10a00000
	v_writelane_b32 v252, s23, 31
	v_writelane_b32 v252, s19, 32
	s_addc_u32 s19, s39, 0
	v_writelane_b32 v252, s19, 33
	s_add_u32 s19, s38, 0xea00000
	v_writelane_b32 v252, s19, 34
	s_addc_u32 s19, s39, 0
	v_writelane_b32 v252, s19, 35
	s_add_u32 s19, s38, 0x12a00000
	v_writelane_b32 v252, s19, 36
	s_addc_u32 s19, s39, 0
	s_add_u32 s54, s38, 0xba00000
	v_and_b32_e32 v1, 15, v18
	v_lshlrev_b32_e32 v19, 4, v187
	v_lshlrev_b32_e32 v18, 2, v18
	s_addc_u32 s55, s39, 0
	s_and_b32 s40, s5, 3
	s_lshl_b32 s58, s4, 6
	v_lshl_or_b32 v19, v1, 6, v19
	s_lshl_b32 s4, s4, 13
	v_and_b32_e32 v18, 32, v18
	s_add_i32 m0, s8, 0x18000
	v_lshl_add_u64 v[10:11], v[10:11], 0, s[34:35]
	v_writelane_b32 v252, s19, 37
	v_bitop3_b32 v20, v19, s4, v18 bitop3:0xde
	s_lshl_b32 s59, s40, 5
	s_lshl_b32 s4, s40, 12
	s_waitcnt vmcnt(2)
	s_barrier
	global_load_lds_dwordx4 v[10:11], off
	v_lshl_add_u64 v[8:9], v[8:9], 0, s[34:35]
	s_add_i32 m0, s8, 0x1a000
	s_add_i32 s19, s8, 0x8000
	s_add_i32 s20, s8, 0xa000
	v_bitop3_b32 v191, v19, s4, v18 bitop3:0xde
	global_load_lds_dwordx4 v[8:9], off
	v_lshl_add_u64 v[4:5], v[4:5], 0, s[34:35]
	s_mov_b32 m0, s19
	s_add_u32 s4, s44, 0x40080
	global_load_lds_dwordx4 v[4:5], off
	v_lshl_add_u64 v[4:5], v[6:7], 0, s[34:35]
	s_mov_b32 m0, s20
	s_addc_u32 s5, s45, 0
	global_load_lds_dwordx4 v[4:5], off
	s_add_i32 m0, s8, 0x1c000
	s_nop 0
	global_load_lds_dwordx4 v2, s[4:5]
	s_add_i32 m0, s8, 0x1e000
	s_cmpk_lt_u32 s21, 0x100
	global_load_lds_dwordx4 v172, s[4:5]
	s_cselect_b64 s[64:65], -1, 0
	s_add_i32 s21, s58, 0xffff0c00
	s_cmp_eq_u32 s40, 0
	v_lshlrev_b32_e32 v4, 14, v16
	s_cselect_b64 s[66:67], -1, 0
	s_cmp_eq_u32 s40, 1
	v_and_b32_e32 v4, 0xffff8000, v4
	s_cselect_b64 s[68:69], -1, 0
	s_lshl_b32 s4, s40, 6
	v_lshl_add_u32 v4, v15, 11, v4
	v_and_b32_e32 v5, 1, v16
	s_or_b32 s23, s4, 0xfffff900
	s_or_b32 s81, s4, 0xfffffb00
	s_lshl_b32 s4, s40, 12
	v_lshl_or_b32 v4, v5, 6, v4
	s_add_u32 s4, s38, s4
	v_lshl_add_u32 v178, v17, 1, v4
	v_lshlrev_b32_e32 v4, 14, v12
	s_addc_u32 s5, s39, 0
	v_and_b32_e32 v4, 0xffff8000, v4
	s_waitcnt vmcnt(0)
	s_add_u32 s70, s4, 0x14a00000
	v_lshl_add_u32 v4, v13, 11, v4
	v_and_b32_e32 v5, 1, v12
	s_addc_u32 s71, s5, 0
	v_lshl_or_b32 v4, v5, 6, v4
	v_readlane_b32 s4, v254, 42
	s_mov_b32 s47, s93
	s_mov_b32 s22, 0
	v_mov_b32_e32 v179, v3
	v_lshl_add_u32 v180, v14, 1, v4
	v_mov_b32_e32 v181, v3
	v_add_u32_e32 v195, 0, v20
	s_mov_b32 s73, s4
	s_barrier
	v_readlane_b32 s5, v254, 43
	s_branch .LBB0_590

; #define PG8_STAGE(bufoff, gbase, voff) do { _Pragma("unroll") for (int _i = 0; _i < 2; ++_i) \
;         __builtin_amdgcn_global_load_lds((const unsigned*)((const char*)(gbase) + (voff)[_i]), (PG8_LAS unsigned*)(lds + (bufoff) + ldsw + _i * 8192), 16, 0, 0); } while (0)
; #define PG8_LDA(dst, b, h) do { _Pragma("unroll") for (int m = 0; m < 4; ++m) _Pragma("unroll") for (int k = 0; k < 2; ++k) dst[m][k] = *(const PG8_LAS bf16x8*)(lds + PG8_SA(b, h) + aoff + m * 2048 + k * 1024); } while (0)
; #define PG8_LDB(dst, b, h) do { _Pragma("unroll") for (int n = 0; n < 2; ++n) _Pragma("unroll") for (int k = 0; k < 2; ++k) dst[n][k] = *(const PG8_LAS bf16x8*)(lds + PG8_SB(b, h) + boff + n * 2048 + k * 1024); } while (0)
; #define PG8_WAIT_V8_UNLESS_FIRST(t) asm volatile("s_cmp_eq_u32 %0, 0\n\ts_cbranch_scc1 .Lpg8skip%=\n\ts_waitcnt vmcnt(8)\n.Lpg8skip%=:" :: "s"(t) : "scc", "memory")
; #define PG8_WAIT_L(n) asm volatile("s_waitcnt lgkmcnt(" #n ")" ::: "memory")
; #define PG8_BAR __builtin_amdgcn_s_barrier()
; #define PG8_SCHED __builtin_amdgcn_sched_barrier(0)
; template <class Epi, class Sched, bool ALIGN_EPI = false, bool SP2 = false, bool FP8 = false, bool ABLK = false>
; __device__ __forceinline__ void gemm_phase(PG8_LAS unsigned char* lds, const Gemm g, const Sched& S, const Epi& E) {
;     ...
;         for (int t = 0; t < nt; t += 2) {
;             const bool last = (t == nt - 2);
;             const char* a1 = cA + (size_t)(t + 1) * kstepA;
;             const char* a2 = last ? nA : cA + (size_t)(t + 2) * kstepA; const char* b2 = last ? nB : cB + (size_t)(t + 2) * kstep;
;             const char* a3 = a2 + kstepA; const char* b3 = b2 + kstep;
;             if (last && has_next) S.a_ready(nxt);
;             if constexpr (SP2) {
;             PG8_LDB(B0, 0, 0); PG8_LDB(B1, 0, 1); PG8_SCHED; PG8_LDA(At, 0, 0); PG8_STAGE(PG8_SA(1, 1), a1 + hstepA, voffA);
;             PG8_WAIT_V8_UNLESS_FIRST(t); PG8_WAIT_L(0); PG8_BAR; PG8_MMA(0, 0, At, B0); PG8_MMA(0, 1, At, B1); PG8_BAR; PG8_SCHED;
;             PG8_LDA(At, 0, 1); PG8_STAGE(PG8_SB(0, 0), b2, voffB); PG8_STAGE(PG8_SB(0, 1), b2 + hstep, voffB); PG8_STAGE(PG8_SA(0, 0), a2, voffA);
;             PG8_WAIT_V8_UNLESS_FIRST(t); PG8_WAIT_L(0); PG8_BAR; PG8_MMA(1, 0, At, B0); PG8_MMA(1, 1, At, B1); PG8_BAR; PG8_SCHED;
.LBB0_600:
	s_add_i32 s95, s44, 2
	s_add_u32 s45, s42, 0xfffc0080
	s_addc_u32 s90, s43, -1
	s_add_i32 s96, 0, 0x10000
	s_cmp_eq_u32 s44, 12
	s_cselect_b32 s91, s4, s90
	s_cselect_b32 s90, s5, s45
	s_cselect_b32 s45, s75, s94
	s_cselect_b32 s44, s77, s92
	s_add_i32 vcc_lo, 0, 0x14000
	v_add_u32_e32 v144, s96, v191
	v_add_u32_e32 v160, vcc_lo, v191
	ds_read_b128 v[132:135], v144
	ds_read_b128 v[136:139], v144 offset:1024
	ds_read_b128 v[140:143], v144 offset:2048
	ds_read_b128 v[144:147], v144 offset:3072
	ds_read_b128 v[148:151], v160
	ds_read_b128 v[152:155], v160 offset:1024
	ds_read_b128 v[156:159], v160 offset:2048
	ds_read_b128 v[160:163], v160 offset:3072
	s_add_i32 m0, s8, 0xc000
	ds_read_b128 v[164:167], v195
	ds_read_b128 v[168:171], v195 offset:1024
	ds_read_b128 v[182:185], v195 offset:2048
	ds_read_b128 v[208:211], v195 offset:3072
	ds_read_b128 v[212:215], v195 offset:4096
	ds_read_b128 v[216:219], v195 offset:5120
	ds_read_b128 v[220:223], v195 offset:6144
	ds_read_b128 v[228:231], v195 offset:7168
	global_load_lds_dwordx4 v178, s[42:43]
	s_add_i32 m0, s8, 0xe000
	s_nop 0
	global_load_lds_dwordx4 v180, s[42:43]
	s_cmp_eq_u32 s95, 0
	s_cbranch_scc1 .Lpg8skip4
	s_waitcnt vmcnt(8)
.Lpg8skip4:
	s_waitcnt lgkmcnt(0)
	s_barrier
	s_setprio 1
	s_waitcnt lgkmcnt(0)
	v_mfma_f32_16x16x32_bf16 v[128:131], v[132:135], v[164:167], v[128:131]
	v_mfma_f32_16x16x32_bf16 v[124:127], v[140:143], v[164:167], v[124:127]
	v_mfma_f32_16x16x32_bf16 v[112:115], v[132:135], v[182:185], v[112:115]
	v_mfma_f32_16x16x32_bf16 v[108:111], v[140:143], v[182:185], v[108:111]
	v_mfma_f32_16x16x32_bf16 v[96:99], v[132:135], v[212:215], v[96:99]
	v_mfma_f32_16x16x32_bf16 v[92:95], v[140:143], v[212:215], v[92:95]
	v_mfma_f32_16x16x32_bf16 v[80:83], v[132:135], v[220:223], v[80:83]
	v_mfma_f32_16x16x32_bf16 v[76:79], v[140:143], v[220:223], v[76:79]
	v_mfma_f32_16x16x32_bf16 v[128:131], v[136:139], v[168:171], v[128:131]
	v_mfma_f32_16x16x32_bf16 v[124:127], v[144:147], v[168:171], v[124:127]
	v_mfma_f32_16x16x32_bf16 v[112:115], v[136:139], v[208:211], v[112:115]
	v_mfma_f32_16x16x32_bf16 v[108:111], v[144:147], v[208:211], v[108:111]
	v_mfma_f32_16x16x32_bf16 v[96:99], v[136:139], v[216:219], v[96:99]
	v_mfma_f32_16x16x32_bf16 v[92:95], v[144:147], v[216:219], v[92:95]
	v_mfma_f32_16x16x32_bf16 v[80:83], v[136:139], v[228:231], v[80:83]
	v_mfma_f32_16x16x32_bf16 v[76:79], v[144:147], v[228:231], v[76:79]
	s_setprio 0
	s_setprio 1
	v_mfma_f32_16x16x32_bf16 v[120:123], v[148:151], v[164:167], v[120:123]
	v_mfma_f32_16x16x32_bf16 v[116:119], v[156:159], v[164:167], v[116:119]
	v_mfma_f32_16x16x32_bf16 v[104:107], v[148:151], v[182:185], v[104:107]
	v_mfma_f32_16x16x32_bf16 v[100:103], v[156:159], v[182:185], v[100:103]
	v_mfma_f32_16x16x32_bf16 v[88:91], v[148:151], v[212:215], v[88:91]
	v_mfma_f32_16x16x32_bf16 v[84:87], v[156:159], v[212:215], v[84:87]
	v_mfma_f32_16x16x32_bf16 v[72:75], v[148:151], v[220:223], v[72:75]
	v_mfma_f32_16x16x32_bf16 v[68:71], v[156:159], v[220:223], v[68:71]
	v_mfma_f32_16x16x32_bf16 v[120:123], v[152:155], v[168:171], v[120:123]
	v_mfma_f32_16x16x32_bf16 v[116:119], v[160:163], v[168:171], v[116:119]
	v_mfma_f32_16x16x32_bf16 v[104:107], v[152:155], v[208:211], v[104:107]
	v_mfma_f32_16x16x32_bf16 v[100:103], v[160:163], v[208:211], v[100:103]
	v_mfma_f32_16x16x32_bf16 v[88:91], v[152:155], v[216:219], v[88:91]
	v_mfma_f32_16x16x32_bf16 v[84:87], v[160:163], v[216:219], v[84:87]
	v_mfma_f32_16x16x32_bf16 v[72:75], v[152:155], v[228:231], v[72:75]
	v_mfma_f32_16x16x32_bf16 v[68:71], v[160:163], v[228:231], v[68:71]
	s_setprio 0
	s_barrier
	s_add_i32 s96, s96, s7
	v_lshl_add_u64 v[188:189], s[44:45], 0, v[2:3]
	s_mov_b32 m0, s96
	ds_read_b128 v[164:167], v195 offset:16384
	ds_read_b128 v[168:171], v195 offset:17408
	ds_read_b128 v[182:185], v195 offset:18432
	ds_read_b128 v[208:211], v195 offset:19456
	ds_read_b128 v[212:215], v195 offset:20480
	ds_read_b128 v[216:219], v195 offset:21504
	ds_read_b128 v[220:223], v195 offset:22528
	ds_read_b128 v[228:231], v195 offset:23552
	global_load_lds_dwordx4 v2, s[44:45]
	s_add_i32 m0, s96, 0x2000
	s_add_u32 s96, s44, 0x40000
	v_lshl_add_u64 v[192:193], s[44:45], 0, v[172:173]
	s_addc_u32 s97, s45, 0
	s_add_i32 vcc_lo, vcc_lo, s7
	global_load_lds_dwordx4 v172, s[44:45]
	s_mov_b32 m0, vcc_lo
	v_lshl_add_u64 v[232:233], s[90:91], 0, v[174:175]
	global_load_lds_dwordx4 v2, s[96:97]
	s_add_i32 m0, vcc_lo, 0x2000
	s_nop 0
	global_load_lds_dwordx4 v172, s[96:97]
	v_lshl_add_u64 v[224:225], s[90:91], 0, v[176:177]
	s_mov_b32 m0, s8
	s_nop 0
	global_load_lds_dwordx4 v176, s[90:91]
	s_mov_b32 m0, s9
	s_nop 0
	global_load_lds_dwordx4 v174, s[90:91]
	s_cmp_eq_u32 s95, 0
	s_cbranch_scc1 .Lpg8skip5
	s_waitcnt vmcnt(8)
; #define PG8_STAGE(bufoff, gbase, voff) do { _Pragma("unroll") for (int _i = 0; _i < 2; ++_i) \
;         __builtin_amdgcn_global_load_lds((const unsigned*)((const char*)(gbase) + (voff)[_i]), (PG8_LAS unsigned*)(lds + (bufoff) + ldsw + _i * 8192), 16, 0, 0); } while (0)
; #define PG8_LDA(dst, b, h) do { _Pragma("unroll") for (int m = 0; m < 4; ++m) _Pragma("unroll") for (int k = 0; k < 2; ++k) dst[m][k] = *(const PG8_LAS bf16x8*)(lds + PG8_SA(b, h) + aoff + m * 2048 + k * 1024); } while (0)
; #define PG8_LDB(dst, b, h) do { _Pragma("unroll") for (int n = 0; n < 2; ++n) _Pragma("unroll") for (int k = 0; k < 2; ++k) dst[n][k] = *(const PG8_LAS bf16x8*)(lds + PG8_SB(b, h) + boff + n * 2048 + k * 1024); } while (0)
; #define PG8_WAIT_V(n) asm volatile("s_waitcnt vmcnt(" #n ")" ::: "memory")
; #define PG8_WAIT_V8_UNLESS_FIRST(t) asm volatile("s_cmp_eq_u32 %0, 0\n\ts_cbranch_scc1 .Lpg8skip%=\n\ts_waitcnt vmcnt(8)\n.Lpg8skip%=:" :: "s"(t) : "scc", "memory")
; #define PG8_WAIT_L(n) asm volatile("s_waitcnt lgkmcnt(" #n ")" ::: "memory")
; #define PG8_BAR __builtin_amdgcn_s_barrier()
; #define PG8_SCHED __builtin_amdgcn_sched_barrier(0)
; template <class Epi, class Sched, bool ALIGN_EPI = false, bool SP2 = false, bool FP8 = false, bool ABLK = false>
; __device__ __forceinline__ void gemm_phase(PG8_LAS unsigned char* lds, const Gemm g, const Sched& S, const Epi& E) {
;     ...
;             PG8_WAIT_V8_UNLESS_FIRST(t); PG8_WAIT_L(0); PG8_BAR; PG8_MMA(0, 0, At, B0); PG8_MMA(0, 1, At, B1); PG8_BAR; PG8_SCHED;
;             PG8_LDA(At, 0, 1); PG8_STAGE(PG8_SB(0, 0), b2, voffB); PG8_STAGE(PG8_SB(0, 1), b2 + hstep, voffB); PG8_STAGE(PG8_SA(0, 0), a2, voffA);
;             PG8_WAIT_V8_UNLESS_FIRST(t); PG8_WAIT_L(0); PG8_BAR; PG8_MMA(1, 0, At, B0); PG8_MMA(1, 1, At, B1); PG8_BAR; PG8_SCHED;
;             PG8_LDB(B0, 1, 0); PG8_LDB(B1, 1, 1); PG8_SCHED; PG8_LDA(At, 1, 0); PG8_STAGE(PG8_SA(0, 1), a2 + hstepA, voffA);
;             PG8_WAIT_V(8); PG8_WAIT_L(0); PG8_BAR; PG8_MMA(0, 0, At, B0); PG8_MMA(0, 1, At, B1); PG8_BAR; PG8_SCHED;
;             PG8_LDA(At, 1, 1); PG8_STAGE(PG8_SB(1, 0), b3, voffB); PG8_STAGE(PG8_SB(1, 1), b3 + hstep, voffB); PG8_STAGE(PG8_SA(1, 0), a3, voffA);
;             PG8_WAIT_V(8); PG8_WAIT_L(0); PG8_BAR; PG8_MMA(1, 0, At, B0); PG8_MMA(1, 1, At, B1); PG8_BAR; PG8_SCHED;
.Lpg8skip5:
	s_waitcnt lgkmcnt(0)
	s_barrier
	s_setprio 1
	s_waitcnt lgkmcnt(0)
	v_mfma_f32_16x16x32_bf16 v[64:67], v[132:135], v[164:167], v[64:67]
	v_mfma_f32_16x16x32_bf16 v[60:63], v[140:143], v[164:167], v[60:63]
	v_mfma_f32_16x16x32_bf16 v[48:51], v[132:135], v[182:185], v[48:51]
	v_mfma_f32_16x16x32_bf16 v[44:47], v[140:143], v[182:185], v[44:47]
	v_mfma_f32_16x16x32_bf16 v[32:35], v[132:135], v[212:215], v[32:35]
	v_mfma_f32_16x16x32_bf16 v[28:31], v[140:143], v[212:215], v[28:31]
	v_mfma_f32_16x16x32_bf16 v[16:19], v[132:135], v[220:223], v[16:19]
	v_mfma_f32_16x16x32_bf16 v[12:15], v[140:143], v[220:223], v[12:15]
	v_mfma_f32_16x16x32_bf16 v[64:67], v[136:139], v[168:171], v[64:67]
	v_mfma_f32_16x16x32_bf16 v[60:63], v[144:147], v[168:171], v[60:63]
	v_mfma_f32_16x16x32_bf16 v[48:51], v[136:139], v[208:211], v[48:51]
	v_mfma_f32_16x16x32_bf16 v[44:47], v[144:147], v[208:211], v[44:47]
	v_mfma_f32_16x16x32_bf16 v[32:35], v[136:139], v[216:219], v[32:35]
	v_mfma_f32_16x16x32_bf16 v[28:31], v[144:147], v[216:219], v[28:31]
	v_mfma_f32_16x16x32_bf16 v[16:19], v[136:139], v[228:231], v[16:19]
	v_mfma_f32_16x16x32_bf16 v[12:15], v[144:147], v[228:231], v[12:15]
	s_setprio 0
	s_setprio 1
	v_mfma_f32_16x16x32_bf16 v[56:59], v[148:151], v[164:167], v[56:59]
	v_mfma_f32_16x16x32_bf16 v[52:55], v[156:159], v[164:167], v[52:55]
	v_mfma_f32_16x16x32_bf16 v[40:43], v[148:151], v[182:185], v[40:43]
	v_mfma_f32_16x16x32_bf16 v[36:39], v[156:159], v[182:185], v[36:39]
	v_mfma_f32_16x16x32_bf16 v[24:27], v[148:151], v[212:215], v[24:27]
	v_mfma_f32_16x16x32_bf16 v[20:23], v[156:159], v[212:215], v[20:23]
	v_mfma_f32_16x16x32_bf16 v[8:11], v[148:151], v[220:223], v[8:11]
	v_mfma_f32_16x16x32_bf16 v[4:7], v[156:159], v[220:223], v[4:7]
	v_mfma_f32_16x16x32_bf16 v[56:59], v[152:155], v[168:171], v[56:59]
	v_mfma_f32_16x16x32_bf16 v[52:55], v[160:163], v[168:171], v[52:55]
	v_mfma_f32_16x16x32_bf16 v[40:43], v[152:155], v[208:211], v[40:43]
	v_mfma_f32_16x16x32_bf16 v[36:39], v[160:163], v[208:211], v[36:39]
	v_mfma_f32_16x16x32_bf16 v[24:27], v[152:155], v[216:219], v[24:27]
	v_mfma_f32_16x16x32_bf16 v[20:23], v[160:163], v[216:219], v[20:23]
	v_mfma_f32_16x16x32_bf16 v[8:11], v[152:155], v[228:231], v[8:11]
	v_mfma_f32_16x16x32_bf16 v[4:7], v[160:163], v[228:231], v[4:7]
	s_setprio 0
	s_barrier
	s_add_i32 s96, 0, 0x18000
	s_add_i32 s97, 0, 0x1c000
	v_add_u32_e32 v144, s96, v191
	v_add_u32_e32 v160, s97, v191
	ds_read_b128 v[132:135], v144
	ds_read_b128 v[136:139], v144 offset:1024
	ds_read_b128 v[140:143], v144 offset:2048
	ds_read_b128 v[144:147], v144 offset:3072
	ds_read_b128 v[148:151], v160
	ds_read_b128 v[152:155], v160 offset:1024
	ds_read_b128 v[156:159], v160 offset:2048
	ds_read_b128 v[160:163], v160 offset:3072
	s_add_u32 s90, s90, 0x40000
	s_addc_u32 s91, s91, 0
	s_mov_b32 m0, s17
	ds_read_b128 v[164:167], v195 offset:32768
	ds_read_b128 v[168:171], v195 offset:33792
	ds_read_b128 v[182:185], v195 offset:34816
	ds_read_b128 v[208:211], v195 offset:35840
	ds_read_b128 v[212:215], v195 offset:36864
	ds_read_b128 v[216:219], v195 offset:37888
	ds_read_b128 v[220:223], v195 offset:38912
	ds_read_b128 v[228:231], v195 offset:39936
	global_load_lds_dwordx4 v176, s[90:91]
	s_mov_b32 m0, s18
	s_nop 0
	global_load_lds_dwordx4 v174, s[90:91]
	s_waitcnt vmcnt(8)
	s_waitcnt lgkmcnt(0)
	s_barrier
	s_setprio 1
	s_waitcnt lgkmcnt(0)
	v_mfma_f32_16x16x32_bf16 v[128:131], v[132:135], v[164:167], v[128:131]
	v_mfma_f32_16x16x32_bf16 v[124:127], v[140:143], v[164:167], v[124:127]
	v_mfma_f32_16x16x32_bf16 v[112:115], v[132:135], v[182:185], v[112:115]
	v_mfma_f32_16x16x32_bf16 v[108:111], v[140:143], v[182:185], v[108:111]
	v_mfma_f32_16x16x32_bf16 v[96:99], v[132:135], v[212:215], v[96:99]
	v_mfma_f32_16x16x32_bf16 v[92:95], v[140:143], v[212:215], v[92:95]
	v_mfma_f32_16x16x32_bf16 v[80:83], v[132:135], v[220:223], v[80:83]
	v_mfma_f32_16x16x32_bf16 v[76:79], v[140:143], v[220:223], v[76:79]
	v_mfma_f32_16x16x32_bf16 v[128:131], v[136:139], v[168:171], v[128:131]
	v_mfma_f32_16x16x32_bf16 v[124:127], v[144:147], v[168:171], v[124:127]
	v_mfma_f32_16x16x32_bf16 v[112:115], v[136:139], v[208:211], v[112:115]
	v_mfma_f32_16x16x32_bf16 v[108:111], v[144:147], v[208:211], v[108:111]
	v_mfma_f32_16x16x32_bf16 v[96:99], v[136:139], v[216:219], v[96:99]
	v_mfma_f32_16x16x32_bf16 v[92:95], v[144:147], v[216:219], v[92:95]
	v_mfma_f32_16x16x32_bf16 v[80:83], v[136:139], v[228:231], v[80:83]
	v_mfma_f32_16x16x32_bf16 v[76:79], v[144:147], v[228:231], v[76:79]
	s_setprio 0
	s_setprio 1
	v_mfma_f32_16x16x32_bf16 v[120:123], v[148:151], v[164:167], v[120:123]
	v_mfma_f32_16x16x32_bf16 v[116:119], v[156:159], v[164:167], v[116:119]
	v_mfma_f32_16x16x32_bf16 v[104:107], v[148:151], v[182:185], v[104:107]
	v_mfma_f32_16x16x32_bf16 v[100:103], v[156:159], v[182:185], v[100:103]
	v_mfma_f32_16x16x32_bf16 v[88:91], v[148:151], v[212:215], v[88:91]
	v_mfma_f32_16x16x32_bf16 v[84:87], v[156:159], v[212:215], v[84:87]
	v_mfma_f32_16x16x32_bf16 v[72:75], v[148:151], v[220:223], v[72:75]
	v_mfma_f32_16x16x32_bf16 v[68:71], v[156:159], v[220:223], v[68:71]
	v_mfma_f32_16x16x32_bf16 v[120:123], v[152:155], v[168:171], v[120:123]
	v_mfma_f32_16x16x32_bf16 v[116:119], v[160:163], v[168:171], v[116:119]
	v_mfma_f32_16x16x32_bf16 v[104:107], v[152:155], v[208:211], v[104:107]
	v_mfma_f32_16x16x32_bf16 v[100:103], v[160:163], v[208:211], v[100:103]
	v_mfma_f32_16x16x32_bf16 v[88:91], v[152:155], v[216:219], v[88:91]
	v_mfma_f32_16x16x32_bf16 v[84:87], v[160:163], v[216:219], v[84:87]
	v_mfma_f32_16x16x32_bf16 v[72:75], v[152:155], v[228:231], v[72:75]
	v_mfma_f32_16x16x32_bf16 v[68:71], v[160:163], v[228:231], v[68:71]
	s_setprio 0
	s_barrier
; #define PG8_WAIT_V(n) asm volatile("s_waitcnt vmcnt(" #n ")" ::: "memory")
; #define PG8_WAIT_L(n) asm volatile("s_waitcnt lgkmcnt(" #n ")" ::: "memory")
; #define PG8_BAR __builtin_amdgcn_s_barrier()
; template <class Epi, class Sched, bool ALIGN_EPI = false, bool SP2 = false, bool FP8 = false, bool ABLK = false>
; __device__ __forceinline__ void gemm_phase(PG8_LAS unsigned char* lds, const Gemm g, const Sched& S, const Epi& E) {
;     ...
;             PG8_WAIT_V(8); PG8_WAIT_L(0); PG8_BAR; PG8_MMA(0, 0, At, B0); PG8_MMA(0, 1, At, B1); PG8_BAR; PG8_SCHED;
;             PG8_LDA(At, 1, 1); PG8_STAGE(PG8_SB(1, 0), b3, voffB); PG8_STAGE(PG8_SB(1, 1), b3 + hstep, voffB); PG8_STAGE(PG8_SA(1, 0), a3, voffA);
;             PG8_WAIT_V(8); PG8_WAIT_L(0); PG8_BAR; PG8_MMA(1, 0, At, B0); PG8_MMA(1, 1, At, B1); PG8_BAR; PG8_SCHED;
;             } else {
;             PG8_LDB(B0, 0, 0); PG8_SCHED; PG8_LDA(At, 0, 0); PG8_STAGE(PG8_SA(1, 1), a1 + hstepA, voffA);
;             PG8_WAIT_L(8); PG8_BAR; PG8_WAIT_L(0); PG8_MMA(0, 0, At, B0); PG8_BAR; PG8_SCHED;
;             PG8_LDB(B1, 0, 1); PG8_STAGE(PG8_SB(0, 0), b2, voffB);
;             PG8_BAR; PG8_WAIT_L(0); PG8_MMA(0, 1, At, B1); PG8_BAR;
;             PG8_LDA(At, 0, 1); PG8_STAGE(PG8_SA(0, 0), a2, voffA);
;             PG8_BAR; PG8_WAIT_L(0); PG8_MMA(1, 0, At, B0); PG8_BAR; PG8_SCHED;
;             PG8_STAGE(PG8_SB(0, 1), b2 + hstep, voffB);
;             PG8_WAIT_V(6); PG8_BAR; PG8_MMA(1, 1, At, B1); PG8_BAR;
;             PG8_LDB(B0, 1, 0); PG8_SCHED; PG8_LDA(At, 1, 0); PG8_STAGE(PG8_SA(0, 1), a2 + hstepA, voffA);
;             PG8_WAIT_L(8); PG8_BAR; PG8_WAIT_L(0); PG8_MMA(0, 0, At, B0); PG8_BAR; PG8_SCHED;
;             PG8_LDB(B1, 1, 1); PG8_STAGE(PG8_SB(1, 0), b3, voffB);
;             PG8_BAR; PG8_WAIT_L(0); PG8_MMA(0, 1, At, B1); PG8_BAR;
;             PG8_LDA(At, 1, 1); PG8_STAGE(PG8_SA(1, 0), a3, voffA);
;             PG8_BAR; PG8_WAIT_L(0); PG8_MMA(1, 0, At, B0); PG8_BAR; PG8_SCHED;
;             PG8_STAGE(PG8_SB(1, 1), b3 + hstep, voffB);
;             PG8_WAIT_V(6); PG8_BAR; PG8_MMA(1, 1, At, B1); PG8_BAR;
;             }
;         }
;         if constexpr (SP2) PG8_WAIT_V(0);
;         if constexpr (FP8) asm volatile("s_nop 15\n\ts_nop 15" ::: "memory");
;         if constexpr (ALIGN_EPI) { if (wr == 0) PG8_BAR; }
;         if constexpr (!Epi::AFTER_DRAIN) { E(acc, cur, wr, wc, fr, fq); S.done(cur); }
	s_add_i32 s90, s96, s7
	v_lshl_add_u64 v[188:189], v[188:189], 0, s[34:35]
	s_mov_b32 m0, s90
	ds_read_b128 v[164:167], v195 offset:49152
	ds_read_b128 v[168:171], v195 offset:50176
	ds_read_b128 v[182:185], v195 offset:51200
	ds_read_b128 v[208:211], v195 offset:52224
	ds_read_b128 v[212:215], v195 offset:53248
	ds_read_b128 v[216:219], v195 offset:54272
	ds_read_b128 v[220:223], v195 offset:55296
	ds_read_b128 v[228:231], v195 offset:56320
	global_load_lds_dwordx4 v[188:189], off
	s_add_i32 m0, s90, 0x2000
	s_add_u32 s44, s44, 0x40080
	v_lshl_add_u64 v[188:189], v[192:193], 0, s[34:35]
	s_addc_u32 s45, s45, 0
	s_add_i32 s90, s97, s7
	global_load_lds_dwordx4 v[188:189], off
	s_mov_b32 m0, s90
	s_nop 0
	global_load_lds_dwordx4 v2, s[44:45]
	s_add_i32 m0, s90, 0x2000
	s_nop 0
	global_load_lds_dwordx4 v172, s[44:45]
	v_lshl_add_u64 v[188:189], v[224:225], 0, s[34:35]
	s_mov_b32 m0, s19
	s_nop 0
	global_load_lds_dwordx4 v[188:189], off
	v_lshl_add_u64 v[188:189], v[232:233], 0, s[34:35]
	s_mov_b32 m0, s20
	s_nop 0
	global_load_lds_dwordx4 v[188:189], off
	s_waitcnt vmcnt(8)
	s_waitcnt lgkmcnt(0)
	s_barrier
	s_setprio 1
	s_waitcnt lgkmcnt(0)
	v_mfma_f32_16x16x32_bf16 v[64:67], v[132:135], v[164:167], v[64:67]
	v_mfma_f32_16x16x32_bf16 v[60:63], v[140:143], v[164:167], v[60:63]
	v_mfma_f32_16x16x32_bf16 v[48:51], v[132:135], v[182:185], v[48:51]
	v_mfma_f32_16x16x32_bf16 v[44:47], v[140:143], v[182:185], v[44:47]
	v_mfma_f32_16x16x32_bf16 v[32:35], v[132:135], v[212:215], v[32:35]
	v_mfma_f32_16x16x32_bf16 v[28:31], v[140:143], v[212:215], v[28:31]
	v_mfma_f32_16x16x32_bf16 v[16:19], v[132:135], v[220:223], v[16:19]
	v_mfma_f32_16x16x32_bf16 v[12:15], v[140:143], v[220:223], v[12:15]
	v_mfma_f32_16x16x32_bf16 v[64:67], v[136:139], v[168:171], v[64:67]
	v_mfma_f32_16x16x32_bf16 v[60:63], v[144:147], v[168:171], v[60:63]
	v_mfma_f32_16x16x32_bf16 v[48:51], v[136:139], v[208:211], v[48:51]
	v_mfma_f32_16x16x32_bf16 v[44:47], v[144:147], v[208:211], v[44:47]
	v_mfma_f32_16x16x32_bf16 v[32:35], v[136:139], v[216:219], v[32:35]
	v_mfma_f32_16x16x32_bf16 v[28:31], v[144:147], v[216:219], v[28:31]
	v_mfma_f32_16x16x32_bf16 v[16:19], v[136:139], v[228:231], v[16:19]
	v_mfma_f32_16x16x32_bf16 v[12:15], v[144:147], v[228:231], v[12:15]
	s_setprio 0
	s_setprio 1
	v_mfma_f32_16x16x32_bf16 v[56:59], v[148:151], v[164:167], v[56:59]
	v_mfma_f32_16x16x32_bf16 v[52:55], v[156:159], v[164:167], v[52:55]
	v_mfma_f32_16x16x32_bf16 v[40:43], v[148:151], v[182:185], v[40:43]
	v_mfma_f32_16x16x32_bf16 v[36:39], v[156:159], v[182:185], v[36:39]
	v_mfma_f32_16x16x32_bf16 v[24:27], v[148:151], v[212:215], v[24:27]
	v_mfma_f32_16x16x32_bf16 v[20:23], v[156:159], v[212:215], v[20:23]
	v_mfma_f32_16x16x32_bf16 v[8:11], v[148:151], v[220:223], v[8:11]
	v_mfma_f32_16x16x32_bf16 v[4:7], v[156:159], v[220:223], v[4:7]
	v_mfma_f32_16x16x32_bf16 v[56:59], v[152:155], v[168:171], v[56:59]
	v_mfma_f32_16x16x32_bf16 v[52:55], v[160:163], v[168:171], v[52:55]
	v_mfma_f32_16x16x32_bf16 v[40:43], v[152:155], v[208:211], v[40:43]
	v_mfma_f32_16x16x32_bf16 v[36:39], v[160:163], v[208:211], v[36:39]
	v_mfma_f32_16x16x32_bf16 v[24:27], v[152:155], v[216:219], v[24:27]
	v_mfma_f32_16x16x32_bf16 v[20:23], v[160:163], v[216:219], v[20:23]
	v_mfma_f32_16x16x32_bf16 v[8:11], v[152:155], v[228:231], v[8:11]
	v_mfma_f32_16x16x32_bf16 v[4:7], v[160:163], v[228:231], v[4:7]
	s_setprio 0
	s_barrier
	s_add_u32 s42, s42, 0x100
	s_addc_u32 s43, s43, 0
	s_add_u32 s92, s92, 0x100
	s_addc_u32 s94, s94, 0
	s_cmp_gt_u32 s95, 13
	s_mov_b32 s44, s95
	s_cbranch_scc0 .LBB0_600
	s_waitcnt vmcnt(0)
	s_and_b64 vcc, exec, s[64:65]
	s_cbranch_vccnz .LBB0_604
	s_cmpk_lt_i32 s73, 0xf4
	s_mov_b64 s[4:5], -1
	s_cbranch_scc1 .LBB0_605

; #define PG8_STAGE(bufoff, gbase, voff) do { _Pragma("unroll") for (int _i = 0; _i < 2; ++_i) \
;         __builtin_amdgcn_global_load_lds((const unsigned*)((const char*)(gbase) + (voff)[_i]), (PG8_LAS unsigned*)(lds + (bufoff) + ldsw + _i * 8192), 16, 0, 0); } while (0)
; #define PG8_WAIT_V(n) asm volatile("s_waitcnt vmcnt(" #n ")" ::: "memory")
; #define PG8_BAR __builtin_amdgcn_s_barrier()
;   __device__ __forceinline__ bool next(int i,AttnUnit&u)const{ const int v=vcu+(i>>2)*grid; if(v>=256)return false; const int k=i&3,s=v&7; u.bh=v>>3; u.qb=(k==0)?s:(k==1)?15-s:(k==2)?16+s:31-s; return true; }
; template <class Epi, class Sched, bool ALIGN_EPI = false, bool SP2 = false, bool FP8 = false, bool ABLK = false>
; __device__ __forceinline__ void gemm_phase(PG8_LAS unsigned char* lds, const Gemm g, const Sched& S, const Epi& E) {
;     ...
;     const char* cA = (const char*)g.A + (size_t)cur.pm * tstep; const char* cB = (const char*)g.Bt + (size_t)cur.pn * tstep;
;     S.a_ready(cur);
;     if constexpr (SP2) {
;         PG8_STAGE(PG8_SB(0, 0), cB, voffB); PG8_STAGE(PG8_SB(0, 1), cB + hstep, voffB); PG8_STAGE(PG8_SA(0, 0), cA, voffA); PG8_STAGE(PG8_SA(0, 1), cA + hstepA, voffA);
;         if (wr == 1) PG8_BAR;
;         PG8_WAIT_V(2); PG8_BAR;
;         PG8_STAGE(PG8_SB(1, 0), cB + kstep, voffB); PG8_STAGE(PG8_SA(1, 0), cA + kstepA, voffA); PG8_STAGE(PG8_SB(1, 1), cB + hstep + kstep, voffB);
;         PG8_WAIT_V(0); PG8_BAR;
;     } else {
;         PG8_STAGE(PG8_SB(0, 0), cB, voffB); PG8_STAGE(PG8_SA(0, 0), cA, voffA); PG8_STAGE(PG8_SB(0, 1), cB + hstep, voffB); PG8_STAGE(PG8_SA(0, 1), cA + hstepA, voffA);
;         if (wr == 1) PG8_BAR;
;         PG8_WAIT_V(4); PG8_BAR;
;         PG8_STAGE(PG8_SB(1, 0), cB + kstep, voffB); PG8_STAGE(PG8_SA(1, 0), cA + kstepA, voffA); PG8_STAGE(PG8_SB(1, 1), cB + hstep + kstep, voffB);
;         PG8_WAIT_V(6); PG8_BAR;
;     }
;     for (;;) {
;         const bool has_next = S.next(ui + 1, nxt);
;         const char* nA = has_next ? (const char*)g.A + (size_t)nxt.pm * tstep : cA; const char* nB = has_next ? (const char*)g.Bt + (size_t)nxt.pn * tstep : cB;
.LBB0_1401:
	s_add_u32 s44, s40, 0x7a00000
	s_addc_u32 s45, s41, 0
	s_add_u32 s46, s40, 0x1c000000
	s_addc_u32 s47, s41, 0
	v_bfe_u32 v194, v17, 4, 2
	s_add_u32 s48, s40, 0x11a00000
	v_and_b32_e32 v1, 15, v17
	v_lshlrev_b32_e32 v19, 4, v194
	v_lshlrev_b32_e32 v17, 2, v17
	s_addc_u32 s49, s41, 0
	s_and_b32 s22, s5, 3
	s_lshl_b32 s23, s4, 6
	v_lshl_or_b32 v19, v1, 6, v19
	s_lshl_b32 s4, s4, 13
	v_and_b32_e32 v17, 32, v17
	s_add_i32 m0, s18, 0x18000
	v_lshl_add_u64 v[10:11], v[10:11], 0, s[34:35]
	v_bitop3_b32 v20, v19, s4, v17 bitop3:0xde
	s_lshl_b32 s64, s22, 5
	s_lshl_b32 s4, s22, 12
	s_waitcnt vmcnt(2)
	s_barrier
	global_load_lds_dwordx4 v[10:11], off
	v_lshl_add_u64 v[8:9], v[8:9], 0, s[34:35]
	s_add_i32 m0, s18, 0x1a000
	s_add_i32 s65, s18, 0x8000
	s_add_i32 s66, s18, 0xa000
	v_bitop3_b32 v195, v19, s4, v17 bitop3:0xde
	global_load_lds_dwordx4 v[8:9], off
	v_lshl_add_u64 v[4:5], v[4:5], 0, s[34:35]
	s_mov_b32 m0, s65
	s_add_u32 s4, s60, 0x40080
	global_load_lds_dwordx4 v[4:5], off
	v_lshl_add_u64 v[4:5], v[6:7], 0, s[34:35]
	s_mov_b32 m0, s66
	s_addc_u32 s5, s61, 0
	global_load_lds_dwordx4 v[4:5], off
	s_add_i32 m0, s18, 0x1c000
	s_nop 0
	global_load_lds_dwordx4 v2, s[4:5]
	s_add_i32 m0, s18, 0x1e000
	s_cmpk_lt_u32 s50, 0x100
	global_load_lds_dwordx4 v160, s[4:5]
	v_lshlrev_b32_e32 v4, 14, v16
	v_and_b32_e32 v4, 0xffff8000, v4
	v_lshl_add_u32 v4, v15, 11, v4
	v_and_b32_e32 v5, 1, v16
	v_lshl_or_b32 v4, v5, 6, v4
	v_lshl_add_u32 v166, v18, 1, v4
	v_lshlrev_b32_e32 v4, 14, v12
	v_and_b32_e32 v4, 0xffff8000, v4
	s_waitcnt vmcnt(0)
	v_lshl_add_u32 v4, v13, 11, v4
	v_and_b32_e32 v5, 1, v12
	v_lshl_or_b32 v4, v5, 6, v4
	v_readlane_b32 s4, v252, 8
	s_cselect_b64 s[50:51], -1, 0
	v_mov_b32_e32 v167, v3
	v_lshl_add_u32 v168, v14, 1, v4
	v_mov_b32_e32 v169, v3
	s_mov_b32 s67, 0
	v_add_u32_e32 v208, 0, v20
	v_readlane_b32 s68, v254, 58
	s_mov_b32 s69, s4
	s_barrier
	v_readlane_b32 s5, v252, 9
	s_branch .LBB0_1404

; #define PG8_STAGE(bufoff, gbase, voff) do { _Pragma("unroll") for (int _i = 0; _i < 2; ++_i) \
;         __builtin_amdgcn_global_load_lds((const unsigned*)((const char*)(gbase) + (voff)[_i]), (PG8_LAS unsigned*)(lds + (bufoff) + ldsw + _i * 8192), 16, 0, 0); } while (0)
; #define PG8_LDA(dst, b, h) do { _Pragma("unroll") for (int m = 0; m < 4; ++m) _Pragma("unroll") for (int k = 0; k < 2; ++k) dst[m][k] = *(const PG8_LAS bf16x8*)(lds + PG8_SA(b, h) + aoff + m * 2048 + k * 1024); } while (0)
; #define PG8_LDB(dst, b, h) do { _Pragma("unroll") for (int n = 0; n < 2; ++n) _Pragma("unroll") for (int k = 0; k < 2; ++k) dst[n][k] = *(const PG8_LAS bf16x8*)(lds + PG8_SB(b, h) + boff + n * 2048 + k * 1024); } while (0)
; #define PG8_WAIT_V8_UNLESS_FIRST(t) asm volatile("s_cmp_eq_u32 %0, 0\n\ts_cbranch_scc1 .Lpg8skip%=\n\ts_waitcnt vmcnt(8)\n.Lpg8skip%=:" :: "s"(t) : "scc", "memory")
; #define PG8_WAIT_L(n) asm volatile("s_waitcnt lgkmcnt(" #n ")" ::: "memory")
; #define PG8_BAR __builtin_amdgcn_s_barrier()
; #define PG8_SCHED __builtin_amdgcn_sched_barrier(0)
; template <class Epi, class Sched, bool ALIGN_EPI = false, bool SP2 = false, bool FP8 = false, bool ABLK = false>
; __device__ __forceinline__ void gemm_phase(PG8_LAS unsigned char* lds, const Gemm g, const Sched& S, const Epi& E) {
;     ...
;         for (int t = 0; t < nt; t += 2) {
;             const bool last = (t == nt - 2);
;             const char* a1 = cA + (size_t)(t + 1) * kstepA;
;             const char* a2 = last ? nA : cA + (size_t)(t + 2) * kstepA; const char* b2 = last ? nB : cB + (size_t)(t + 2) * kstep;
;             const char* a3 = a2 + kstepA; const char* b3 = b2 + kstep;
;             if (last && has_next) S.a_ready(nxt);
;             if constexpr (SP2) {
;             PG8_LDB(B0, 0, 0); PG8_LDB(B1, 0, 1); PG8_SCHED; PG8_LDA(At, 0, 0); PG8_STAGE(PG8_SA(1, 1), a1 + hstepA, voffA);
;             PG8_WAIT_V8_UNLESS_FIRST(t); PG8_WAIT_L(0); PG8_BAR; PG8_MMA(0, 0, At, B0); PG8_MMA(0, 1, At, B1); PG8_BAR; PG8_SCHED;
;             PG8_LDA(At, 0, 1); PG8_STAGE(PG8_SB(0, 0), b2, voffB); PG8_STAGE(PG8_SB(0, 1), b2 + hstep, voffB); PG8_STAGE(PG8_SA(0, 0), a2, voffA);
;             PG8_WAIT_V8_UNLESS_FIRST(t); PG8_WAIT_L(0); PG8_BAR; PG8_MMA(1, 0, At, B0); PG8_MMA(1, 1, At, B1); PG8_BAR; PG8_SCHED;
.LBB0_1411:
	s_add_i32 s72, s60, 2
	s_add_u32 s61, s42, 0xfffc0080
	s_addc_u32 s62, s43, -1
	s_add_i32 s73, 0, 0x10000
	s_cmp_eq_u32 s60, 12
	s_cselect_b32 s63, s4, s62
	s_cselect_b32 s62, s5, s61
	s_cselect_b32 s61, s53, s71
	s_cselect_b32 s60, s55, s70
	s_add_i32 s76, 0, 0x14000
	v_add_u32_e32 v136, s73, v195
	v_add_u32_e32 v170, s76, v195
	ds_read_b128 v[124:127], v136
	ds_read_b128 v[128:131], v136 offset:1024
	ds_read_b128 v[132:135], v136 offset:2048
	ds_read_b128 v[136:139], v136 offset:3072
	ds_read_b128 v[140:143], v170
	ds_read_b128 v[144:147], v170 offset:1024
	ds_read_b128 v[156:159], v170 offset:2048
	ds_read_b128 v[170:173], v170 offset:3072
	s_add_i32 m0, s18, 0xc000
	ds_read_b128 v[174:177], v208
	ds_read_b128 v[178:181], v208 offset:1024
	ds_read_b128 v[182:185], v208 offset:2048
	ds_read_b128 v[186:189], v208 offset:3072
	ds_read_b128 v[190:193], v208 offset:4096
	ds_read_b128 v[210:213], v208 offset:5120
	ds_read_b128 v[214:217], v208 offset:6144
	ds_read_b128 v[218:221], v208 offset:7168
	global_load_lds_dwordx4 v166, s[42:43]
	s_add_i32 m0, s18, 0xe000
	s_nop 0
	global_load_lds_dwordx4 v168, s[42:43]
	s_cmp_eq_u32 s72, 0
	s_cbranch_scc1 .Lpg8skip6
	s_waitcnt vmcnt(8)
.Lpg8skip6:
	s_waitcnt lgkmcnt(0)
	s_barrier
	s_setprio 1
	s_waitcnt lgkmcnt(0)
	v_mfma_f32_16x16x32_bf16 v[152:155], v[124:127], v[174:177], v[152:155]
	v_mfma_f32_16x16x32_bf16 v[148:151], v[132:135], v[174:177], v[148:151]
	v_mfma_f32_16x16x32_bf16 v[112:115], v[124:127], v[182:185], v[112:115]
	v_mfma_f32_16x16x32_bf16 v[108:111], v[132:135], v[182:185], v[108:111]
	v_mfma_f32_16x16x32_bf16 v[96:99], v[124:127], v[190:193], v[96:99]
	v_mfma_f32_16x16x32_bf16 v[92:95], v[132:135], v[190:193], v[92:95]
	v_mfma_f32_16x16x32_bf16 v[80:83], v[124:127], v[214:217], v[80:83]
	v_mfma_f32_16x16x32_bf16 v[76:79], v[132:135], v[214:217], v[76:79]
	v_mfma_f32_16x16x32_bf16 v[152:155], v[128:131], v[178:181], v[152:155]
	v_mfma_f32_16x16x32_bf16 v[148:151], v[136:139], v[178:181], v[148:151]
	v_mfma_f32_16x16x32_bf16 v[112:115], v[128:131], v[186:189], v[112:115]
	v_mfma_f32_16x16x32_bf16 v[108:111], v[136:139], v[186:189], v[108:111]
	v_mfma_f32_16x16x32_bf16 v[96:99], v[128:131], v[210:213], v[96:99]
	v_mfma_f32_16x16x32_bf16 v[92:95], v[136:139], v[210:213], v[92:95]
	v_mfma_f32_16x16x32_bf16 v[80:83], v[128:131], v[218:221], v[80:83]
	v_mfma_f32_16x16x32_bf16 v[76:79], v[136:139], v[218:221], v[76:79]
	s_setprio 0
	s_setprio 1
	v_mfma_f32_16x16x32_bf16 v[120:123], v[140:143], v[174:177], v[120:123]
	v_mfma_f32_16x16x32_bf16 v[116:119], v[156:159], v[174:177], v[116:119]
	v_mfma_f32_16x16x32_bf16 v[104:107], v[140:143], v[182:185], v[104:107]
	v_mfma_f32_16x16x32_bf16 v[100:103], v[156:159], v[182:185], v[100:103]
	v_mfma_f32_16x16x32_bf16 v[88:91], v[140:143], v[190:193], v[88:91]
	v_mfma_f32_16x16x32_bf16 v[84:87], v[156:159], v[190:193], v[84:87]
	v_mfma_f32_16x16x32_bf16 v[72:75], v[140:143], v[214:217], v[72:75]
	v_mfma_f32_16x16x32_bf16 v[68:71], v[156:159], v[214:217], v[68:71]
	v_mfma_f32_16x16x32_bf16 v[120:123], v[144:147], v[178:181], v[120:123]
	v_mfma_f32_16x16x32_bf16 v[116:119], v[170:173], v[178:181], v[116:119]
	v_mfma_f32_16x16x32_bf16 v[104:107], v[144:147], v[186:189], v[104:107]
	v_mfma_f32_16x16x32_bf16 v[100:103], v[170:173], v[186:189], v[100:103]
	v_mfma_f32_16x16x32_bf16 v[88:91], v[144:147], v[210:213], v[88:91]
	v_mfma_f32_16x16x32_bf16 v[84:87], v[170:173], v[210:213], v[84:87]
	v_mfma_f32_16x16x32_bf16 v[72:75], v[144:147], v[218:221], v[72:75]
	v_mfma_f32_16x16x32_bf16 v[68:71], v[170:173], v[218:221], v[68:71]
	s_setprio 0
	s_barrier
	s_add_i32 s73, s73, s17
	v_lshl_add_u64 v[204:205], s[60:61], 0, v[2:3]
	s_mov_b32 m0, s73
	ds_read_b128 v[174:177], v208 offset:16384
	ds_read_b128 v[178:181], v208 offset:17408
	ds_read_b128 v[182:185], v208 offset:18432
	ds_read_b128 v[186:189], v208 offset:19456
	ds_read_b128 v[190:193], v208 offset:20480
	ds_read_b128 v[210:213], v208 offset:21504
	ds_read_b128 v[214:217], v208 offset:22528
	ds_read_b128 v[218:221], v208 offset:23552
	global_load_lds_dwordx4 v2, s[60:61]
	s_add_i32 m0, s73, 0x2000
	s_add_u32 s74, s60, 0x40000
	v_lshl_add_u64 v[206:207], s[60:61], 0, v[160:161]
	s_addc_u32 s75, s61, 0
	s_add_i32 s73, s76, s17
	global_load_lds_dwordx4 v160, s[60:61]
	s_mov_b32 m0, s73
	v_lshl_add_u64 v[224:225], s[62:63], 0, v[162:163]
	global_load_lds_dwordx4 v2, s[74:75]
	s_add_i32 m0, s73, 0x2000
	s_nop 0
	global_load_lds_dwordx4 v160, s[74:75]
	v_lshl_add_u64 v[222:223], s[62:63], 0, v[164:165]
	s_mov_b32 m0, s18
	s_nop 0
	global_load_lds_dwordx4 v164, s[62:63]
	s_mov_b32 m0, s19
	s_nop 0
	global_load_lds_dwordx4 v162, s[62:63]
	s_cmp_eq_u32 s72, 0
	s_cbranch_scc1 .Lpg8skip7
	s_waitcnt vmcnt(8)
; #define PG8_STAGE(bufoff, gbase, voff) do { _Pragma("unroll") for (int _i = 0; _i < 2; ++_i) \
;         __builtin_amdgcn_global_load_lds((const unsigned*)((const char*)(gbase) + (voff)[_i]), (PG8_LAS unsigned*)(lds + (bufoff) + ldsw + _i * 8192), 16, 0, 0); } while (0)
; #define PG8_LDA(dst, b, h) do { _Pragma("unroll") for (int m = 0; m < 4; ++m) _Pragma("unroll") for (int k = 0; k < 2; ++k) dst[m][k] = *(const PG8_LAS bf16x8*)(lds + PG8_SA(b, h) + aoff + m * 2048 + k * 1024); } while (0)
; #define PG8_LDB(dst, b, h) do { _Pragma("unroll") for (int n = 0; n < 2; ++n) _Pragma("unroll") for (int k = 0; k < 2; ++k) dst[n][k] = *(const PG8_LAS bf16x8*)(lds + PG8_SB(b, h) + boff + n * 2048 + k * 1024); } while (0)
; #define PG8_WAIT_V(n) asm volatile("s_waitcnt vmcnt(" #n ")" ::: "memory")
; #define PG8_WAIT_V8_UNLESS_FIRST(t) asm volatile("s_cmp_eq_u32 %0, 0\n\ts_cbranch_scc1 .Lpg8skip%=\n\ts_waitcnt vmcnt(8)\n.Lpg8skip%=:" :: "s"(t) : "scc", "memory")
; #define PG8_WAIT_L(n) asm volatile("s_waitcnt lgkmcnt(" #n ")" ::: "memory")
; #define PG8_BAR __builtin_amdgcn_s_barrier()
; #define PG8_SCHED __builtin_amdgcn_sched_barrier(0)
; template <class Epi, class Sched, bool ALIGN_EPI = false, bool SP2 = false, bool FP8 = false, bool ABLK = false>
; __device__ __forceinline__ void gemm_phase(PG8_LAS unsigned char* lds, const Gemm g, const Sched& S, const Epi& E) {
;     ...
;             PG8_WAIT_V8_UNLESS_FIRST(t); PG8_WAIT_L(0); PG8_BAR; PG8_MMA(0, 0, At, B0); PG8_MMA(0, 1, At, B1); PG8_BAR; PG8_SCHED;
;             PG8_LDA(At, 0, 1); PG8_STAGE(PG8_SB(0, 0), b2, voffB); PG8_STAGE(PG8_SB(0, 1), b2 + hstep, voffB); PG8_STAGE(PG8_SA(0, 0), a2, voffA);
;             PG8_WAIT_V8_UNLESS_FIRST(t); PG8_WAIT_L(0); PG8_BAR; PG8_MMA(1, 0, At, B0); PG8_MMA(1, 1, At, B1); PG8_BAR; PG8_SCHED;
;             PG8_LDB(B0, 1, 0); PG8_LDB(B1, 1, 1); PG8_SCHED; PG8_LDA(At, 1, 0); PG8_STAGE(PG8_SA(0, 1), a2 + hstepA, voffA);
;             PG8_WAIT_V(8); PG8_WAIT_L(0); PG8_BAR; PG8_MMA(0, 0, At, B0); PG8_MMA(0, 1, At, B1); PG8_BAR; PG8_SCHED;
;             PG8_LDA(At, 1, 1); PG8_STAGE(PG8_SB(1, 0), b3, voffB); PG8_STAGE(PG8_SB(1, 1), b3 + hstep, voffB); PG8_STAGE(PG8_SA(1, 0), a3, voffA);
;             PG8_WAIT_V(8); PG8_WAIT_L(0); PG8_BAR; PG8_MMA(1, 0, At, B0); PG8_MMA(1, 1, At, B1); PG8_BAR; PG8_SCHED;
.Lpg8skip7:
	s_waitcnt lgkmcnt(0)
	s_barrier
	s_setprio 1
	s_waitcnt lgkmcnt(0)
	v_mfma_f32_16x16x32_bf16 v[64:67], v[124:127], v[174:177], v[64:67]
	v_mfma_f32_16x16x32_bf16 v[60:63], v[132:135], v[174:177], v[60:63]
	v_mfma_f32_16x16x32_bf16 v[48:51], v[124:127], v[182:185], v[48:51]
	v_mfma_f32_16x16x32_bf16 v[44:47], v[132:135], v[182:185], v[44:47]
	v_mfma_f32_16x16x32_bf16 v[32:35], v[124:127], v[190:193], v[32:35]
	v_mfma_f32_16x16x32_bf16 v[28:31], v[132:135], v[190:193], v[28:31]
	v_mfma_f32_16x16x32_bf16 v[16:19], v[124:127], v[214:217], v[16:19]
	v_mfma_f32_16x16x32_bf16 v[12:15], v[132:135], v[214:217], v[12:15]
	v_mfma_f32_16x16x32_bf16 v[64:67], v[128:131], v[178:181], v[64:67]
	v_mfma_f32_16x16x32_bf16 v[60:63], v[136:139], v[178:181], v[60:63]
	v_mfma_f32_16x16x32_bf16 v[48:51], v[128:131], v[186:189], v[48:51]
	v_mfma_f32_16x16x32_bf16 v[44:47], v[136:139], v[186:189], v[44:47]
	v_mfma_f32_16x16x32_bf16 v[32:35], v[128:131], v[210:213], v[32:35]
	v_mfma_f32_16x16x32_bf16 v[28:31], v[136:139], v[210:213], v[28:31]
	v_mfma_f32_16x16x32_bf16 v[16:19], v[128:131], v[218:221], v[16:19]
	v_mfma_f32_16x16x32_bf16 v[12:15], v[136:139], v[218:221], v[12:15]
	s_setprio 0
	s_setprio 1
	v_mfma_f32_16x16x32_bf16 v[56:59], v[140:143], v[174:177], v[56:59]
	v_mfma_f32_16x16x32_bf16 v[52:55], v[156:159], v[174:177], v[52:55]
	v_mfma_f32_16x16x32_bf16 v[40:43], v[140:143], v[182:185], v[40:43]
	v_mfma_f32_16x16x32_bf16 v[36:39], v[156:159], v[182:185], v[36:39]
	v_mfma_f32_16x16x32_bf16 v[24:27], v[140:143], v[190:193], v[24:27]
	v_mfma_f32_16x16x32_bf16 v[20:23], v[156:159], v[190:193], v[20:23]
	v_mfma_f32_16x16x32_bf16 v[8:11], v[140:143], v[214:217], v[8:11]
	v_mfma_f32_16x16x32_bf16 v[4:7], v[156:159], v[214:217], v[4:7]
	v_mfma_f32_16x16x32_bf16 v[56:59], v[144:147], v[178:181], v[56:59]
	v_mfma_f32_16x16x32_bf16 v[52:55], v[170:173], v[178:181], v[52:55]
	v_mfma_f32_16x16x32_bf16 v[40:43], v[144:147], v[186:189], v[40:43]
	v_mfma_f32_16x16x32_bf16 v[36:39], v[170:173], v[186:189], v[36:39]
	v_mfma_f32_16x16x32_bf16 v[24:27], v[144:147], v[210:213], v[24:27]
	v_mfma_f32_16x16x32_bf16 v[20:23], v[170:173], v[210:213], v[20:23]
	v_mfma_f32_16x16x32_bf16 v[8:11], v[144:147], v[218:221], v[8:11]
	v_mfma_f32_16x16x32_bf16 v[4:7], v[170:173], v[218:221], v[4:7]
	s_setprio 0
	s_barrier
	s_add_i32 s73, 0, 0x18000
	s_add_i32 s74, 0, 0x1c000
	v_add_u32_e32 v136, s73, v195
	v_add_u32_e32 v170, s74, v195
	ds_read_b128 v[124:127], v136
	ds_read_b128 v[128:131], v136 offset:1024
	ds_read_b128 v[132:135], v136 offset:2048
	ds_read_b128 v[136:139], v136 offset:3072
	ds_read_b128 v[140:143], v170
	ds_read_b128 v[144:147], v170 offset:1024
	ds_read_b128 v[156:159], v170 offset:2048
	ds_read_b128 v[170:173], v170 offset:3072
	s_add_u32 s62, s62, 0x40000
	s_addc_u32 s63, s63, 0
	s_mov_b32 m0, s20
	ds_read_b128 v[174:177], v208 offset:32768
	ds_read_b128 v[178:181], v208 offset:33792
	ds_read_b128 v[182:185], v208 offset:34816
	ds_read_b128 v[186:189], v208 offset:35840
	ds_read_b128 v[190:193], v208 offset:36864
	ds_read_b128 v[210:213], v208 offset:37888
	ds_read_b128 v[214:217], v208 offset:38912
	ds_read_b128 v[218:221], v208 offset:39936
	global_load_lds_dwordx4 v164, s[62:63]
	s_mov_b32 m0, s21
	s_nop 0
	global_load_lds_dwordx4 v162, s[62:63]
	s_waitcnt vmcnt(8)
	s_waitcnt lgkmcnt(0)
	s_barrier
	s_setprio 1
	s_waitcnt lgkmcnt(0)
	v_mfma_f32_16x16x32_bf16 v[152:155], v[124:127], v[174:177], v[152:155]
	v_mfma_f32_16x16x32_bf16 v[148:151], v[132:135], v[174:177], v[148:151]
	v_mfma_f32_16x16x32_bf16 v[112:115], v[124:127], v[182:185], v[112:115]
	v_mfma_f32_16x16x32_bf16 v[108:111], v[132:135], v[182:185], v[108:111]
	v_mfma_f32_16x16x32_bf16 v[96:99], v[124:127], v[190:193], v[96:99]
	v_mfma_f32_16x16x32_bf16 v[92:95], v[132:135], v[190:193], v[92:95]
	v_mfma_f32_16x16x32_bf16 v[80:83], v[124:127], v[214:217], v[80:83]
	v_mfma_f32_16x16x32_bf16 v[76:79], v[132:135], v[214:217], v[76:79]
	v_mfma_f32_16x16x32_bf16 v[152:155], v[128:131], v[178:181], v[152:155]
	v_mfma_f32_16x16x32_bf16 v[148:151], v[136:139], v[178:181], v[148:151]
	v_mfma_f32_16x16x32_bf16 v[112:115], v[128:131], v[186:189], v[112:115]
	v_mfma_f32_16x16x32_bf16 v[108:111], v[136:139], v[186:189], v[108:111]
	v_mfma_f32_16x16x32_bf16 v[96:99], v[128:131], v[210:213], v[96:99]
	v_mfma_f32_16x16x32_bf16 v[92:95], v[136:139], v[210:213], v[92:95]
	v_mfma_f32_16x16x32_bf16 v[80:83], v[128:131], v[218:221], v[80:83]
	v_mfma_f32_16x16x32_bf16 v[76:79], v[136:139], v[218:221], v[76:79]
	s_setprio 0
	s_setprio 1
	v_mfma_f32_16x16x32_bf16 v[120:123], v[140:143], v[174:177], v[120:123]
	v_mfma_f32_16x16x32_bf16 v[116:119], v[156:159], v[174:177], v[116:119]
	v_mfma_f32_16x16x32_bf16 v[104:107], v[140:143], v[182:185], v[104:107]
	v_mfma_f32_16x16x32_bf16 v[100:103], v[156:159], v[182:185], v[100:103]
	v_mfma_f32_16x16x32_bf16 v[88:91], v[140:143], v[190:193], v[88:91]
	v_mfma_f32_16x16x32_bf16 v[84:87], v[156:159], v[190:193], v[84:87]
	v_mfma_f32_16x16x32_bf16 v[72:75], v[140:143], v[214:217], v[72:75]
	v_mfma_f32_16x16x32_bf16 v[68:71], v[156:159], v[214:217], v[68:71]
	v_mfma_f32_16x16x32_bf16 v[120:123], v[144:147], v[178:181], v[120:123]
	v_mfma_f32_16x16x32_bf16 v[116:119], v[170:173], v[178:181], v[116:119]
	v_mfma_f32_16x16x32_bf16 v[104:107], v[144:147], v[186:189], v[104:107]
	v_mfma_f32_16x16x32_bf16 v[100:103], v[170:173], v[186:189], v[100:103]
	v_mfma_f32_16x16x32_bf16 v[88:91], v[144:147], v[210:213], v[88:91]
	v_mfma_f32_16x16x32_bf16 v[84:87], v[170:173], v[210:213], v[84:87]
	v_mfma_f32_16x16x32_bf16 v[72:75], v[144:147], v[218:221], v[72:75]
	v_mfma_f32_16x16x32_bf16 v[68:71], v[170:173], v[218:221], v[68:71]
	s_setprio 0
	s_barrier
; #define PG8_STAGE(bufoff, gbase, voff) do { _Pragma("unroll") for (int _i = 0; _i < 2; ++_i) \
;         __builtin_amdgcn_global_load_lds((const unsigned*)((const char*)(gbase) + (voff)[_i]), (PG8_LAS unsigned*)(lds + (bufoff) + ldsw + _i * 8192), 16, 0, 0); } while (0)
; template <class Epi, class Sched, bool ALIGN_EPI = false, bool SP2 = false, bool FP8 = false, bool ABLK = false>
; __device__ __forceinline__ void gemm_phase(PG8_LAS unsigned char* lds, const Gemm g, const Sched& S, const Epi& E) {
;     ...
;             PG8_WAIT_V(8); PG8_WAIT_L(0); PG8_BAR; PG8_MMA(0, 0, At, B0); PG8_MMA(0, 1, At, B1); PG8_BAR; PG8_SCHED;
;             PG8_LDA(At, 1, 1); PG8_STAGE(PG8_SB(1, 0), b3, voffB); PG8_STAGE(PG8_SB(1, 1), b3 + hstep, voffB); PG8_STAGE(PG8_SA(1, 0), a3, voffA);
;             PG8_WAIT_V(8); PG8_WAIT_L(0); PG8_BAR; PG8_MMA(1, 0, At, B0); PG8_MMA(1, 1, At, B1); PG8_BAR; PG8_SCHED;
;             } else {
;             PG8_LDB(B0, 0, 0); PG8_SCHED; PG8_LDA(At, 0, 0); PG8_STAGE(PG8_SA(1, 1), a1 + hstepA, voffA);
;             PG8_WAIT_L(8); PG8_BAR; PG8_WAIT_L(0); PG8_MMA(0, 0, At, B0); PG8_BAR; PG8_SCHED;
;             PG8_LDB(B1, 0, 1); PG8_STAGE(PG8_SB(0, 0), b2, voffB);
;             PG8_BAR; PG8_WAIT_L(0); PG8_MMA(0, 1, At, B1); PG8_BAR;
;             PG8_LDA(At, 0, 1); PG8_STAGE(PG8_SA(0, 0), a2, voffA);
;             PG8_BAR; PG8_WAIT_L(0); PG8_MMA(1, 0, At, B0); PG8_BAR; PG8_SCHED;
;             PG8_STAGE(PG8_SB(0, 1), b2 + hstep, voffB);
;             PG8_WAIT_V(6); PG8_BAR; PG8_MMA(1, 1, At, B1); PG8_BAR;
;             PG8_LDB(B0, 1, 0); PG8_SCHED; PG8_LDA(At, 1, 0); PG8_STAGE(PG8_SA(0, 1), a2 + hstepA, voffA);
;             PG8_WAIT_L(8); PG8_BAR; PG8_WAIT_L(0); PG8_MMA(0, 0, At, B0); PG8_BAR; PG8_SCHED;
;             PG8_LDB(B1, 1, 1); PG8_STAGE(PG8_SB(1, 0), b3, voffB);
;             PG8_BAR; PG8_WAIT_L(0); PG8_MMA(0, 1, At, B1); PG8_BAR;
;             PG8_LDA(At, 1, 1); PG8_STAGE(PG8_SA(1, 0), a3, voffA);
;             PG8_BAR; PG8_WAIT_L(0); PG8_MMA(1, 0, At, B0); PG8_BAR; PG8_SCHED;
;             PG8_STAGE(PG8_SB(1, 1), b3 + hstep, voffB);
;             PG8_WAIT_V(6); PG8_BAR; PG8_MMA(1, 1, At, B1); PG8_BAR;
;             }
;         }
;         if constexpr (SP2) PG8_WAIT_V(0);
;         if constexpr (FP8) asm volatile("s_nop 15\n\ts_nop 15" ::: "memory");
;         if constexpr (ALIGN_EPI) { if (wr == 0) PG8_BAR; }
	s_add_i32 s62, s73, s17
	v_lshl_add_u64 v[204:205], v[204:205], 0, s[34:35]
	s_mov_b32 m0, s62
	ds_read_b128 v[174:177], v208 offset:49152
	ds_read_b128 v[178:181], v208 offset:50176
	ds_read_b128 v[182:185], v208 offset:51200
	ds_read_b128 v[186:189], v208 offset:52224
	ds_read_b128 v[190:193], v208 offset:53248
	ds_read_b128 v[210:213], v208 offset:54272
	ds_read_b128 v[214:217], v208 offset:55296
	ds_read_b128 v[218:221], v208 offset:56320
	global_load_lds_dwordx4 v[204:205], off
	s_add_i32 m0, s62, 0x2000
	s_add_u32 s60, s60, 0x40080
	v_lshl_add_u64 v[204:205], v[206:207], 0, s[34:35]
	s_addc_u32 s61, s61, 0
	s_add_i32 s62, s74, s17
	global_load_lds_dwordx4 v[204:205], off
	s_mov_b32 m0, s62
	s_nop 0
	global_load_lds_dwordx4 v2, s[60:61]
	s_add_i32 m0, s62, 0x2000
	s_nop 0
	global_load_lds_dwordx4 v160, s[60:61]
	v_lshl_add_u64 v[204:205], v[222:223], 0, s[34:35]
	s_mov_b32 m0, s65
	s_nop 0
	global_load_lds_dwordx4 v[204:205], off
	v_lshl_add_u64 v[204:205], v[224:225], 0, s[34:35]
	s_mov_b32 m0, s66
	s_nop 0
	global_load_lds_dwordx4 v[204:205], off
	s_waitcnt vmcnt(8)
	s_waitcnt lgkmcnt(0)
	s_barrier
	s_setprio 1
	s_waitcnt lgkmcnt(0)
	v_mfma_f32_16x16x32_bf16 v[64:67], v[124:127], v[174:177], v[64:67]
	v_mfma_f32_16x16x32_bf16 v[60:63], v[132:135], v[174:177], v[60:63]
	v_mfma_f32_16x16x32_bf16 v[48:51], v[124:127], v[182:185], v[48:51]
	v_mfma_f32_16x16x32_bf16 v[44:47], v[132:135], v[182:185], v[44:47]
	v_mfma_f32_16x16x32_bf16 v[32:35], v[124:127], v[190:193], v[32:35]
	v_mfma_f32_16x16x32_bf16 v[28:31], v[132:135], v[190:193], v[28:31]
	v_mfma_f32_16x16x32_bf16 v[16:19], v[124:127], v[214:217], v[16:19]
	v_mfma_f32_16x16x32_bf16 v[12:15], v[132:135], v[214:217], v[12:15]
	v_mfma_f32_16x16x32_bf16 v[64:67], v[128:131], v[178:181], v[64:67]
	v_mfma_f32_16x16x32_bf16 v[60:63], v[136:139], v[178:181], v[60:63]
	v_mfma_f32_16x16x32_bf16 v[48:51], v[128:131], v[186:189], v[48:51]
	v_mfma_f32_16x16x32_bf16 v[44:47], v[136:139], v[186:189], v[44:47]
	v_mfma_f32_16x16x32_bf16 v[32:35], v[128:131], v[210:213], v[32:35]
	v_mfma_f32_16x16x32_bf16 v[28:31], v[136:139], v[210:213], v[28:31]
	v_mfma_f32_16x16x32_bf16 v[16:19], v[128:131], v[218:221], v[16:19]
	v_mfma_f32_16x16x32_bf16 v[12:15], v[136:139], v[218:221], v[12:15]
	s_setprio 0
	s_setprio 1
	v_mfma_f32_16x16x32_bf16 v[56:59], v[140:143], v[174:177], v[56:59]
	v_mfma_f32_16x16x32_bf16 v[52:55], v[156:159], v[174:177], v[52:55]
	v_mfma_f32_16x16x32_bf16 v[40:43], v[140:143], v[182:185], v[40:43]
	v_mfma_f32_16x16x32_bf16 v[36:39], v[156:159], v[182:185], v[36:39]
	v_mfma_f32_16x16x32_bf16 v[24:27], v[140:143], v[190:193], v[24:27]
	v_mfma_f32_16x16x32_bf16 v[20:23], v[156:159], v[190:193], v[20:23]
	v_mfma_f32_16x16x32_bf16 v[8:11], v[140:143], v[214:217], v[8:11]
	v_mfma_f32_16x16x32_bf16 v[4:7], v[156:159], v[214:217], v[4:7]
	v_mfma_f32_16x16x32_bf16 v[56:59], v[144:147], v[178:181], v[56:59]
	v_mfma_f32_16x16x32_bf16 v[52:55], v[170:173], v[178:181], v[52:55]
	v_mfma_f32_16x16x32_bf16 v[40:43], v[144:147], v[186:189], v[40:43]
	v_mfma_f32_16x16x32_bf16 v[36:39], v[170:173], v[186:189], v[36:39]
	v_mfma_f32_16x16x32_bf16 v[24:27], v[144:147], v[210:213], v[24:27]
	v_mfma_f32_16x16x32_bf16 v[20:23], v[170:173], v[210:213], v[20:23]
	v_mfma_f32_16x16x32_bf16 v[8:11], v[144:147], v[218:221], v[8:11]
	v_mfma_f32_16x16x32_bf16 v[4:7], v[170:173], v[218:221], v[4:7]
	s_setprio 0
	s_barrier
	s_add_u32 s42, s42, 0x100
	s_addc_u32 s43, s43, 0
	s_add_u32 s70, s70, 0x100
	s_addc_u32 s71, s71, 0
	s_cmp_gt_u32 s72, 13
	s_mov_b32 s60, s72
	s_cbranch_scc0 .LBB0_1411
	s_waitcnt vmcnt(0)
	s_and_b64 vcc, exec, s[50:51]
	s_cbranch_vccz .LBB0_1414
	s_barrier

; #define PG8_STAGE(bufoff, gbase, voff) do { _Pragma("unroll") for (int _i = 0; _i < 2; ++_i) \
;         __builtin_amdgcn_global_load_lds((const unsigned*)((const char*)(gbase) + (voff)[_i]), (PG8_LAS unsigned*)(lds + (bufoff) + ldsw + _i * 8192), 16, 0, 0); } while (0)
; #define PG8_WAIT_V(n) asm volatile("s_waitcnt vmcnt(" #n ")" ::: "memory")
; #define PG8_BAR __builtin_amdgcn_s_barrier()
;   __device__ __forceinline__ bool next(int i,AttnUnit&u)const{ const int v=vcu+(i>>2)*grid; if(v>=256)return false; const int k=i&3,s=v&7; u.bh=v>>3; u.qb=(k==0)?s:(k==1)?15-s:(k==2)?16+s:31-s; return true; }
; template <class Epi, class Sched, bool ALIGN_EPI = false, bool SP2 = false, bool FP8 = false, bool ABLK = false>
; __device__ __forceinline__ void gemm_phase(PG8_LAS unsigned char* lds, const Gemm g, const Sched& S, const Epi& E) {
;     ...
;     const char* cA = (const char*)g.A + (size_t)cur.pm * tstep; const char* cB = (const char*)g.Bt + (size_t)cur.pn * tstep;
;     S.a_ready(cur);
;     if constexpr (SP2) {
;         PG8_STAGE(PG8_SB(0, 0), cB, voffB); PG8_STAGE(PG8_SB(0, 1), cB + hstep, voffB); PG8_STAGE(PG8_SA(0, 0), cA, voffA); PG8_STAGE(PG8_SA(0, 1), cA + hstepA, voffA);
;         if (wr == 1) PG8_BAR;
;         PG8_WAIT_V(2); PG8_BAR;
;         PG8_STAGE(PG8_SB(1, 0), cB + kstep, voffB); PG8_STAGE(PG8_SA(1, 0), cA + kstepA, voffA); PG8_STAGE(PG8_SB(1, 1), cB + hstep + kstep, voffB);
;         PG8_WAIT_V(0); PG8_BAR;
;     } else {
;         PG8_STAGE(PG8_SB(0, 0), cB, voffB); PG8_STAGE(PG8_SA(0, 0), cA, voffA); PG8_STAGE(PG8_SB(0, 1), cB + hstep, voffB); PG8_STAGE(PG8_SA(0, 1), cA + hstepA, voffA);
;         if (wr == 1) PG8_BAR;
;         PG8_WAIT_V(4); PG8_BAR;
;         PG8_STAGE(PG8_SB(1, 0), cB + kstep, voffB); PG8_STAGE(PG8_SA(1, 0), cA + kstepA, voffA); PG8_STAGE(PG8_SB(1, 1), cB + hstep + kstep, voffB);
;         PG8_WAIT_V(6); PG8_BAR;
;     }
;     for (;;) {
;         const bool has_next = S.next(ui + 1, nxt);
;         const char* nA = has_next ? (const char*)g.A + (size_t)nxt.pm * tstep : cA; const char* nB = has_next ? (const char*)g.Bt + (size_t)nxt.pn * tstep : cB;
.LBB0_1488:
	s_add_u32 s42, s40, 0xba00000
	s_addc_u32 s43, s41, 0
	s_add_u32 s44, s40, 0x1c000000
	s_addc_u32 s45, s41, 0
	v_bfe_u32 v182, v17, 4, 2
	s_lshl_b32 s4, s4, 5
	v_and_b32_e32 v1, 15, v17
	v_lshlrev_b32_e32 v19, 4, v182
	v_lshlrev_b32_e32 v17, 2, v17
	s_and_b32 s23, s4, 0x60
	s_add_i32 m0, s18, 0x18000
	v_lshl_add_u64 v[10:11], v[10:11], 0, s[34:35]
	s_lshl_b32 s22, s5, 6
	v_lshl_or_b32 v19, v1, 6, v19
	s_lshl_b32 s5, s5, 13
	v_and_b32_e32 v17, 32, v17
	s_lshl_b32 s4, s23, 7
	s_waitcnt vmcnt(2)
	s_barrier
	global_load_lds_dwordx4 v[10:11], off
	v_lshl_add_u64 v[8:9], v[8:9], 0, s[34:35]
	s_add_i32 m0, s18, 0x1a000
	s_add_i32 s62, s18, 0x8000
	s_add_i32 s63, s18, 0xa000
	v_bitop3_b32 v183, v19, s4, v17 bitop3:0xde
	global_load_lds_dwordx4 v[8:9], off
	v_lshl_add_u64 v[4:5], v[4:5], 0, s[34:35]
	s_mov_b32 m0, s62
	s_add_u32 s4, s58, 0x20080
	v_bitop3_b32 v20, v19, s5, v17 bitop3:0xde
	global_load_lds_dwordx4 v[4:5], off
	v_lshl_add_u64 v[4:5], v[6:7], 0, s[34:35]
	s_mov_b32 m0, s63
	s_addc_u32 s5, s59, 0
	global_load_lds_dwordx4 v[4:5], off
	s_add_i32 m0, s18, 0x1c000
	s_nop 0
	global_load_lds_dwordx4 v2, s[4:5]
	s_add_i32 m0, s18, 0x1e000
	s_cmpk_lt_u32 s46, 0x100
	global_load_lds_dwordx4 v164, s[4:5]
	v_lshlrev_b32_e32 v4, 13, v16
	v_and_b32_e32 v4, 0xffffc000, v4
	v_lshl_add_u32 v4, v15, 10, v4
	v_and_b32_e32 v5, 1, v16
	v_lshl_or_b32 v4, v5, 6, v4
	v_lshl_add_u32 v170, v18, 1, v4
	v_lshlrev_b32_e32 v4, 13, v12
	v_and_b32_e32 v4, 0xffffc000, v4
	s_waitcnt vmcnt(0)
	v_lshl_add_u32 v4, v13, 10, v4
	v_and_b32_e32 v5, 1, v12
	v_lshl_or_b32 v4, v5, 6, v4
	v_readlane_b32 s4, v252, 8
	s_cselect_b64 s[46:47], -1, 0
	v_mov_b32_e32 v171, v3
	v_lshl_add_u32 v172, v14, 1, v4
	v_mov_b32_e32 v173, v3
	s_mov_b32 s64, 0
	v_add_u32_e32 v184, 0, v20
	v_readlane_b32 s65, v254, 58
	s_mov_b32 s66, s4
	s_barrier
	v_readlane_b32 s5, v252, 9
	s_branch .LBB0_1491

; #define PG8_STAGE(bufoff, gbase, voff) do { _Pragma("unroll") for (int _i = 0; _i < 2; ++_i) \
;         __builtin_amdgcn_global_load_lds((const unsigned*)((const char*)(gbase) + (voff)[_i]), (PG8_LAS unsigned*)(lds + (bufoff) + ldsw + _i * 8192), 16, 0, 0); } while (0)
; #define PG8_LDA(dst, b, h) do { _Pragma("unroll") for (int m = 0; m < 4; ++m) _Pragma("unroll") for (int k = 0; k < 2; ++k) dst[m][k] = *(const PG8_LAS bf16x8*)(lds + PG8_SA(b, h) + aoff + m * 2048 + k * 1024); } while (0)
; #define PG8_LDB(dst, b, h) do { _Pragma("unroll") for (int n = 0; n < 2; ++n) _Pragma("unroll") for (int k = 0; k < 2; ++k) dst[n][k] = *(const PG8_LAS bf16x8*)(lds + PG8_SB(b, h) + boff + n * 2048 + k * 1024); } while (0)
; #define PG8_WAIT_V8_UNLESS_FIRST(t) asm volatile("s_cmp_eq_u32 %0, 0\n\ts_cbranch_scc1 .Lpg8skip%=\n\ts_waitcnt vmcnt(8)\n.Lpg8skip%=:" :: "s"(t) : "scc", "memory")
; #define PG8_WAIT_L(n) asm volatile("s_waitcnt lgkmcnt(" #n ")" ::: "memory")
; #define PG8_BAR __builtin_amdgcn_s_barrier()
; #define PG8_SCHED __builtin_amdgcn_sched_barrier(0)
; template <class Epi, class Sched, bool ALIGN_EPI = false, bool SP2 = false, bool FP8 = false, bool ABLK = false>
; __device__ __forceinline__ void gemm_phase(PG8_LAS unsigned char* lds, const Gemm g, const Sched& S, const Epi& E) {
;     ...
;         for (int t = 0; t < nt; t += 2) {
;             const bool last = (t == nt - 2);
;             const char* a1 = cA + (size_t)(t + 1) * kstepA;
;             const char* a2 = last ? nA : cA + (size_t)(t + 2) * kstepA; const char* b2 = last ? nB : cB + (size_t)(t + 2) * kstep;
;             const char* a3 = a2 + kstepA; const char* b3 = b2 + kstep;
;             if (last && has_next) S.a_ready(nxt);
;             if constexpr (SP2) {
;             PG8_LDB(B0, 0, 0); PG8_LDB(B1, 0, 1); PG8_SCHED; PG8_LDA(At, 0, 0); PG8_STAGE(PG8_SA(1, 1), a1 + hstepA, voffA);
;             PG8_WAIT_V8_UNLESS_FIRST(t); PG8_WAIT_L(0); PG8_BAR; PG8_MMA(0, 0, At, B0); PG8_MMA(0, 1, At, B1); PG8_BAR; PG8_SCHED;
;             PG8_LDA(At, 0, 1); PG8_STAGE(PG8_SB(0, 0), b2, voffB); PG8_STAGE(PG8_SB(0, 1), b2 + hstep, voffB); PG8_STAGE(PG8_SA(0, 0), a2, voffA);
;             PG8_WAIT_V8_UNLESS_FIRST(t); PG8_WAIT_L(0); PG8_BAR; PG8_MMA(1, 0, At, B0); PG8_MMA(1, 1, At, B1); PG8_BAR; PG8_SCHED;
.LBB0_1498:
	s_add_i32 s69, s58, 2
	s_add_u32 s59, s56, 0xfffe0080
	s_addc_u32 s60, s57, -1
	s_add_i32 s70, 0, 0x10000
	s_cmp_eq_u32 s58, 4
	s_cselect_b32 s61, s4, s60
	s_cselect_b32 s60, s5, s59
	s_cselect_b32 s59, s49, s68
	s_cselect_b32 s58, s51, s67
	s_add_i32 s71, 0, 0x14000
	v_add_u32_e32 v4, s70, v183
	v_add_u32_e32 v8, s71, v183
	ds_read_b128 v[28:31], v4
	ds_read_b128 v[32:35], v4 offset:1024
	ds_read_b128 v[20:23], v4 offset:2048
	ds_read_b128 v[24:27], v4 offset:3072
	ds_read_b128 v[12:15], v8
	ds_read_b128 v[16:19], v8 offset:1024
	ds_read_b128 v[4:7], v8 offset:2048
	ds_read_b128 v[8:11], v8 offset:3072
	s_add_i32 m0, s18, 0xc000
	ds_read_b128 v[174:177], v184
	ds_read_b128 v[178:181], v184 offset:1024
	ds_read_b128 v[186:189], v184 offset:2048
	ds_read_b128 v[190:193], v184 offset:3072
	ds_read_b128 v[208:211], v184 offset:4096
	ds_read_b128 v[212:215], v184 offset:5120
	ds_read_b128 v[216:219], v184 offset:6144
	ds_read_b128 v[220:223], v184 offset:7168
	global_load_lds_dwordx4 v170, s[56:57]
	s_add_i32 m0, s18, 0xe000
	s_nop 0
	global_load_lds_dwordx4 v172, s[56:57]
	s_cmp_eq_u32 s69, 0
	s_cbranch_scc1 .Lpg8skip8
	s_waitcnt vmcnt(8)
.Lpg8skip8:
	s_waitcnt lgkmcnt(0)
	s_barrier
	s_setprio 1
	s_waitcnt lgkmcnt(0)
	v_mfma_scale_f32_16x16x128_f8f6f4 v[160:163], v[28:35], v[174:181], v[160:163], v245, v245 op_sel_hi:[0,0,0]
	v_mfma_scale_f32_16x16x128_f8f6f4 v[156:159], v[20:27], v[174:181], v[156:159], v245, v245 op_sel_hi:[0,0,0]
	v_mfma_scale_f32_16x16x128_f8f6f4 v[144:147], v[28:35], v[186:193], v[144:147], v245, v245 op_sel_hi:[0,0,0]
	v_mfma_scale_f32_16x16x128_f8f6f4 v[140:143], v[20:27], v[186:193], v[140:143], v245, v245 op_sel_hi:[0,0,0]
	v_mfma_scale_f32_16x16x128_f8f6f4 v[128:131], v[28:35], v[208:215], v[128:131], v245, v245 op_sel_hi:[0,0,0]
	v_mfma_scale_f32_16x16x128_f8f6f4 v[124:127], v[20:27], v[208:215], v[124:127], v245, v245 op_sel_hi:[0,0,0]
	v_mfma_scale_f32_16x16x128_f8f6f4 v[112:115], v[28:35], v[216:223], v[112:115], v245, v245 op_sel_hi:[0,0,0]
	v_mfma_scale_f32_16x16x128_f8f6f4 v[108:111], v[20:27], v[216:223], v[108:111], v245, v245 op_sel_hi:[0,0,0]
	s_setprio 0
	s_setprio 1
	v_mfma_scale_f32_16x16x128_f8f6f4 v[152:155], v[12:19], v[174:181], v[152:155], v245, v245 op_sel_hi:[0,0,0]
	v_mfma_scale_f32_16x16x128_f8f6f4 v[148:151], v[4:11], v[174:181], v[148:151], v245, v245 op_sel_hi:[0,0,0]
	v_mfma_scale_f32_16x16x128_f8f6f4 v[136:139], v[12:19], v[186:193], v[136:139], v245, v245 op_sel_hi:[0,0,0]
	v_mfma_scale_f32_16x16x128_f8f6f4 v[132:135], v[4:11], v[186:193], v[132:135], v245, v245 op_sel_hi:[0,0,0]
	v_mfma_scale_f32_16x16x128_f8f6f4 v[120:123], v[12:19], v[208:215], v[120:123], v245, v245 op_sel_hi:[0,0,0]
	v_mfma_scale_f32_16x16x128_f8f6f4 v[116:119], v[4:11], v[208:215], v[116:119], v245, v245 op_sel_hi:[0,0,0]
	v_mfma_scale_f32_16x16x128_f8f6f4 v[104:107], v[12:19], v[216:223], v[104:107], v245, v245 op_sel_hi:[0,0,0]
	v_mfma_scale_f32_16x16x128_f8f6f4 v[100:103], v[4:11], v[216:223], v[100:103], v245, v245 op_sel_hi:[0,0,0]
	s_setprio 0
	s_barrier
	s_add_i32 s70, s70, s17
	v_lshl_add_u64 v[174:175], s[58:59], 0, v[2:3]
	s_mov_b32 m0, s70
	ds_read_b128 v[186:189], v184 offset:16384
	ds_read_b128 v[190:193], v184 offset:17408
	ds_read_b128 v[208:211], v184 offset:18432
	ds_read_b128 v[212:215], v184 offset:19456
	ds_read_b128 v[216:219], v184 offset:20480
	ds_read_b128 v[220:223], v184 offset:21504
	ds_read_b128 v[228:231], v184 offset:22528
	ds_read_b128 v[232:235], v184 offset:23552
	global_load_lds_dwordx4 v2, s[58:59]
	s_add_i32 m0, s70, 0x2000
	s_add_u32 s72, s58, 0x20000
	v_lshl_add_u64 v[176:177], s[58:59], 0, v[164:165]
	s_addc_u32 s73, s59, 0
	s_add_i32 s70, s71, s17
	global_load_lds_dwordx4 v164, s[58:59]
	s_mov_b32 m0, s70
	v_lshl_add_u64 v[180:181], s[60:61], 0, v[166:167]
	global_load_lds_dwordx4 v2, s[72:73]
	s_add_i32 m0, s70, 0x2000
	s_nop 0
	global_load_lds_dwordx4 v164, s[72:73]
	v_lshl_add_u64 v[178:179], s[60:61], 0, v[168:169]
	s_mov_b32 m0, s18
	s_nop 0
	global_load_lds_dwordx4 v168, s[60:61]
	s_mov_b32 m0, s19
	s_nop 0
	global_load_lds_dwordx4 v166, s[60:61]
	s_cmp_eq_u32 s69, 0
	s_cbranch_scc1 .Lpg8skip9
	s_waitcnt vmcnt(8)
.Lpg8skip9:
	s_waitcnt lgkmcnt(0)
	s_barrier
	s_setprio 1
	s_waitcnt lgkmcnt(0)
	v_mfma_scale_f32_16x16x128_f8f6f4 v[96:99], v[28:35], v[186:193], v[96:99], v245, v245 op_sel_hi:[0,0,0]
	v_mfma_scale_f32_16x16x128_f8f6f4 v[92:95], v[20:27], v[186:193], v[92:95], v245, v245 op_sel_hi:[0,0,0]
	v_mfma_scale_f32_16x16x128_f8f6f4 v[80:83], v[28:35], v[208:215], v[80:83], v245, v245 op_sel_hi:[0,0,0]
	v_mfma_scale_f32_16x16x128_f8f6f4 v[76:79], v[20:27], v[208:215], v[76:79], v245, v245 op_sel_hi:[0,0,0]
	v_mfma_scale_f32_16x16x128_f8f6f4 v[64:67], v[28:35], v[216:223], v[64:67], v245, v245 op_sel_hi:[0,0,0]
	v_mfma_scale_f32_16x16x128_f8f6f4 v[60:63], v[20:27], v[216:223], v[60:63], v245, v245 op_sel_hi:[0,0,0]
	v_mfma_scale_f32_16x16x128_f8f6f4 v[48:51], v[28:35], v[228:235], v[48:51], v245, v245 op_sel_hi:[0,0,0]
	v_mfma_scale_f32_16x16x128_f8f6f4 v[44:47], v[20:27], v[228:235], v[44:47], v245, v245 op_sel_hi:[0,0,0]
	s_setprio 0
	s_setprio 1
	v_mfma_scale_f32_16x16x128_f8f6f4 v[88:91], v[12:19], v[186:193], v[88:91], v245, v245 op_sel_hi:[0,0,0]
	v_mfma_scale_f32_16x16x128_f8f6f4 v[84:87], v[4:11], v[186:193], v[84:87], v245, v245 op_sel_hi:[0,0,0]
	v_mfma_scale_f32_16x16x128_f8f6f4 v[72:75], v[12:19], v[208:215], v[72:75], v245, v245 op_sel_hi:[0,0,0]
	v_mfma_scale_f32_16x16x128_f8f6f4 v[68:71], v[4:11], v[208:215], v[68:71], v245, v245 op_sel_hi:[0,0,0]
	v_mfma_scale_f32_16x16x128_f8f6f4 v[56:59], v[12:19], v[216:223], v[56:59], v245, v245 op_sel_hi:[0,0,0]
	v_mfma_scale_f32_16x16x128_f8f6f4 v[52:55], v[4:11], v[216:223], v[52:55], v245, v245 op_sel_hi:[0,0,0]
	v_mfma_scale_f32_16x16x128_f8f6f4 v[40:43], v[12:19], v[228:235], v[40:43], v245, v245 op_sel_hi:[0,0,0]
	v_mfma_scale_f32_16x16x128_f8f6f4 v[36:39], v[4:11], v[228:235], v[36:39], v245, v245 op_sel_hi:[0,0,0]
	s_setprio 0
	s_barrier
; #define PG8_WAIT_V(n) asm volatile("s_waitcnt vmcnt(" #n ")" ::: "memory")
; #define PG8_WAIT_L(n) asm volatile("s_waitcnt lgkmcnt(" #n ")" ::: "memory")
; template <class Epi, class Sched, bool ALIGN_EPI = false, bool SP2 = false, bool FP8 = false, bool ABLK = false>
; __device__ __forceinline__ void gemm_phase(PG8_LAS unsigned char* lds, const Gemm g, const Sched& S, const Epi& E) {
;     ...
;             PG8_LDB(B0, 1, 0); PG8_LDB(B1, 1, 1); PG8_SCHED; PG8_LDA(At, 1, 0); PG8_STAGE(PG8_SA(0, 1), a2 + hstepA, voffA);
;             PG8_WAIT_V(8); PG8_WAIT_L(0); PG8_BAR; PG8_MMA(0, 0, At, B0); PG8_MMA(0, 1, At, B1); PG8_BAR; PG8_SCHED;
;             PG8_LDA(At, 1, 1); PG8_STAGE(PG8_SB(1, 0), b3, voffB); PG8_STAGE(PG8_SB(1, 1), b3 + hstep, voffB); PG8_STAGE(PG8_SA(1, 0), a3, voffA);
;             PG8_WAIT_V(8); PG8_WAIT_L(0); PG8_BAR; PG8_MMA(1, 0, At, B0); PG8_MMA(1, 1, At, B1); PG8_BAR; PG8_SCHED;
;             } else {
;             PG8_LDB(B0, 0, 0); PG8_SCHED; PG8_LDA(At, 0, 0); PG8_STAGE(PG8_SA(1, 1), a1 + hstepA, voffA);
;             PG8_WAIT_L(8); PG8_BAR; PG8_WAIT_L(0); PG8_MMA(0, 0, At, B0); PG8_BAR; PG8_SCHED;
;             PG8_LDB(B1, 0, 1); PG8_STAGE(PG8_SB(0, 0), b2, voffB);
;             PG8_BAR; PG8_WAIT_L(0); PG8_MMA(0, 1, At, B1); PG8_BAR;
;             PG8_LDA(At, 0, 1); PG8_STAGE(PG8_SA(0, 0), a2, voffA);
;             PG8_BAR; PG8_WAIT_L(0); PG8_MMA(1, 0, At, B0); PG8_BAR; PG8_SCHED;
;             PG8_STAGE(PG8_SB(0, 1), b2 + hstep, voffB);
;             PG8_WAIT_V(6); PG8_BAR; PG8_MMA(1, 1, At, B1); PG8_BAR;
;             PG8_LDB(B0, 1, 0); PG8_SCHED; PG8_LDA(At, 1, 0); PG8_STAGE(PG8_SA(0, 1), a2 + hstepA, voffA);
;             PG8_WAIT_L(8); PG8_BAR; PG8_WAIT_L(0); PG8_MMA(0, 0, At, B0); PG8_BAR; PG8_SCHED;
;             PG8_LDB(B1, 1, 1); PG8_STAGE(PG8_SB(1, 0), b3, voffB);
;             PG8_BAR; PG8_WAIT_L(0); PG8_MMA(0, 1, At, B1); PG8_BAR;
;             PG8_LDA(At, 1, 1); PG8_STAGE(PG8_SA(1, 0), a3, voffA);
;             PG8_BAR; PG8_WAIT_L(0); PG8_MMA(1, 0, At, B0); PG8_BAR; PG8_SCHED;
;             PG8_STAGE(PG8_SB(1, 1), b3 + hstep, voffB);
;             PG8_WAIT_V(6); PG8_BAR; PG8_MMA(1, 1, At, B1); PG8_BAR;
;             }
;         }
;         if constexpr (SP2) PG8_WAIT_V(0);
;         if constexpr (FP8) asm volatile("s_nop 15\n\ts_nop 15" ::: "memory");
;         if constexpr (ALIGN_EPI) { if (wr == 0) PG8_BAR; }
	s_add_i32 s70, 0, 0x18000
	s_add_i32 s71, 0, 0x1c000
	v_add_u32_e32 v16, s70, v183
	v_add_u32_e32 v32, s71, v183
	ds_read_b128 v[4:7], v16
	ds_read_b128 v[8:11], v16 offset:1024
	ds_read_b128 v[12:15], v16 offset:2048
	ds_read_b128 v[16:19], v16 offset:3072
	ds_read_b128 v[20:23], v32
	ds_read_b128 v[24:27], v32 offset:1024
	ds_read_b128 v[28:31], v32 offset:2048
	ds_read_b128 v[32:35], v32 offset:3072
	s_add_u32 s60, s60, 0x20000
	s_addc_u32 s61, s61, 0
	s_mov_b32 m0, s20
	ds_read_b128 v[186:189], v184 offset:32768
	ds_read_b128 v[190:193], v184 offset:33792
	ds_read_b128 v[208:211], v184 offset:34816
	ds_read_b128 v[212:215], v184 offset:35840
	ds_read_b128 v[216:219], v184 offset:36864
	ds_read_b128 v[220:223], v184 offset:37888
	ds_read_b128 v[228:231], v184 offset:38912
	ds_read_b128 v[232:235], v184 offset:39936
	global_load_lds_dwordx4 v168, s[60:61]
	s_mov_b32 m0, s21
	s_nop 0
	global_load_lds_dwordx4 v166, s[60:61]
	s_waitcnt vmcnt(8)
	s_waitcnt lgkmcnt(0)
	s_barrier
	s_setprio 1
	s_waitcnt lgkmcnt(0)
	v_mfma_scale_f32_16x16x128_f8f6f4 v[160:163], v[4:11], v[186:193], v[160:163], v245, v245 op_sel_hi:[0,0,0]
	v_mfma_scale_f32_16x16x128_f8f6f4 v[156:159], v[12:19], v[186:193], v[156:159], v245, v245 op_sel_hi:[0,0,0]
	v_mfma_scale_f32_16x16x128_f8f6f4 v[144:147], v[4:11], v[208:215], v[144:147], v245, v245 op_sel_hi:[0,0,0]
	v_mfma_scale_f32_16x16x128_f8f6f4 v[140:143], v[12:19], v[208:215], v[140:143], v245, v245 op_sel_hi:[0,0,0]
	v_mfma_scale_f32_16x16x128_f8f6f4 v[128:131], v[4:11], v[216:223], v[128:131], v245, v245 op_sel_hi:[0,0,0]
	v_mfma_scale_f32_16x16x128_f8f6f4 v[124:127], v[12:19], v[216:223], v[124:127], v245, v245 op_sel_hi:[0,0,0]
	v_mfma_scale_f32_16x16x128_f8f6f4 v[112:115], v[4:11], v[228:235], v[112:115], v245, v245 op_sel_hi:[0,0,0]
	v_mfma_scale_f32_16x16x128_f8f6f4 v[108:111], v[12:19], v[228:235], v[108:111], v245, v245 op_sel_hi:[0,0,0]
	s_setprio 0
	s_setprio 1
	v_mfma_scale_f32_16x16x128_f8f6f4 v[152:155], v[20:27], v[186:193], v[152:155], v245, v245 op_sel_hi:[0,0,0]
	v_mfma_scale_f32_16x16x128_f8f6f4 v[148:151], v[28:35], v[186:193], v[148:151], v245, v245 op_sel_hi:[0,0,0]
	v_mfma_scale_f32_16x16x128_f8f6f4 v[136:139], v[20:27], v[208:215], v[136:139], v245, v245 op_sel_hi:[0,0,0]
	v_mfma_scale_f32_16x16x128_f8f6f4 v[132:135], v[28:35], v[208:215], v[132:135], v245, v245 op_sel_hi:[0,0,0]
	v_mfma_scale_f32_16x16x128_f8f6f4 v[120:123], v[20:27], v[216:223], v[120:123], v245, v245 op_sel_hi:[0,0,0]
	v_mfma_scale_f32_16x16x128_f8f6f4 v[116:119], v[28:35], v[216:223], v[116:119], v245, v245 op_sel_hi:[0,0,0]
	v_mfma_scale_f32_16x16x128_f8f6f4 v[104:107], v[20:27], v[228:235], v[104:107], v245, v245 op_sel_hi:[0,0,0]
	v_mfma_scale_f32_16x16x128_f8f6f4 v[100:103], v[28:35], v[228:235], v[100:103], v245, v245 op_sel_hi:[0,0,0]
	s_setprio 0
	s_barrier
	s_add_i32 s60, s70, s17
	v_lshl_add_u64 v[174:175], v[174:175], 0, s[34:35]
	s_mov_b32 m0, s60
	ds_read_b128 v[186:189], v184 offset:49152
	ds_read_b128 v[190:193], v184 offset:50176
	ds_read_b128 v[208:211], v184 offset:51200
	ds_read_b128 v[212:215], v184 offset:52224
	ds_read_b128 v[216:219], v184 offset:53248
	ds_read_b128 v[220:223], v184 offset:54272
	ds_read_b128 v[228:231], v184 offset:55296
	ds_read_b128 v[232:235], v184 offset:56320
	global_load_lds_dwordx4 v[174:175], off
	s_add_i32 m0, s60, 0x2000
	s_add_u32 s58, s58, 0x20080
	v_lshl_add_u64 v[174:175], v[176:177], 0, s[34:35]
	s_addc_u32 s59, s59, 0
	s_add_i32 s60, s71, s17
	global_load_lds_dwordx4 v[174:175], off
	s_mov_b32 m0, s60
	s_nop 0
	global_load_lds_dwordx4 v2, s[58:59]
	s_add_i32 m0, s60, 0x2000
	s_nop 0
	global_load_lds_dwordx4 v164, s[58:59]
	v_lshl_add_u64 v[174:175], v[178:179], 0, s[34:35]
	s_mov_b32 m0, s62
	s_nop 0
	global_load_lds_dwordx4 v[174:175], off
	v_lshl_add_u64 v[174:175], v[180:181], 0, s[34:35]
	s_mov_b32 m0, s63
	s_nop 0
	global_load_lds_dwordx4 v[174:175], off
	s_waitcnt vmcnt(8)
	s_waitcnt lgkmcnt(0)
	s_barrier
	s_setprio 1
	s_waitcnt lgkmcnt(0)
	v_mfma_scale_f32_16x16x128_f8f6f4 v[96:99], v[4:11], v[186:193], v[96:99], v245, v245 op_sel_hi:[0,0,0]
	v_mfma_scale_f32_16x16x128_f8f6f4 v[92:95], v[12:19], v[186:193], v[92:95], v245, v245 op_sel_hi:[0,0,0]
	v_mfma_scale_f32_16x16x128_f8f6f4 v[80:83], v[4:11], v[208:215], v[80:83], v245, v245 op_sel_hi:[0,0,0]
	v_mfma_scale_f32_16x16x128_f8f6f4 v[76:79], v[12:19], v[208:215], v[76:79], v245, v245 op_sel_hi:[0,0,0]
	v_mfma_scale_f32_16x16x128_f8f6f4 v[64:67], v[4:11], v[216:223], v[64:67], v245, v245 op_sel_hi:[0,0,0]
	v_mfma_scale_f32_16x16x128_f8f6f4 v[60:63], v[12:19], v[216:223], v[60:63], v245, v245 op_sel_hi:[0,0,0]
	v_mfma_scale_f32_16x16x128_f8f6f4 v[48:51], v[4:11], v[228:235], v[48:51], v245, v245 op_sel_hi:[0,0,0]
	v_mfma_scale_f32_16x16x128_f8f6f4 v[44:47], v[12:19], v[228:235], v[44:47], v245, v245 op_sel_hi:[0,0,0]
	s_setprio 0
	s_setprio 1
	v_mfma_scale_f32_16x16x128_f8f6f4 v[88:91], v[20:27], v[186:193], v[88:91], v245, v245 op_sel_hi:[0,0,0]
	v_mfma_scale_f32_16x16x128_f8f6f4 v[84:87], v[28:35], v[186:193], v[84:87], v245, v245 op_sel_hi:[0,0,0]
	v_mfma_scale_f32_16x16x128_f8f6f4 v[72:75], v[20:27], v[208:215], v[72:75], v245, v245 op_sel_hi:[0,0,0]
	v_mfma_scale_f32_16x16x128_f8f6f4 v[68:71], v[28:35], v[208:215], v[68:71], v245, v245 op_sel_hi:[0,0,0]
	v_mfma_scale_f32_16x16x128_f8f6f4 v[56:59], v[20:27], v[216:223], v[56:59], v245, v245 op_sel_hi:[0,0,0]
	v_mfma_scale_f32_16x16x128_f8f6f4 v[52:55], v[28:35], v[216:223], v[52:55], v245, v245 op_sel_hi:[0,0,0]
	v_mfma_scale_f32_16x16x128_f8f6f4 v[40:43], v[20:27], v[228:235], v[40:43], v245, v245 op_sel_hi:[0,0,0]
	v_mfma_scale_f32_16x16x128_f8f6f4 v[36:39], v[28:35], v[228:235], v[36:39], v245, v245 op_sel_hi:[0,0,0]
	s_setprio 0
	s_barrier
	s_add_u32 s56, s56, 0x100
	s_addc_u32 s57, s57, 0
	s_add_u32 s67, s67, 0x100
	s_addc_u32 s68, s68, 0
	s_cmp_gt_u32 s69, 5
	s_mov_b32 s58, s69
	s_cbranch_scc0 .LBB0_1498
	s_waitcnt vmcnt(0)
	s_nop 15
	s_nop 15
	s_and_b64 vcc, exec, s[46:47]
	s_cbranch_vccz .LBB0_1501
	s_barrier

; #define PG8_STAGE(bufoff, gbase, voff) do { _Pragma("unroll") for (int _i = 0; _i < 2; ++_i) \
;         __builtin_amdgcn_global_load_lds((const unsigned*)((const char*)(gbase) + (voff)[_i]), (PG8_LAS unsigned*)(lds + (bufoff) + ldsw + _i * 8192), 16, 0, 0); } while (0)
; #define PG8_WAIT_V(n) asm volatile("s_waitcnt vmcnt(" #n ")" ::: "memory")
; #define PG8_BAR __builtin_amdgcn_s_barrier()
;   __device__ __forceinline__ bool next(int i,AttnUnit&u)const{ const int v=vcu+(i>>2)*grid; if(v>=256)return false; const int k=i&3,s=v&7; u.bh=v>>3; u.qb=(k==0)?s:(k==1)?15-s:(k==2)?16+s:31-s; return true; }
; template <class Epi, class Sched, bool ALIGN_EPI = false, bool SP2 = false, bool FP8 = false, bool ABLK = false>
; __device__ __forceinline__ void gemm_phase(PG8_LAS unsigned char* lds, const Gemm g, const Sched& S, const Epi& E) {
;     ...
;     const char* cA = (const char*)g.A + (size_t)cur.pm * tstep; const char* cB = (const char*)g.Bt + (size_t)cur.pn * tstep;
;     S.a_ready(cur);
;     if constexpr (SP2) {
;         PG8_STAGE(PG8_SB(0, 0), cB, voffB); PG8_STAGE(PG8_SB(0, 1), cB + hstep, voffB); PG8_STAGE(PG8_SA(0, 0), cA, voffA); PG8_STAGE(PG8_SA(0, 1), cA + hstepA, voffA);
;         if (wr == 1) PG8_BAR;
;         PG8_WAIT_V(2); PG8_BAR;
;         PG8_STAGE(PG8_SB(1, 0), cB + kstep, voffB); PG8_STAGE(PG8_SA(1, 0), cA + kstepA, voffA); PG8_STAGE(PG8_SB(1, 1), cB + hstep + kstep, voffB);
;         PG8_WAIT_V(0); PG8_BAR;
;     } else {
;         PG8_STAGE(PG8_SB(0, 0), cB, voffB); PG8_STAGE(PG8_SA(0, 0), cA, voffA); PG8_STAGE(PG8_SB(0, 1), cB + hstep, voffB); PG8_STAGE(PG8_SA(0, 1), cA + hstepA, voffA);
;         if (wr == 1) PG8_BAR;
;         PG8_WAIT_V(4); PG8_BAR;
;         PG8_STAGE(PG8_SB(1, 0), cB + kstep, voffB); PG8_STAGE(PG8_SA(1, 0), cA + kstepA, voffA); PG8_STAGE(PG8_SB(1, 1), cB + hstep + kstep, voffB);
;         PG8_WAIT_V(6); PG8_BAR;
;     }
;     for (;;) {
;         const bool has_next = S.next(ui + 1, nxt);
;         const char* nA = has_next ? (const char*)g.A + (size_t)nxt.pm * tstep : cA; const char* nB = has_next ? (const char*)g.Bt + (size_t)nxt.pn * tstep : cB;
.LBB0_1577:
	s_add_u32 s44, s40, 0x7a00000
	s_addc_u32 s45, s41, 0
	s_add_u32 s46, s40, 0x1c200000
	s_addc_u32 s47, s41, 0
	v_bfe_u32 v194, v17, 4, 2
	s_add_u32 s48, s40, 0x11a00000
	v_and_b32_e32 v1, 15, v17
	v_lshlrev_b32_e32 v19, 4, v194
	v_lshlrev_b32_e32 v17, 2, v17
	s_addc_u32 s49, s41, 0
	s_and_b32 s22, s5, 3
	s_lshl_b32 s23, s4, 6
	v_lshl_or_b32 v19, v1, 6, v19
	s_lshl_b32 s4, s4, 13
	v_and_b32_e32 v17, 32, v17
	s_add_i32 m0, s18, 0x18000
	v_lshl_add_u64 v[10:11], v[10:11], 0, s[34:35]
	v_bitop3_b32 v20, v19, s4, v17 bitop3:0xde
	s_lshl_b32 s64, s22, 5
	s_lshl_b32 s4, s22, 12
	s_waitcnt vmcnt(2)
	s_barrier
	global_load_lds_dwordx4 v[10:11], off
	v_lshl_add_u64 v[8:9], v[8:9], 0, s[34:35]
	s_add_i32 m0, s18, 0x1a000
	s_add_i32 s65, s18, 0x8000
	s_add_i32 s66, s18, 0xa000
	v_bitop3_b32 v195, v19, s4, v17 bitop3:0xde
	global_load_lds_dwordx4 v[8:9], off
	v_lshl_add_u64 v[4:5], v[4:5], 0, s[34:35]
	s_mov_b32 m0, s65
	s_add_u32 s4, s60, 0x20080
	global_load_lds_dwordx4 v[4:5], off
	v_lshl_add_u64 v[4:5], v[6:7], 0, s[34:35]
	s_mov_b32 m0, s66
	s_addc_u32 s5, s61, 0
	global_load_lds_dwordx4 v[4:5], off
	s_add_i32 m0, s18, 0x1c000
	s_nop 0
	global_load_lds_dwordx4 v2, s[4:5]
	s_add_i32 m0, s18, 0x1e000
	s_cmpk_lt_u32 s50, 0x100
	global_load_lds_dwordx4 v164, s[4:5]
	v_lshlrev_b32_e32 v4, 13, v16
	v_and_b32_e32 v4, 0xffffc000, v4
	v_lshl_add_u32 v4, v15, 10, v4
	v_and_b32_e32 v5, 1, v16
	v_lshl_or_b32 v4, v5, 6, v4
	v_lshl_add_u32 v170, v18, 1, v4
	v_lshlrev_b32_e32 v4, 13, v12
	v_and_b32_e32 v4, 0xffffc000, v4
	s_waitcnt vmcnt(0)
	v_lshl_add_u32 v4, v13, 10, v4
	v_and_b32_e32 v5, 1, v12
	v_lshl_or_b32 v4, v5, 6, v4
	v_readlane_b32 s4, v252, 8
	s_cselect_b64 s[50:51], -1, 0
	v_mov_b32_e32 v171, v3
	v_lshl_add_u32 v172, v14, 1, v4
	v_mov_b32_e32 v173, v3
	s_mov_b32 s67, 0
	v_add_u32_e32 v208, 0, v20
	v_readlane_b32 s68, v254, 58
	s_mov_b32 s69, s4
	s_barrier
	v_readlane_b32 s5, v252, 9
	s_branch .LBB0_1580

; #define PG8_STAGE(bufoff, gbase, voff) do { _Pragma("unroll") for (int _i = 0; _i < 2; ++_i) \
;         __builtin_amdgcn_global_load_lds((const unsigned*)((const char*)(gbase) + (voff)[_i]), (PG8_LAS unsigned*)(lds + (bufoff) + ldsw + _i * 8192), 16, 0, 0); } while (0)
; #define PG8_LDA(dst, b, h) do { _Pragma("unroll") for (int m = 0; m < 4; ++m) _Pragma("unroll") for (int k = 0; k < 2; ++k) dst[m][k] = *(const PG8_LAS bf16x8*)(lds + PG8_SA(b, h) + aoff + m * 2048 + k * 1024); } while (0)
; #define PG8_LDB(dst, b, h) do { _Pragma("unroll") for (int n = 0; n < 2; ++n) _Pragma("unroll") for (int k = 0; k < 2; ++k) dst[n][k] = *(const PG8_LAS bf16x8*)(lds + PG8_SB(b, h) + boff + n * 2048 + k * 1024); } while (0)
; #define PG8_WAIT_V8_UNLESS_FIRST(t) asm volatile("s_cmp_eq_u32 %0, 0\n\ts_cbranch_scc1 .Lpg8skip%=\n\ts_waitcnt vmcnt(8)\n.Lpg8skip%=:" :: "s"(t) : "scc", "memory")
; #define PG8_WAIT_L(n) asm volatile("s_waitcnt lgkmcnt(" #n ")" ::: "memory")
; #define PG8_BAR __builtin_amdgcn_s_barrier()
; #define PG8_SCHED __builtin_amdgcn_sched_barrier(0)
; template <class Epi, class Sched, bool ALIGN_EPI = false, bool SP2 = false, bool FP8 = false, bool ABLK = false>
; __device__ __forceinline__ void gemm_phase(PG8_LAS unsigned char* lds, const Gemm g, const Sched& S, const Epi& E) {
;     ...
;         for (int t = 0; t < nt; t += 2) {
;             const bool last = (t == nt - 2);
;             const char* a1 = cA + (size_t)(t + 1) * kstepA;
;             const char* a2 = last ? nA : cA + (size_t)(t + 2) * kstepA; const char* b2 = last ? nB : cB + (size_t)(t + 2) * kstep;
;             const char* a3 = a2 + kstepA; const char* b3 = b2 + kstep;
;             if (last && has_next) S.a_ready(nxt);
;             if constexpr (SP2) {
;             PG8_LDB(B0, 0, 0); PG8_LDB(B1, 0, 1); PG8_SCHED; PG8_LDA(At, 0, 0); PG8_STAGE(PG8_SA(1, 1), a1 + hstepA, voffA);
;             PG8_WAIT_V8_UNLESS_FIRST(t); PG8_WAIT_L(0); PG8_BAR; PG8_MMA(0, 0, At, B0); PG8_MMA(0, 1, At, B1); PG8_BAR; PG8_SCHED;
;             PG8_LDA(At, 0, 1); PG8_STAGE(PG8_SB(0, 0), b2, voffB); PG8_STAGE(PG8_SB(0, 1), b2 + hstep, voffB); PG8_STAGE(PG8_SA(0, 0), a2, voffA);
;             PG8_WAIT_V8_UNLESS_FIRST(t); PG8_WAIT_L(0); PG8_BAR; PG8_MMA(1, 0, At, B0); PG8_MMA(1, 1, At, B1); PG8_BAR; PG8_SCHED;
.LBB0_1587:
	s_add_i32 s72, s60, 2
	s_add_u32 s61, s42, 0xfffe0080
	s_addc_u32 s62, s43, -1
	s_add_i32 s73, 0, 0x10000
	s_cmp_eq_u32 s60, 4
	s_cselect_b32 s63, s4, s62
	s_cselect_b32 s62, s5, s61
	s_cselect_b32 s61, s53, s71
	s_cselect_b32 s60, s55, s70
	s_add_i32 s74, 0, 0x14000
	v_add_u32_e32 v4, s73, v195
	v_add_u32_e32 v8, s74, v195
	ds_read_b128 v[28:31], v4
	ds_read_b128 v[32:35], v4 offset:1024
	ds_read_b128 v[20:23], v4 offset:2048
	ds_read_b128 v[24:27], v4 offset:3072
	ds_read_b128 v[12:15], v8
	ds_read_b128 v[16:19], v8 offset:1024
	s_waitcnt lgkmcnt(0)
	ds_read_b128 v[4:7], v8 offset:2048
	ds_read_b128 v[8:11], v8 offset:3072
	s_add_i32 m0, s18, 0xc000
	ds_read_b128 v[174:177], v208
	ds_read_b128 v[178:181], v208 offset:1024
	ds_read_b128 v[182:185], v208 offset:2048
	ds_read_b128 v[186:189], v208 offset:3072
	ds_read_b128 v[210:213], v208 offset:4096
	ds_read_b128 v[214:217], v208 offset:5120
	ds_read_b128 v[218:221], v208 offset:6144
	ds_read_b128 v[222:225], v208 offset:7168
	global_load_lds_dwordx4 v170, s[42:43]
	s_add_i32 m0, s18, 0xe000
	s_nop 0
	global_load_lds_dwordx4 v172, s[42:43]
	s_cmp_eq_u32 s72, 0
	s_cbranch_scc1 .Lpg8skip10
	s_waitcnt vmcnt(8)
.Lpg8skip10:
	s_waitcnt lgkmcnt(0)
	s_barrier
	s_setprio 1
	s_waitcnt lgkmcnt(0)
	v_mfma_scale_f32_16x16x128_f8f6f4 v[160:163], v[28:35], v[174:181], v[160:163], v245, v245 op_sel_hi:[0,0,0]
	v_mfma_scale_f32_16x16x128_f8f6f4 v[156:159], v[20:27], v[174:181], v[156:159], v245, v245 op_sel_hi:[0,0,0]
	v_mfma_scale_f32_16x16x128_f8f6f4 v[144:147], v[28:35], v[182:189], v[144:147], v245, v245 op_sel_hi:[0,0,0]
	v_mfma_scale_f32_16x16x128_f8f6f4 v[140:143], v[20:27], v[182:189], v[140:143], v245, v245 op_sel_hi:[0,0,0]
	v_mfma_scale_f32_16x16x128_f8f6f4 v[128:131], v[28:35], v[210:217], v[128:131], v245, v245 op_sel_hi:[0,0,0]
	v_mfma_scale_f32_16x16x128_f8f6f4 v[124:127], v[20:27], v[210:217], v[124:127], v245, v245 op_sel_hi:[0,0,0]
	v_mfma_scale_f32_16x16x128_f8f6f4 v[112:115], v[28:35], v[218:225], v[112:115], v245, v245 op_sel_hi:[0,0,0]
	v_mfma_scale_f32_16x16x128_f8f6f4 v[108:111], v[20:27], v[218:225], v[108:111], v245, v245 op_sel_hi:[0,0,0]
	s_setprio 0
	s_setprio 1
	v_mfma_scale_f32_16x16x128_f8f6f4 v[152:155], v[12:19], v[174:181], v[152:155], v245, v245 op_sel_hi:[0,0,0]
	v_mfma_scale_f32_16x16x128_f8f6f4 v[148:151], v[4:11], v[174:181], v[148:151], v245, v245 op_sel_hi:[0,0,0]
	v_mfma_scale_f32_16x16x128_f8f6f4 v[136:139], v[12:19], v[182:189], v[136:139], v245, v245 op_sel_hi:[0,0,0]
	v_mfma_scale_f32_16x16x128_f8f6f4 v[132:135], v[4:11], v[182:189], v[132:135], v245, v245 op_sel_hi:[0,0,0]
	v_mfma_scale_f32_16x16x128_f8f6f4 v[120:123], v[12:19], v[210:217], v[120:123], v245, v245 op_sel_hi:[0,0,0]
	v_mfma_scale_f32_16x16x128_f8f6f4 v[116:119], v[4:11], v[210:217], v[116:119], v245, v245 op_sel_hi:[0,0,0]
	v_mfma_scale_f32_16x16x128_f8f6f4 v[104:107], v[12:19], v[218:225], v[104:107], v245, v245 op_sel_hi:[0,0,0]
	v_mfma_scale_f32_16x16x128_f8f6f4 v[100:103], v[4:11], v[218:225], v[100:103], v245, v245 op_sel_hi:[0,0,0]
	s_setprio 0
	s_barrier
	s_add_i32 s73, s73, s17
	v_lshl_add_u64 v[174:175], s[60:61], 0, v[2:3]
	s_mov_b32 m0, s73
	ds_read_b128 v[182:185], v208 offset:16384
	ds_read_b128 v[186:189], v208 offset:17408
	ds_read_b128 v[210:213], v208 offset:18432
	ds_read_b128 v[214:217], v208 offset:19456
	ds_read_b128 v[218:221], v208 offset:20480
	ds_read_b128 v[222:225], v208 offset:21504
	ds_read_b128 v[228:231], v208 offset:22528
	ds_read_b128 v[232:235], v208 offset:23552
	global_load_lds_dwordx4 v2, s[60:61]
	s_add_i32 m0, s73, 0x2000
	s_add_u32 s76, s60, 0x20000
	v_lshl_add_u64 v[176:177], s[60:61], 0, v[164:165]
	s_addc_u32 s77, s61, 0
	s_add_i32 s73, s74, s17
	global_load_lds_dwordx4 v164, s[60:61]
	s_mov_b32 m0, s73
	v_lshl_add_u64 v[180:181], s[62:63], 0, v[166:167]
	global_load_lds_dwordx4 v2, s[76:77]
	s_add_i32 m0, s73, 0x2000
	s_nop 0
	global_load_lds_dwordx4 v164, s[76:77]
	v_lshl_add_u64 v[178:179], s[62:63], 0, v[168:169]
	s_mov_b32 m0, s18
	s_nop 0
	global_load_lds_dwordx4 v168, s[62:63]
	s_mov_b32 m0, s19
	s_nop 0
	global_load_lds_dwordx4 v166, s[62:63]
	s_cmp_eq_u32 s72, 0
	s_cbranch_scc1 .Lpg8skip11
	s_waitcnt vmcnt(8)
.Lpg8skip11:
	s_waitcnt lgkmcnt(0)
	s_barrier
	s_setprio 1
	s_waitcnt lgkmcnt(0)
	v_mfma_scale_f32_16x16x128_f8f6f4 v[96:99], v[28:35], v[182:189], v[96:99], v245, v245 op_sel_hi:[0,0,0]
	v_mfma_scale_f32_16x16x128_f8f6f4 v[92:95], v[20:27], v[182:189], v[92:95], v245, v245 op_sel_hi:[0,0,0]
	v_mfma_scale_f32_16x16x128_f8f6f4 v[80:83], v[28:35], v[210:217], v[80:83], v245, v245 op_sel_hi:[0,0,0]
	v_mfma_scale_f32_16x16x128_f8f6f4 v[76:79], v[20:27], v[210:217], v[76:79], v245, v245 op_sel_hi:[0,0,0]
	v_mfma_scale_f32_16x16x128_f8f6f4 v[64:67], v[28:35], v[218:225], v[64:67], v245, v245 op_sel_hi:[0,0,0]
	v_mfma_scale_f32_16x16x128_f8f6f4 v[60:63], v[20:27], v[218:225], v[60:63], v245, v245 op_sel_hi:[0,0,0]
	v_mfma_scale_f32_16x16x128_f8f6f4 v[48:51], v[28:35], v[228:235], v[48:51], v245, v245 op_sel_hi:[0,0,0]
	v_mfma_scale_f32_16x16x128_f8f6f4 v[44:47], v[20:27], v[228:235], v[44:47], v245, v245 op_sel_hi:[0,0,0]
	s_setprio 0
	s_setprio 1
	v_mfma_scale_f32_16x16x128_f8f6f4 v[88:91], v[12:19], v[182:189], v[88:91], v245, v245 op_sel_hi:[0,0,0]
	v_mfma_scale_f32_16x16x128_f8f6f4 v[84:87], v[4:11], v[182:189], v[84:87], v245, v245 op_sel_hi:[0,0,0]
	v_mfma_scale_f32_16x16x128_f8f6f4 v[72:75], v[12:19], v[210:217], v[72:75], v245, v245 op_sel_hi:[0,0,0]
	v_mfma_scale_f32_16x16x128_f8f6f4 v[68:71], v[4:11], v[210:217], v[68:71], v245, v245 op_sel_hi:[0,0,0]
	v_mfma_scale_f32_16x16x128_f8f6f4 v[56:59], v[12:19], v[218:225], v[56:59], v245, v245 op_sel_hi:[0,0,0]
	v_mfma_scale_f32_16x16x128_f8f6f4 v[52:55], v[4:11], v[218:225], v[52:55], v245, v245 op_sel_hi:[0,0,0]
	v_mfma_scale_f32_16x16x128_f8f6f4 v[40:43], v[12:19], v[228:235], v[40:43], v245, v245 op_sel_hi:[0,0,0]
	v_mfma_scale_f32_16x16x128_f8f6f4 v[36:39], v[4:11], v[228:235], v[36:39], v245, v245 op_sel_hi:[0,0,0]
	s_setprio 0
	s_barrier
; #define PG8_WAIT_V(n) asm volatile("s_waitcnt vmcnt(" #n ")" ::: "memory")
; #define PG8_WAIT_L(n) asm volatile("s_waitcnt lgkmcnt(" #n ")" ::: "memory")
; template <class Epi, class Sched, bool ALIGN_EPI = false, bool SP2 = false, bool FP8 = false, bool ABLK = false>
; __device__ __forceinline__ void gemm_phase(PG8_LAS unsigned char* lds, const Gemm g, const Sched& S, const Epi& E) {
;     ...
;             PG8_LDB(B0, 1, 0); PG8_LDB(B1, 1, 1); PG8_SCHED; PG8_LDA(At, 1, 0); PG8_STAGE(PG8_SA(0, 1), a2 + hstepA, voffA);
;             PG8_WAIT_V(8); PG8_WAIT_L(0); PG8_BAR; PG8_MMA(0, 0, At, B0); PG8_MMA(0, 1, At, B1); PG8_BAR; PG8_SCHED;
;             PG8_LDA(At, 1, 1); PG8_STAGE(PG8_SB(1, 0), b3, voffB); PG8_STAGE(PG8_SB(1, 1), b3 + hstep, voffB); PG8_STAGE(PG8_SA(1, 0), a3, voffA);
;             PG8_WAIT_V(8); PG8_WAIT_L(0); PG8_BAR; PG8_MMA(1, 0, At, B0); PG8_MMA(1, 1, At, B1); PG8_BAR; PG8_SCHED;
;             } else {
;             PG8_LDB(B0, 0, 0); PG8_SCHED; PG8_LDA(At, 0, 0); PG8_STAGE(PG8_SA(1, 1), a1 + hstepA, voffA);
;             PG8_WAIT_L(8); PG8_BAR; PG8_WAIT_L(0); PG8_MMA(0, 0, At, B0); PG8_BAR; PG8_SCHED;
;             PG8_LDB(B1, 0, 1); PG8_STAGE(PG8_SB(0, 0), b2, voffB);
;             PG8_BAR; PG8_WAIT_L(0); PG8_MMA(0, 1, At, B1); PG8_BAR;
;             PG8_LDA(At, 0, 1); PG8_STAGE(PG8_SA(0, 0), a2, voffA);
;             PG8_BAR; PG8_WAIT_L(0); PG8_MMA(1, 0, At, B0); PG8_BAR; PG8_SCHED;
;             PG8_STAGE(PG8_SB(0, 1), b2 + hstep, voffB);
;             PG8_WAIT_V(6); PG8_BAR; PG8_MMA(1, 1, At, B1); PG8_BAR;
;             PG8_LDB(B0, 1, 0); PG8_SCHED; PG8_LDA(At, 1, 0); PG8_STAGE(PG8_SA(0, 1), a2 + hstepA, voffA);
;             PG8_WAIT_L(8); PG8_BAR; PG8_WAIT_L(0); PG8_MMA(0, 0, At, B0); PG8_BAR; PG8_SCHED;
;             PG8_LDB(B1, 1, 1); PG8_STAGE(PG8_SB(1, 0), b3, voffB);
;             PG8_BAR; PG8_WAIT_L(0); PG8_MMA(0, 1, At, B1); PG8_BAR;
;             PG8_LDA(At, 1, 1); PG8_STAGE(PG8_SA(1, 0), a3, voffA);
;             PG8_BAR; PG8_WAIT_L(0); PG8_MMA(1, 0, At, B0); PG8_BAR; PG8_SCHED;
;             PG8_STAGE(PG8_SB(1, 1), b3 + hstep, voffB);
;             PG8_WAIT_V(6); PG8_BAR; PG8_MMA(1, 1, At, B1); PG8_BAR;
;             }
;         }
;         if constexpr (SP2) PG8_WAIT_V(0);
;         if constexpr (FP8) asm volatile("s_nop 15\n\ts_nop 15" ::: "memory");
;         if constexpr (ALIGN_EPI) { if (wr == 0) PG8_BAR; }
	s_add_i32 s73, 0, 0x18000
	s_add_i32 s74, 0, 0x1c000
	v_add_u32_e32 v16, s73, v195
	v_add_u32_e32 v32, s74, v195
	ds_read_b128 v[4:7], v16
	ds_read_b128 v[8:11], v16 offset:1024
	ds_read_b128 v[12:15], v16 offset:2048
	ds_read_b128 v[16:19], v16 offset:3072
	ds_read_b128 v[20:23], v32
	ds_read_b128 v[24:27], v32 offset:1024
	ds_read_b128 v[28:31], v32 offset:2048
	ds_read_b128 v[32:35], v32 offset:3072
	s_add_u32 s62, s62, 0x20000
	s_addc_u32 s63, s63, 0
	s_mov_b32 m0, s20
	ds_read_b128 v[182:185], v208 offset:32768
	ds_read_b128 v[186:189], v208 offset:33792
	ds_read_b128 v[210:213], v208 offset:34816
	ds_read_b128 v[214:217], v208 offset:35840
	ds_read_b128 v[218:221], v208 offset:36864
	ds_read_b128 v[222:225], v208 offset:37888
	ds_read_b128 v[228:231], v208 offset:38912
	ds_read_b128 v[232:235], v208 offset:39936
	global_load_lds_dwordx4 v168, s[62:63]
	s_mov_b32 m0, s21
	s_nop 0
	global_load_lds_dwordx4 v166, s[62:63]
	s_waitcnt vmcnt(8)
	s_waitcnt lgkmcnt(0)
	s_barrier
	s_setprio 1
	s_waitcnt lgkmcnt(0)
	v_mfma_scale_f32_16x16x128_f8f6f4 v[160:163], v[4:11], v[182:189], v[160:163], v245, v245 op_sel_hi:[0,0,0]
	v_mfma_scale_f32_16x16x128_f8f6f4 v[156:159], v[12:19], v[182:189], v[156:159], v245, v245 op_sel_hi:[0,0,0]
	v_mfma_scale_f32_16x16x128_f8f6f4 v[144:147], v[4:11], v[210:217], v[144:147], v245, v245 op_sel_hi:[0,0,0]
	v_mfma_scale_f32_16x16x128_f8f6f4 v[140:143], v[12:19], v[210:217], v[140:143], v245, v245 op_sel_hi:[0,0,0]
	v_mfma_scale_f32_16x16x128_f8f6f4 v[128:131], v[4:11], v[218:225], v[128:131], v245, v245 op_sel_hi:[0,0,0]
	v_mfma_scale_f32_16x16x128_f8f6f4 v[124:127], v[12:19], v[218:225], v[124:127], v245, v245 op_sel_hi:[0,0,0]
	v_mfma_scale_f32_16x16x128_f8f6f4 v[112:115], v[4:11], v[228:235], v[112:115], v245, v245 op_sel_hi:[0,0,0]
	v_mfma_scale_f32_16x16x128_f8f6f4 v[108:111], v[12:19], v[228:235], v[108:111], v245, v245 op_sel_hi:[0,0,0]
	s_setprio 0
	s_setprio 1
	v_mfma_scale_f32_16x16x128_f8f6f4 v[152:155], v[20:27], v[182:189], v[152:155], v245, v245 op_sel_hi:[0,0,0]
	v_mfma_scale_f32_16x16x128_f8f6f4 v[148:151], v[28:35], v[182:189], v[148:151], v245, v245 op_sel_hi:[0,0,0]
	v_mfma_scale_f32_16x16x128_f8f6f4 v[136:139], v[20:27], v[210:217], v[136:139], v245, v245 op_sel_hi:[0,0,0]
	v_mfma_scale_f32_16x16x128_f8f6f4 v[132:135], v[28:35], v[210:217], v[132:135], v245, v245 op_sel_hi:[0,0,0]
	v_mfma_scale_f32_16x16x128_f8f6f4 v[120:123], v[20:27], v[218:225], v[120:123], v245, v245 op_sel_hi:[0,0,0]
	v_mfma_scale_f32_16x16x128_f8f6f4 v[116:119], v[28:35], v[218:225], v[116:119], v245, v245 op_sel_hi:[0,0,0]
	v_mfma_scale_f32_16x16x128_f8f6f4 v[104:107], v[20:27], v[228:235], v[104:107], v245, v245 op_sel_hi:[0,0,0]
	v_mfma_scale_f32_16x16x128_f8f6f4 v[100:103], v[28:35], v[228:235], v[100:103], v245, v245 op_sel_hi:[0,0,0]
	s_setprio 0
	s_barrier
	s_add_i32 s62, s73, s17
	v_lshl_add_u64 v[174:175], v[174:175], 0, s[34:35]
	s_mov_b32 m0, s62
	ds_read_b128 v[182:185], v208 offset:49152
	ds_read_b128 v[186:189], v208 offset:50176
	ds_read_b128 v[210:213], v208 offset:51200
	ds_read_b128 v[214:217], v208 offset:52224
	ds_read_b128 v[218:221], v208 offset:53248
	ds_read_b128 v[222:225], v208 offset:54272
	ds_read_b128 v[228:231], v208 offset:55296
	ds_read_b128 v[232:235], v208 offset:56320
	global_load_lds_dwordx4 v[174:175], off
	s_add_i32 m0, s62, 0x2000
	s_add_u32 s60, s60, 0x20080
	v_lshl_add_u64 v[174:175], v[176:177], 0, s[34:35]
	s_addc_u32 s61, s61, 0
	s_add_i32 s62, s74, s17
	global_load_lds_dwordx4 v[174:175], off
	s_mov_b32 m0, s62
	s_nop 0
	global_load_lds_dwordx4 v2, s[60:61]
	s_add_i32 m0, s62, 0x2000
	s_nop 0
	global_load_lds_dwordx4 v164, s[60:61]
	v_lshl_add_u64 v[174:175], v[178:179], 0, s[34:35]
	s_mov_b32 m0, s65
	s_nop 0
	global_load_lds_dwordx4 v[174:175], off
	v_lshl_add_u64 v[174:175], v[180:181], 0, s[34:35]
	s_mov_b32 m0, s66
	s_nop 0
	global_load_lds_dwordx4 v[174:175], off
	s_waitcnt vmcnt(8)
	s_waitcnt lgkmcnt(0)
	s_barrier
	s_setprio 1
	s_waitcnt lgkmcnt(0)
	v_mfma_scale_f32_16x16x128_f8f6f4 v[96:99], v[4:11], v[182:189], v[96:99], v245, v245 op_sel_hi:[0,0,0]
	v_mfma_scale_f32_16x16x128_f8f6f4 v[92:95], v[12:19], v[182:189], v[92:95], v245, v245 op_sel_hi:[0,0,0]
	v_mfma_scale_f32_16x16x128_f8f6f4 v[80:83], v[4:11], v[210:217], v[80:83], v245, v245 op_sel_hi:[0,0,0]
	v_mfma_scale_f32_16x16x128_f8f6f4 v[76:79], v[12:19], v[210:217], v[76:79], v245, v245 op_sel_hi:[0,0,0]
	v_mfma_scale_f32_16x16x128_f8f6f4 v[64:67], v[4:11], v[218:225], v[64:67], v245, v245 op_sel_hi:[0,0,0]
	v_mfma_scale_f32_16x16x128_f8f6f4 v[60:63], v[12:19], v[218:225], v[60:63], v245, v245 op_sel_hi:[0,0,0]
	v_mfma_scale_f32_16x16x128_f8f6f4 v[48:51], v[4:11], v[228:235], v[48:51], v245, v245 op_sel_hi:[0,0,0]
	v_mfma_scale_f32_16x16x128_f8f6f4 v[44:47], v[12:19], v[228:235], v[44:47], v245, v245 op_sel_hi:[0,0,0]
	s_setprio 0
	s_setprio 1
	v_mfma_scale_f32_16x16x128_f8f6f4 v[88:91], v[20:27], v[182:189], v[88:91], v245, v245 op_sel_hi:[0,0,0]
	v_mfma_scale_f32_16x16x128_f8f6f4 v[84:87], v[28:35], v[182:189], v[84:87], v245, v245 op_sel_hi:[0,0,0]
	v_mfma_scale_f32_16x16x128_f8f6f4 v[72:75], v[20:27], v[210:217], v[72:75], v245, v245 op_sel_hi:[0,0,0]
	v_mfma_scale_f32_16x16x128_f8f6f4 v[68:71], v[28:35], v[210:217], v[68:71], v245, v245 op_sel_hi:[0,0,0]
	v_mfma_scale_f32_16x16x128_f8f6f4 v[56:59], v[20:27], v[218:225], v[56:59], v245, v245 op_sel_hi:[0,0,0]
	v_mfma_scale_f32_16x16x128_f8f6f4 v[52:55], v[28:35], v[218:225], v[52:55], v245, v245 op_sel_hi:[0,0,0]
	v_mfma_scale_f32_16x16x128_f8f6f4 v[40:43], v[20:27], v[228:235], v[40:43], v245, v245 op_sel_hi:[0,0,0]
	v_mfma_scale_f32_16x16x128_f8f6f4 v[36:39], v[28:35], v[228:235], v[36:39], v245, v245 op_sel_hi:[0,0,0]
	s_setprio 0
	s_barrier
	s_add_u32 s42, s42, 0x100
	s_addc_u32 s43, s43, 0
	s_add_u32 s70, s70, 0x100
	s_addc_u32 s71, s71, 0
	s_cmp_gt_u32 s72, 5
	s_mov_b32 s60, s72
	s_cbranch_scc0 .LBB0_1587
	s_waitcnt vmcnt(0)
	s_nop 15
	s_nop 15
	s_and_b64 vcc, exec, s[50:51]
	s_cbranch_vccz .LBB0_1590
	s_barrier

; #define PG8_STAGE(bufoff, gbase, voff) do { _Pragma("unroll") for (int _i = 0; _i < 2; ++_i) \
;         __builtin_amdgcn_global_load_lds((const unsigned*)((const char*)(gbase) + (voff)[_i]), (PG8_LAS unsigned*)(lds + (bufoff) + ldsw + _i * 8192), 16, 0, 0); } while (0)
; #define PG8_WAIT_V(n) asm volatile("s_waitcnt vmcnt(" #n ")" ::: "memory")
; #define PG8_BAR __builtin_amdgcn_s_barrier()
;   __device__ __forceinline__ bool next(int i,AttnUnit&u)const{ const int v=vcu+(i>>2)*grid; if(v>=256)return false; const int k=i&3,s=v&7; u.bh=v>>3; u.qb=(k==0)?s:(k==1)?15-s:(k==2)?16+s:31-s; return true; }
; template <class Epi, class Sched, bool ALIGN_EPI = false, bool SP2 = false, bool FP8 = false, bool ABLK = false>
; __device__ __forceinline__ void gemm_phase(PG8_LAS unsigned char* lds, const Gemm g, const Sched& S, const Epi& E) {
;     ...
;     const char* cA = (const char*)g.A + (size_t)cur.pm * tstep; const char* cB = (const char*)g.Bt + (size_t)cur.pn * tstep;
;     S.a_ready(cur);
;     if constexpr (SP2) {
;         PG8_STAGE(PG8_SB(0, 0), cB, voffB); PG8_STAGE(PG8_SB(0, 1), cB + hstep, voffB); PG8_STAGE(PG8_SA(0, 0), cA, voffA); PG8_STAGE(PG8_SA(0, 1), cA + hstepA, voffA);
;         if (wr == 1) PG8_BAR;
;         PG8_WAIT_V(2); PG8_BAR;
;         PG8_STAGE(PG8_SB(1, 0), cB + kstep, voffB); PG8_STAGE(PG8_SA(1, 0), cA + kstepA, voffA); PG8_STAGE(PG8_SB(1, 1), cB + hstep + kstep, voffB);
;         PG8_WAIT_V(0); PG8_BAR;
;     } else {
;         PG8_STAGE(PG8_SB(0, 0), cB, voffB); PG8_STAGE(PG8_SA(0, 0), cA, voffA); PG8_STAGE(PG8_SB(0, 1), cB + hstep, voffB); PG8_STAGE(PG8_SA(0, 1), cA + hstepA, voffA);
;         if (wr == 1) PG8_BAR;
;         PG8_WAIT_V(4); PG8_BAR;
;         PG8_STAGE(PG8_SB(1, 0), cB + kstep, voffB); PG8_STAGE(PG8_SA(1, 0), cA + kstepA, voffA); PG8_STAGE(PG8_SB(1, 1), cB + hstep + kstep, voffB);
;         PG8_WAIT_V(6); PG8_BAR;
;     }
;     for (;;) {
;         const bool has_next = S.next(ui + 1, nxt);
;         const char* nA = has_next ? (const char*)g.A + (size_t)nxt.pm * tstep : cA; const char* nB = has_next ? (const char*)g.Bt + (size_t)nxt.pn * tstep : cB;
.LBB0_1665:
	v_bfe_u32 v182, v10, 4, 2
	v_and_b32_e32 v1, 15, v10
	v_lshlrev_b32_e32 v11, 4, v182
	v_lshlrev_b32_e32 v10, 2, v10
	s_and_b32 s52, s40, 3
	v_lshl_or_b32 v11, v1, 6, v11
	s_lshl_b32 s40, s5, 13
	v_and_b32_e32 v10, 32, v10
	v_lshl_add_u64 v[12:13], s[62:63], 0, v[2:3]
	v_mov_b32_e32 v165, v3
	v_bitop3_b32 v20, v11, s40, v10 bitop3:0xde
	s_lshl_b32 s40, s52, 12
	v_lshl_add_u64 v[14:15], s[62:63], 0, v[164:165]
	v_mov_b32_e32 v169, v3
	v_bitop3_b32 v183, v11, s40, v10 bitop3:0xde
	s_add_i32 m0, s20, 0x18000
	v_lshl_add_u64 v[10:11], v[12:13], 0, s[34:35]
	v_lshl_add_u64 v[16:17], s[60:61], 0, v[168:169]
	v_mov_b32_e32 v167, v3
	s_lshl_b32 s66, s5, 6
	s_waitcnt vmcnt(2)
	s_barrier
	global_load_lds_dwordx4 v[10:11], off
	v_lshl_add_u64 v[10:11], v[14:15], 0, s[34:35]
	s_add_i32 m0, s20, 0x1a000
	s_add_i32 s67, s20, 0x8000
	s_add_i32 s68, s20, 0xa000
	v_lshl_add_u64 v[18:19], s[60:61], 0, v[166:167]
	global_load_lds_dwordx4 v[10:11], off
	v_lshl_add_u64 v[10:11], v[16:17], 0, s[34:35]
	s_mov_b32 m0, s67
	s_add_u32 s40, s62, 0x20080
	global_load_lds_dwordx4 v[10:11], off
	v_lshl_add_u64 v[10:11], v[18:19], 0, s[34:35]
	s_mov_b32 m0, s68
	s_addc_u32 s41, s63, 0
	global_load_lds_dwordx4 v[10:11], off
	s_add_i32 m0, s20, 0x1c000
	s_nop 0
	global_load_lds_dwordx4 v2, s[40:41]
	s_add_i32 m0, s20, 0x1e000
	s_cmpk_lt_u32 s4, 0x100
	global_load_lds_dwordx4 v164, s[40:41]
	v_lshlrev_b32_e32 v10, 13, v8
	v_and_b32_e32 v10, 0xffffc000, v10
	v_lshl_add_u32 v7, v7, 10, v10
	v_and_b32_e32 v8, 1, v8
	v_lshl_or_b32 v7, v8, 6, v7
	v_lshl_add_u32 v170, v9, 1, v7
	v_lshlrev_b32_e32 v7, 13, v4
	v_and_b32_e32 v7, 0xffffc000, v7
	s_waitcnt vmcnt(0)
	s_cselect_b64 s[50:51], -1, 0
	s_lshl_b32 s4, s5, 11
	s_lshl_b32 s5, s52, 9
	v_lshl_add_u32 v5, v5, 10, v7
	v_and_b32_e32 v4, 1, v4
	s_or_b32 s69, s5, s4
	v_lshl_or_b32 v4, v4, 6, v5
	v_readlane_b32 s4, v252, 4
	v_mov_b32_e32 v171, v3
	v_lshl_add_u32 v172, v6, 1, v4
	v_mov_b32_e32 v173, v3
	s_mov_b32 s70, 0
	v_add_u32_e32 v184, 0, v20
	v_readlane_b32 s71, v254, 46
	s_mov_b32 s72, s4
	s_barrier
	v_readlane_b32 s5, v252, 5
	s_branch .LBB0_1668

; #define PG8_STAGE(bufoff, gbase, voff) do { _Pragma("unroll") for (int _i = 0; _i < 2; ++_i) \
;         __builtin_amdgcn_global_load_lds((const unsigned*)((const char*)(gbase) + (voff)[_i]), (PG8_LAS unsigned*)(lds + (bufoff) + ldsw + _i * 8192), 16, 0, 0); } while (0)
; #define PG8_LDA(dst, b, h) do { _Pragma("unroll") for (int m = 0; m < 4; ++m) _Pragma("unroll") for (int k = 0; k < 2; ++k) dst[m][k] = *(const PG8_LAS bf16x8*)(lds + PG8_SA(b, h) + aoff + m * 2048 + k * 1024); } while (0)
; #define PG8_LDB(dst, b, h) do { _Pragma("unroll") for (int n = 0; n < 2; ++n) _Pragma("unroll") for (int k = 0; k < 2; ++k) dst[n][k] = *(const PG8_LAS bf16x8*)(lds + PG8_SB(b, h) + boff + n * 2048 + k * 1024); } while (0)
; #define PG8_WAIT_V8_UNLESS_FIRST(t) asm volatile("s_cmp_eq_u32 %0, 0\n\ts_cbranch_scc1 .Lpg8skip%=\n\ts_waitcnt vmcnt(8)\n.Lpg8skip%=:" :: "s"(t) : "scc", "memory")
; #define PG8_WAIT_L(n) asm volatile("s_waitcnt lgkmcnt(" #n ")" ::: "memory")
; #define PG8_BAR __builtin_amdgcn_s_barrier()
; #define PG8_SCHED __builtin_amdgcn_sched_barrier(0)
; template <class Epi, class Sched, bool ALIGN_EPI = false, bool SP2 = false, bool FP8 = false, bool ABLK = false>
; __device__ __forceinline__ void gemm_phase(PG8_LAS unsigned char* lds, const Gemm g, const Sched& S, const Epi& E) {
;     ...
;         for (int t = 0; t < nt; t += 2) {
;             const bool last = (t == nt - 2);
;             const char* a1 = cA + (size_t)(t + 1) * kstepA;
;             const char* a2 = last ? nA : cA + (size_t)(t + 2) * kstepA; const char* b2 = last ? nB : cB + (size_t)(t + 2) * kstep;
;             const char* a3 = a2 + kstepA; const char* b3 = b2 + kstep;
;             if (last && has_next) S.a_ready(nxt);
;             if constexpr (SP2) {
;             PG8_LDB(B0, 0, 0); PG8_LDB(B1, 0, 1); PG8_SCHED; PG8_LDA(At, 0, 0); PG8_STAGE(PG8_SA(1, 1), a1 + hstepA, voffA);
;             PG8_WAIT_V8_UNLESS_FIRST(t); PG8_WAIT_L(0); PG8_BAR; PG8_MMA(0, 0, At, B0); PG8_MMA(0, 1, At, B1); PG8_BAR; PG8_SCHED;
;             PG8_LDA(At, 0, 1); PG8_STAGE(PG8_SB(0, 0), b2, voffB); PG8_STAGE(PG8_SB(0, 1), b2 + hstep, voffB); PG8_STAGE(PG8_SA(0, 0), a2, voffA);
;             PG8_WAIT_V8_UNLESS_FIRST(t); PG8_WAIT_L(0); PG8_BAR; PG8_MMA(1, 0, At, B0); PG8_MMA(1, 1, At, B1); PG8_BAR; PG8_SCHED;
.LBB0_1671:
	s_add_i32 s75, s62, 2
	s_add_u32 s63, s60, 0xfffe0080
	s_addc_u32 s64, s61, -1
	s_add_i32 s76, 0, 0x10000
	s_cmp_eq_u32 s62, 4
	s_cselect_b32 s65, s4, s64
	s_cselect_b32 s64, s5, s63
	s_cselect_b32 s63, s53, s74
	s_cselect_b32 s62, s55, s73
	s_add_i32 s77, 0, 0x14000
	v_add_u32_e32 v4, s76, v183
	v_add_u32_e32 v8, s77, v183
	ds_read_b128 v[28:31], v4
	ds_read_b128 v[32:35], v4 offset:1024
	ds_read_b128 v[20:23], v4 offset:2048
	ds_read_b128 v[24:27], v4 offset:3072
	ds_read_b128 v[12:15], v8
	ds_read_b128 v[16:19], v8 offset:1024
	ds_read_b128 v[4:7], v8 offset:2048
	ds_read_b128 v[8:11], v8 offset:3072
	s_add_i32 m0, s20, 0xc000
	ds_read_b128 v[174:177], v184
	ds_read_b128 v[178:181], v184 offset:1024
	ds_read_b128 v[186:189], v184 offset:2048
	ds_read_b128 v[190:193], v184 offset:3072
	ds_read_b128 v[208:211], v184 offset:4096
	ds_read_b128 v[212:215], v184 offset:5120
	ds_read_b128 v[216:219], v184 offset:6144
	ds_read_b128 v[220:223], v184 offset:7168
	global_load_lds_dwordx4 v170, s[60:61]
	s_add_i32 m0, s20, 0xe000
	s_nop 0
	global_load_lds_dwordx4 v172, s[60:61]
	s_cmp_eq_u32 s75, 0
	s_cbranch_scc1 .Lpg8skip12
	s_waitcnt vmcnt(8)
.Lpg8skip12:
	s_waitcnt lgkmcnt(0)
	s_barrier
	s_setprio 1
	s_waitcnt lgkmcnt(0)
	v_mfma_scale_f32_16x16x128_f8f6f4 v[160:163], v[28:35], v[174:181], v[160:163], v245, v245 op_sel_hi:[0,0,0]
	v_mfma_scale_f32_16x16x128_f8f6f4 v[156:159], v[20:27], v[174:181], v[156:159], v245, v245 op_sel_hi:[0,0,0]
	v_mfma_scale_f32_16x16x128_f8f6f4 v[144:147], v[28:35], v[186:193], v[144:147], v245, v245 op_sel_hi:[0,0,0]
	v_mfma_scale_f32_16x16x128_f8f6f4 v[140:143], v[20:27], v[186:193], v[140:143], v245, v245 op_sel_hi:[0,0,0]
	v_mfma_scale_f32_16x16x128_f8f6f4 v[128:131], v[28:35], v[208:215], v[128:131], v245, v245 op_sel_hi:[0,0,0]
	v_mfma_scale_f32_16x16x128_f8f6f4 v[124:127], v[20:27], v[208:215], v[124:127], v245, v245 op_sel_hi:[0,0,0]
	v_mfma_scale_f32_16x16x128_f8f6f4 v[112:115], v[28:35], v[216:223], v[112:115], v245, v245 op_sel_hi:[0,0,0]
	v_mfma_scale_f32_16x16x128_f8f6f4 v[108:111], v[20:27], v[216:223], v[108:111], v245, v245 op_sel_hi:[0,0,0]
	s_setprio 0
	s_setprio 1
	v_mfma_scale_f32_16x16x128_f8f6f4 v[152:155], v[12:19], v[174:181], v[152:155], v245, v245 op_sel_hi:[0,0,0]
	v_mfma_scale_f32_16x16x128_f8f6f4 v[148:151], v[4:11], v[174:181], v[148:151], v245, v245 op_sel_hi:[0,0,0]
	v_mfma_scale_f32_16x16x128_f8f6f4 v[136:139], v[12:19], v[186:193], v[136:139], v245, v245 op_sel_hi:[0,0,0]
	v_mfma_scale_f32_16x16x128_f8f6f4 v[132:135], v[4:11], v[186:193], v[132:135], v245, v245 op_sel_hi:[0,0,0]
	v_mfma_scale_f32_16x16x128_f8f6f4 v[120:123], v[12:19], v[208:215], v[120:123], v245, v245 op_sel_hi:[0,0,0]
	v_mfma_scale_f32_16x16x128_f8f6f4 v[116:119], v[4:11], v[208:215], v[116:119], v245, v245 op_sel_hi:[0,0,0]
	v_mfma_scale_f32_16x16x128_f8f6f4 v[104:107], v[12:19], v[216:223], v[104:107], v245, v245 op_sel_hi:[0,0,0]
	v_mfma_scale_f32_16x16x128_f8f6f4 v[100:103], v[4:11], v[216:223], v[100:103], v245, v245 op_sel_hi:[0,0,0]
	s_setprio 0
	s_barrier
	s_add_i32 s76, s76, s19
	v_lshl_add_u64 v[174:175], s[62:63], 0, v[2:3]
	s_mov_b32 m0, s76
	ds_read_b128 v[186:189], v184 offset:16384
	ds_read_b128 v[190:193], v184 offset:17408
	ds_read_b128 v[208:211], v184 offset:18432
	ds_read_b128 v[212:215], v184 offset:19456
	ds_read_b128 v[216:219], v184 offset:20480
	ds_read_b128 v[220:223], v184 offset:21504
	ds_read_b128 v[228:231], v184 offset:22528
	ds_read_b128 v[232:235], v184 offset:23552
	global_load_lds_dwordx4 v2, s[62:63]
	s_add_i32 m0, s76, 0x2000
	s_add_u32 s84, s62, 0x20000
	v_lshl_add_u64 v[176:177], s[62:63], 0, v[164:165]
	s_addc_u32 s85, s63, 0
	s_add_i32 s76, s77, s19
	global_load_lds_dwordx4 v164, s[62:63]
	s_mov_b32 m0, s76
	v_lshl_add_u64 v[180:181], s[64:65], 0, v[166:167]
	global_load_lds_dwordx4 v2, s[84:85]
	s_add_i32 m0, s76, 0x2000
	s_nop 0
	global_load_lds_dwordx4 v164, s[84:85]
	v_lshl_add_u64 v[178:179], s[64:65], 0, v[168:169]
	s_mov_b32 m0, s20
	s_nop 0
	global_load_lds_dwordx4 v168, s[64:65]
	s_mov_b32 m0, s21
	s_nop 0
	global_load_lds_dwordx4 v166, s[64:65]
	s_cmp_eq_u32 s75, 0
	s_cbranch_scc1 .Lpg8skip13
	s_waitcnt vmcnt(8)
.Lpg8skip13:
	s_waitcnt lgkmcnt(0)
	s_barrier
	s_setprio 1
	s_waitcnt lgkmcnt(0)
	v_mfma_scale_f32_16x16x128_f8f6f4 v[96:99], v[28:35], v[186:193], v[96:99], v245, v245 op_sel_hi:[0,0,0]
	v_mfma_scale_f32_16x16x128_f8f6f4 v[92:95], v[20:27], v[186:193], v[92:95], v245, v245 op_sel_hi:[0,0,0]
	v_mfma_scale_f32_16x16x128_f8f6f4 v[80:83], v[28:35], v[208:215], v[80:83], v245, v245 op_sel_hi:[0,0,0]
	v_mfma_scale_f32_16x16x128_f8f6f4 v[76:79], v[20:27], v[208:215], v[76:79], v245, v245 op_sel_hi:[0,0,0]
	v_mfma_scale_f32_16x16x128_f8f6f4 v[64:67], v[28:35], v[216:223], v[64:67], v245, v245 op_sel_hi:[0,0,0]
	v_mfma_scale_f32_16x16x128_f8f6f4 v[60:63], v[20:27], v[216:223], v[60:63], v245, v245 op_sel_hi:[0,0,0]
	v_mfma_scale_f32_16x16x128_f8f6f4 v[48:51], v[28:35], v[228:235], v[48:51], v245, v245 op_sel_hi:[0,0,0]
	v_mfma_scale_f32_16x16x128_f8f6f4 v[44:47], v[20:27], v[228:235], v[44:47], v245, v245 op_sel_hi:[0,0,0]
	s_setprio 0
	s_setprio 1
	v_mfma_scale_f32_16x16x128_f8f6f4 v[88:91], v[12:19], v[186:193], v[88:91], v245, v245 op_sel_hi:[0,0,0]
	v_mfma_scale_f32_16x16x128_f8f6f4 v[84:87], v[4:11], v[186:193], v[84:87], v245, v245 op_sel_hi:[0,0,0]
	v_mfma_scale_f32_16x16x128_f8f6f4 v[72:75], v[12:19], v[208:215], v[72:75], v245, v245 op_sel_hi:[0,0,0]
	v_mfma_scale_f32_16x16x128_f8f6f4 v[68:71], v[4:11], v[208:215], v[68:71], v245, v245 op_sel_hi:[0,0,0]
	v_mfma_scale_f32_16x16x128_f8f6f4 v[56:59], v[12:19], v[216:223], v[56:59], v245, v245 op_sel_hi:[0,0,0]
	v_mfma_scale_f32_16x16x128_f8f6f4 v[52:55], v[4:11], v[216:223], v[52:55], v245, v245 op_sel_hi:[0,0,0]
	v_mfma_scale_f32_16x16x128_f8f6f4 v[40:43], v[12:19], v[228:235], v[40:43], v245, v245 op_sel_hi:[0,0,0]
	v_mfma_scale_f32_16x16x128_f8f6f4 v[36:39], v[4:11], v[228:235], v[36:39], v245, v245 op_sel_hi:[0,0,0]
	s_setprio 0
	s_barrier
; #define PG8_WAIT_V(n) asm volatile("s_waitcnt vmcnt(" #n ")" ::: "memory")
; #define PG8_WAIT_L(n) asm volatile("s_waitcnt lgkmcnt(" #n ")" ::: "memory")
; template <class Epi, class Sched, bool ALIGN_EPI = false, bool SP2 = false, bool FP8 = false, bool ABLK = false>
; __device__ __forceinline__ void gemm_phase(PG8_LAS unsigned char* lds, const Gemm g, const Sched& S, const Epi& E) {
;     ...
;             PG8_LDB(B0, 1, 0); PG8_LDB(B1, 1, 1); PG8_SCHED; PG8_LDA(At, 1, 0); PG8_STAGE(PG8_SA(0, 1), a2 + hstepA, voffA);
;             PG8_WAIT_V(8); PG8_WAIT_L(0); PG8_BAR; PG8_MMA(0, 0, At, B0); PG8_MMA(0, 1, At, B1); PG8_BAR; PG8_SCHED;
;             PG8_LDA(At, 1, 1); PG8_STAGE(PG8_SB(1, 0), b3, voffB); PG8_STAGE(PG8_SB(1, 1), b3 + hstep, voffB); PG8_STAGE(PG8_SA(1, 0), a3, voffA);
;             PG8_WAIT_V(8); PG8_WAIT_L(0); PG8_BAR; PG8_MMA(1, 0, At, B0); PG8_MMA(1, 1, At, B1); PG8_BAR; PG8_SCHED;
;             } else {
;             PG8_LDB(B0, 0, 0); PG8_SCHED; PG8_LDA(At, 0, 0); PG8_STAGE(PG8_SA(1, 1), a1 + hstepA, voffA);
;             PG8_WAIT_L(8); PG8_BAR; PG8_WAIT_L(0); PG8_MMA(0, 0, At, B0); PG8_BAR; PG8_SCHED;
;             PG8_LDB(B1, 0, 1); PG8_STAGE(PG8_SB(0, 0), b2, voffB);
;             PG8_BAR; PG8_WAIT_L(0); PG8_MMA(0, 1, At, B1); PG8_BAR;
;             PG8_LDA(At, 0, 1); PG8_STAGE(PG8_SA(0, 0), a2, voffA);
;             PG8_BAR; PG8_WAIT_L(0); PG8_MMA(1, 0, At, B0); PG8_BAR; PG8_SCHED;
;             PG8_STAGE(PG8_SB(0, 1), b2 + hstep, voffB);
;             PG8_WAIT_V(6); PG8_BAR; PG8_MMA(1, 1, At, B1); PG8_BAR;
;             PG8_LDB(B0, 1, 0); PG8_SCHED; PG8_LDA(At, 1, 0); PG8_STAGE(PG8_SA(0, 1), a2 + hstepA, voffA);
;             PG8_WAIT_L(8); PG8_BAR; PG8_WAIT_L(0); PG8_MMA(0, 0, At, B0); PG8_BAR; PG8_SCHED;
;             PG8_LDB(B1, 1, 1); PG8_STAGE(PG8_SB(1, 0), b3, voffB);
;             PG8_BAR; PG8_WAIT_L(0); PG8_MMA(0, 1, At, B1); PG8_BAR;
;             PG8_LDA(At, 1, 1); PG8_STAGE(PG8_SA(1, 0), a3, voffA);
;             PG8_BAR; PG8_WAIT_L(0); PG8_MMA(1, 0, At, B0); PG8_BAR; PG8_SCHED;
;             PG8_STAGE(PG8_SB(1, 1), b3 + hstep, voffB);
;             PG8_WAIT_V(6); PG8_BAR; PG8_MMA(1, 1, At, B1); PG8_BAR;
;             }
;         }
;         if constexpr (SP2) PG8_WAIT_V(0);
;         if constexpr (FP8) asm volatile("s_nop 15\n\ts_nop 15" ::: "memory");
;         if constexpr (ALIGN_EPI) { if (wr == 0) PG8_BAR; }
	s_add_i32 s76, 0, 0x18000
	s_add_i32 s77, 0, 0x1c000
	v_add_u32_e32 v16, s76, v183
	v_add_u32_e32 v32, s77, v183
	ds_read_b128 v[4:7], v16
	ds_read_b128 v[8:11], v16 offset:1024
	ds_read_b128 v[12:15], v16 offset:2048
	ds_read_b128 v[16:19], v16 offset:3072
	ds_read_b128 v[20:23], v32
	ds_read_b128 v[24:27], v32 offset:1024
	ds_read_b128 v[28:31], v32 offset:2048
	ds_read_b128 v[32:35], v32 offset:3072
	s_add_u32 s64, s64, 0x20000
	s_addc_u32 s65, s65, 0
	s_mov_b32 m0, s22
	ds_read_b128 v[186:189], v184 offset:32768
	ds_read_b128 v[190:193], v184 offset:33792
	ds_read_b128 v[208:211], v184 offset:34816
	ds_read_b128 v[212:215], v184 offset:35840
	ds_read_b128 v[216:219], v184 offset:36864
	ds_read_b128 v[220:223], v184 offset:37888
	ds_read_b128 v[228:231], v184 offset:38912
	ds_read_b128 v[232:235], v184 offset:39936
	global_load_lds_dwordx4 v168, s[64:65]
	s_mov_b32 m0, s23
	s_nop 0
	global_load_lds_dwordx4 v166, s[64:65]
	s_waitcnt vmcnt(8)
	s_waitcnt lgkmcnt(0)
	s_barrier
	s_setprio 1
	s_waitcnt lgkmcnt(0)
	v_mfma_scale_f32_16x16x128_f8f6f4 v[160:163], v[4:11], v[186:193], v[160:163], v245, v245 op_sel_hi:[0,0,0]
	v_mfma_scale_f32_16x16x128_f8f6f4 v[156:159], v[12:19], v[186:193], v[156:159], v245, v245 op_sel_hi:[0,0,0]
	v_mfma_scale_f32_16x16x128_f8f6f4 v[144:147], v[4:11], v[208:215], v[144:147], v245, v245 op_sel_hi:[0,0,0]
	v_mfma_scale_f32_16x16x128_f8f6f4 v[140:143], v[12:19], v[208:215], v[140:143], v245, v245 op_sel_hi:[0,0,0]
	v_mfma_scale_f32_16x16x128_f8f6f4 v[128:131], v[4:11], v[216:223], v[128:131], v245, v245 op_sel_hi:[0,0,0]
	v_mfma_scale_f32_16x16x128_f8f6f4 v[124:127], v[12:19], v[216:223], v[124:127], v245, v245 op_sel_hi:[0,0,0]
	v_mfma_scale_f32_16x16x128_f8f6f4 v[112:115], v[4:11], v[228:235], v[112:115], v245, v245 op_sel_hi:[0,0,0]
	v_mfma_scale_f32_16x16x128_f8f6f4 v[108:111], v[12:19], v[228:235], v[108:111], v245, v245 op_sel_hi:[0,0,0]
	s_setprio 0
	s_setprio 1
	v_mfma_scale_f32_16x16x128_f8f6f4 v[152:155], v[20:27], v[186:193], v[152:155], v245, v245 op_sel_hi:[0,0,0]
	v_mfma_scale_f32_16x16x128_f8f6f4 v[148:151], v[28:35], v[186:193], v[148:151], v245, v245 op_sel_hi:[0,0,0]
	v_mfma_scale_f32_16x16x128_f8f6f4 v[136:139], v[20:27], v[208:215], v[136:139], v245, v245 op_sel_hi:[0,0,0]
	v_mfma_scale_f32_16x16x128_f8f6f4 v[132:135], v[28:35], v[208:215], v[132:135], v245, v245 op_sel_hi:[0,0,0]
	v_mfma_scale_f32_16x16x128_f8f6f4 v[120:123], v[20:27], v[216:223], v[120:123], v245, v245 op_sel_hi:[0,0,0]
	v_mfma_scale_f32_16x16x128_f8f6f4 v[116:119], v[28:35], v[216:223], v[116:119], v245, v245 op_sel_hi:[0,0,0]
	v_mfma_scale_f32_16x16x128_f8f6f4 v[104:107], v[20:27], v[228:235], v[104:107], v245, v245 op_sel_hi:[0,0,0]
	v_mfma_scale_f32_16x16x128_f8f6f4 v[100:103], v[28:35], v[228:235], v[100:103], v245, v245 op_sel_hi:[0,0,0]
	s_setprio 0
	s_barrier
	s_add_i32 s64, s76, s19
	v_lshl_add_u64 v[174:175], v[174:175], 0, s[34:35]
	s_mov_b32 m0, s64
	ds_read_b128 v[186:189], v184 offset:49152
	ds_read_b128 v[190:193], v184 offset:50176
	ds_read_b128 v[208:211], v184 offset:51200
	ds_read_b128 v[212:215], v184 offset:52224
	ds_read_b128 v[216:219], v184 offset:53248
	ds_read_b128 v[220:223], v184 offset:54272
	ds_read_b128 v[228:231], v184 offset:55296
	ds_read_b128 v[232:235], v184 offset:56320
	global_load_lds_dwordx4 v[174:175], off
	s_add_i32 m0, s64, 0x2000
	s_add_u32 s62, s62, 0x20080
	v_lshl_add_u64 v[174:175], v[176:177], 0, s[34:35]
	s_addc_u32 s63, s63, 0
	s_add_i32 s64, s77, s19
	global_load_lds_dwordx4 v[174:175], off
	s_mov_b32 m0, s64
	s_nop 0
	global_load_lds_dwordx4 v2, s[62:63]
	s_add_i32 m0, s64, 0x2000
	s_nop 0
	global_load_lds_dwordx4 v164, s[62:63]
	v_lshl_add_u64 v[174:175], v[178:179], 0, s[34:35]
	s_mov_b32 m0, s67
	s_nop 0
	global_load_lds_dwordx4 v[174:175], off
	v_lshl_add_u64 v[174:175], v[180:181], 0, s[34:35]
	s_mov_b32 m0, s68
	s_nop 0
	global_load_lds_dwordx4 v[174:175], off
	s_waitcnt vmcnt(8)
	s_waitcnt lgkmcnt(0)
	s_barrier
	s_setprio 1
	s_waitcnt lgkmcnt(0)
	v_mfma_scale_f32_16x16x128_f8f6f4 v[96:99], v[4:11], v[186:193], v[96:99], v245, v245 op_sel_hi:[0,0,0]
	v_mfma_scale_f32_16x16x128_f8f6f4 v[92:95], v[12:19], v[186:193], v[92:95], v245, v245 op_sel_hi:[0,0,0]
	v_mfma_scale_f32_16x16x128_f8f6f4 v[80:83], v[4:11], v[208:215], v[80:83], v245, v245 op_sel_hi:[0,0,0]
	v_mfma_scale_f32_16x16x128_f8f6f4 v[76:79], v[12:19], v[208:215], v[76:79], v245, v245 op_sel_hi:[0,0,0]
	v_mfma_scale_f32_16x16x128_f8f6f4 v[64:67], v[4:11], v[216:223], v[64:67], v245, v245 op_sel_hi:[0,0,0]
	v_mfma_scale_f32_16x16x128_f8f6f4 v[60:63], v[12:19], v[216:223], v[60:63], v245, v245 op_sel_hi:[0,0,0]
	v_mfma_scale_f32_16x16x128_f8f6f4 v[48:51], v[4:11], v[228:235], v[48:51], v245, v245 op_sel_hi:[0,0,0]
	v_mfma_scale_f32_16x16x128_f8f6f4 v[44:47], v[12:19], v[228:235], v[44:47], v245, v245 op_sel_hi:[0,0,0]
	s_setprio 0
	s_setprio 1
	v_mfma_scale_f32_16x16x128_f8f6f4 v[88:91], v[20:27], v[186:193], v[88:91], v245, v245 op_sel_hi:[0,0,0]
	v_mfma_scale_f32_16x16x128_f8f6f4 v[84:87], v[28:35], v[186:193], v[84:87], v245, v245 op_sel_hi:[0,0,0]
	v_mfma_scale_f32_16x16x128_f8f6f4 v[72:75], v[20:27], v[208:215], v[72:75], v245, v245 op_sel_hi:[0,0,0]
	v_mfma_scale_f32_16x16x128_f8f6f4 v[68:71], v[28:35], v[208:215], v[68:71], v245, v245 op_sel_hi:[0,0,0]
	v_mfma_scale_f32_16x16x128_f8f6f4 v[56:59], v[20:27], v[216:223], v[56:59], v245, v245 op_sel_hi:[0,0,0]
	v_mfma_scale_f32_16x16x128_f8f6f4 v[52:55], v[28:35], v[216:223], v[52:55], v245, v245 op_sel_hi:[0,0,0]
	v_mfma_scale_f32_16x16x128_f8f6f4 v[40:43], v[20:27], v[228:235], v[40:43], v245, v245 op_sel_hi:[0,0,0]
	v_mfma_scale_f32_16x16x128_f8f6f4 v[36:39], v[28:35], v[228:235], v[36:39], v245, v245 op_sel_hi:[0,0,0]
	s_setprio 0
	s_barrier
	s_add_u32 s60, s60, 0x100
	s_addc_u32 s61, s61, 0
	s_add_u32 s73, s73, 0x100
	s_addc_u32 s74, s74, 0
	s_cmp_gt_u32 s75, 5
	s_mov_b32 s62, s75
	s_cbranch_scc0 .LBB0_1671
	s_waitcnt vmcnt(0)
	s_nop 15
	s_nop 15
	s_and_b64 vcc, exec, s[50:51]
	s_cbranch_vccz .LBB0_1674
	s_barrier

; #define PG8_STAGE(bufoff, gbase, voff) do { _Pragma("unroll") for (int _i = 0; _i < 2; ++_i) \
;         __builtin_amdgcn_global_load_lds((const unsigned*)((const char*)(gbase) + (voff)[_i]), (PG8_LAS unsigned*)(lds + (bufoff) + ldsw + _i * 8192), 16, 0, 0); } while (0)
; #define PG8_WAIT_V(n) asm volatile("s_waitcnt vmcnt(" #n ")" ::: "memory")
; #define PG8_BAR __builtin_amdgcn_s_barrier()
;   __device__ __forceinline__ bool next(int i,AttnUnit&u)const{ const int v=vcu+(i>>2)*grid; if(v>=256)return false; const int k=i&3,s=v&7; u.bh=v>>3; u.qb=(k==0)?s:(k==1)?15-s:(k==2)?16+s:31-s; return true; }
; template <class Epi, class Sched, bool ALIGN_EPI = false, bool SP2 = false, bool FP8 = false, bool ABLK = false>
; __device__ __forceinline__ void gemm_phase(PG8_LAS unsigned char* lds, const Gemm g, const Sched& S, const Epi& E) {
;     ...
;     const char* cA = (const char*)g.A + (size_t)cur.pm * tstep; const char* cB = (const char*)g.Bt + (size_t)cur.pn * tstep;
;     S.a_ready(cur);
;     if constexpr (SP2) {
;         PG8_STAGE(PG8_SB(0, 0), cB, voffB); PG8_STAGE(PG8_SB(0, 1), cB + hstep, voffB); PG8_STAGE(PG8_SA(0, 0), cA, voffA); PG8_STAGE(PG8_SA(0, 1), cA + hstepA, voffA);
;         if (wr == 1) PG8_BAR;
;         PG8_WAIT_V(2); PG8_BAR;
;         PG8_STAGE(PG8_SB(1, 0), cB + kstep, voffB); PG8_STAGE(PG8_SA(1, 0), cA + kstepA, voffA); PG8_STAGE(PG8_SB(1, 1), cB + hstep + kstep, voffB);
;         PG8_WAIT_V(0); PG8_BAR;
;     } else {
;         PG8_STAGE(PG8_SB(0, 0), cB, voffB); PG8_STAGE(PG8_SA(0, 0), cA, voffA); PG8_STAGE(PG8_SB(0, 1), cB + hstep, voffB); PG8_STAGE(PG8_SA(0, 1), cA + hstepA, voffA);
;         if (wr == 1) PG8_BAR;
;         PG8_WAIT_V(4); PG8_BAR;
;         PG8_STAGE(PG8_SB(1, 0), cB + kstep, voffB); PG8_STAGE(PG8_SA(1, 0), cA + kstepA, voffA); PG8_STAGE(PG8_SB(1, 1), cB + hstep + kstep, voffB);
;         PG8_WAIT_V(6); PG8_BAR;
;     }
;     for (;;) {
;         const bool has_next = S.next(ui + 1, nxt);
;         const char* nA = has_next ? (const char*)g.A + (size_t)nxt.pm * tstep : cA; const char* nB = has_next ? (const char*)g.Bt + (size_t)nxt.pn * tstep : cB;
.LBB0_1683:
	s_add_u32 s22, s40, 0xba00000
	s_addc_u32 s23, s41, 0
	v_bfe_u32 v182, v18, 4, 2
	s_add_u32 s42, s40, 0x1c200000
	v_and_b32_e32 v1, 15, v18
	v_lshlrev_b32_e32 v19, 4, v182
	v_lshlrev_b32_e32 v18, 2, v18
	s_addc_u32 s43, s41, 0
	s_and_b32 s5, s5, 3
	v_lshl_or_b32 v19, v1, 6, v19
	s_lshl_b32 s40, s4, 13
	v_and_b32_e32 v18, 32, v18
	s_add_i32 m0, s18, 0x18000
	v_lshl_add_u64 v[10:11], v[10:11], 0, s[34:35]
	s_lshl_b32 s62, s4, 6
	v_bitop3_b32 v20, v19, s40, v18 bitop3:0xde
	s_lshl_b32 s40, s5, 12
	s_waitcnt vmcnt(2)
	s_barrier
	global_load_lds_dwordx4 v[10:11], off
	v_lshl_add_u64 v[8:9], v[8:9], 0, s[34:35]
	s_add_i32 m0, s18, 0x1a000
	s_add_i32 s63, s18, 0x8000
	s_add_i32 s64, s18, 0xa000
	v_bitop3_b32 v183, v19, s40, v18 bitop3:0xde
	global_load_lds_dwordx4 v[8:9], off
	v_lshl_add_u64 v[4:5], v[4:5], 0, s[34:35]
	s_mov_b32 m0, s63
	s_add_u32 s40, s58, 0x20080
	global_load_lds_dwordx4 v[4:5], off
	v_lshl_add_u64 v[4:5], v[6:7], 0, s[34:35]
	s_mov_b32 m0, s64
	s_addc_u32 s41, s59, 0
	global_load_lds_dwordx4 v[4:5], off
	s_add_i32 m0, s18, 0x1c000
	s_nop 0
	global_load_lds_dwordx4 v2, s[40:41]
	s_add_i32 m0, s18, 0x1e000
	s_cmpk_lt_u32 s46, 0x100
	global_load_lds_dwordx4 v164, s[40:41]
	v_lshlrev_b32_e32 v4, 13, v16
	v_and_b32_e32 v4, 0xffffc000, v4
	v_lshl_add_u32 v4, v15, 10, v4
	v_and_b32_e32 v5, 1, v16
	v_lshl_or_b32 v4, v5, 6, v4
	v_lshl_add_u32 v170, v17, 1, v4
	v_lshlrev_b32_e32 v4, 13, v12
	v_and_b32_e32 v4, 0xffffc000, v4
	s_waitcnt vmcnt(0)
	s_cselect_b64 s[46:47], -1, 0
	s_lshl_b32 s4, s4, 11
	s_lshl_b32 s5, s5, 9
	v_lshl_add_u32 v4, v13, 10, v4
	v_and_b32_e32 v5, 1, v12
	s_or_b32 s65, s5, s4
	v_lshl_or_b32 v4, v5, 6, v4
	v_readlane_b32 s4, v252, 12
	v_mov_b32_e32 v171, v3
	v_lshl_add_u32 v172, v14, 1, v4
	v_mov_b32_e32 v173, v3
	s_mov_b32 s66, 0
	v_add_u32_e32 v184, 0, v20
	v_readlane_b32 s67, v254, 34
	s_mov_b32 s68, s4
	s_barrier
	v_readlane_b32 s5, v252, 13
	s_branch .LBB0_1686

; #define PG8_STAGE(bufoff, gbase, voff) do { _Pragma("unroll") for (int _i = 0; _i < 2; ++_i) \
;         __builtin_amdgcn_global_load_lds((const unsigned*)((const char*)(gbase) + (voff)[_i]), (PG8_LAS unsigned*)(lds + (bufoff) + ldsw + _i * 8192), 16, 0, 0); } while (0)
; #define PG8_LDA(dst, b, h) do { _Pragma("unroll") for (int m = 0; m < 4; ++m) _Pragma("unroll") for (int k = 0; k < 2; ++k) dst[m][k] = *(const PG8_LAS bf16x8*)(lds + PG8_SA(b, h) + aoff + m * 2048 + k * 1024); } while (0)
; #define PG8_LDB(dst, b, h) do { _Pragma("unroll") for (int n = 0; n < 2; ++n) _Pragma("unroll") for (int k = 0; k < 2; ++k) dst[n][k] = *(const PG8_LAS bf16x8*)(lds + PG8_SB(b, h) + boff + n * 2048 + k * 1024); } while (0)
; #define PG8_WAIT_V8_UNLESS_FIRST(t) asm volatile("s_cmp_eq_u32 %0, 0\n\ts_cbranch_scc1 .Lpg8skip%=\n\ts_waitcnt vmcnt(8)\n.Lpg8skip%=:" :: "s"(t) : "scc", "memory")
; #define PG8_WAIT_L(n) asm volatile("s_waitcnt lgkmcnt(" #n ")" ::: "memory")
; #define PG8_BAR __builtin_amdgcn_s_barrier()
; #define PG8_SCHED __builtin_amdgcn_sched_barrier(0)
; template <class Epi, class Sched, bool ALIGN_EPI = false, bool SP2 = false, bool FP8 = false, bool ABLK = false>
; __device__ __forceinline__ void gemm_phase(PG8_LAS unsigned char* lds, const Gemm g, const Sched& S, const Epi& E) {
;     ...
;         for (int t = 0; t < nt; t += 2) {
;             const bool last = (t == nt - 2);
;             const char* a1 = cA + (size_t)(t + 1) * kstepA;
;             const char* a2 = last ? nA : cA + (size_t)(t + 2) * kstepA; const char* b2 = last ? nB : cB + (size_t)(t + 2) * kstep;
;             const char* a3 = a2 + kstepA; const char* b3 = b2 + kstep;
;             if (last && has_next) S.a_ready(nxt);
;             if constexpr (SP2) {
;             PG8_LDB(B0, 0, 0); PG8_LDB(B1, 0, 1); PG8_SCHED; PG8_LDA(At, 0, 0); PG8_STAGE(PG8_SA(1, 1), a1 + hstepA, voffA);
;             PG8_WAIT_V8_UNLESS_FIRST(t); PG8_WAIT_L(0); PG8_BAR; PG8_MMA(0, 0, At, B0); PG8_MMA(0, 1, At, B1); PG8_BAR; PG8_SCHED;
;             PG8_LDA(At, 0, 1); PG8_STAGE(PG8_SB(0, 0), b2, voffB); PG8_STAGE(PG8_SB(0, 1), b2 + hstep, voffB); PG8_STAGE(PG8_SA(0, 0), a2, voffA);
;             PG8_WAIT_V8_UNLESS_FIRST(t); PG8_WAIT_L(0); PG8_BAR; PG8_MMA(1, 0, At, B0); PG8_MMA(1, 1, At, B1); PG8_BAR; PG8_SCHED;
.LBB0_1689:
	s_add_i32 s71, s58, 2
	s_add_u32 s59, s56, 0xfffe0080
	s_addc_u32 s60, s57, -1
	s_add_i32 s72, 0, 0x10000
	s_cmp_eq_u32 s58, 4
	s_cselect_b32 s61, s4, s60
	s_cselect_b32 s60, s5, s59
	s_cselect_b32 s59, s49, s70
	s_cselect_b32 s58, s51, s69
	s_add_i32 s73, 0, 0x14000
	v_add_u32_e32 v4, s72, v183
	v_add_u32_e32 v8, s73, v183
	ds_read_b128 v[28:31], v4
	ds_read_b128 v[32:35], v4 offset:1024
	ds_read_b128 v[20:23], v4 offset:2048
	ds_read_b128 v[24:27], v4 offset:3072
	ds_read_b128 v[12:15], v8
	ds_read_b128 v[16:19], v8 offset:1024
	ds_read_b128 v[4:7], v8 offset:2048
	ds_read_b128 v[8:11], v8 offset:3072
	s_add_i32 m0, s18, 0xc000
	ds_read_b128 v[174:177], v184
	ds_read_b128 v[178:181], v184 offset:1024
	ds_read_b128 v[186:189], v184 offset:2048
	ds_read_b128 v[190:193], v184 offset:3072
	ds_read_b128 v[208:211], v184 offset:4096
	ds_read_b128 v[212:215], v184 offset:5120
	ds_read_b128 v[216:219], v184 offset:6144
	ds_read_b128 v[220:223], v184 offset:7168
	global_load_lds_dwordx4 v170, s[56:57]
	s_add_i32 m0, s18, 0xe000
	s_nop 0
	global_load_lds_dwordx4 v172, s[56:57]
	s_cmp_eq_u32 s71, 0
	s_cbranch_scc1 .Lpg8skip14
	s_waitcnt vmcnt(8)
.Lpg8skip14:
	s_waitcnt lgkmcnt(0)
	s_barrier
	s_setprio 1
	s_waitcnt lgkmcnt(0)
	v_mfma_scale_f32_16x16x128_f8f6f4 v[160:163], v[28:35], v[174:181], v[160:163], v245, v245 op_sel_hi:[0,0,0]
	v_mfma_scale_f32_16x16x128_f8f6f4 v[156:159], v[20:27], v[174:181], v[156:159], v245, v245 op_sel_hi:[0,0,0]
	v_mfma_scale_f32_16x16x128_f8f6f4 v[144:147], v[28:35], v[186:193], v[144:147], v245, v245 op_sel_hi:[0,0,0]
	v_mfma_scale_f32_16x16x128_f8f6f4 v[140:143], v[20:27], v[186:193], v[140:143], v245, v245 op_sel_hi:[0,0,0]
	v_mfma_scale_f32_16x16x128_f8f6f4 v[128:131], v[28:35], v[208:215], v[128:131], v245, v245 op_sel_hi:[0,0,0]
	v_mfma_scale_f32_16x16x128_f8f6f4 v[124:127], v[20:27], v[208:215], v[124:127], v245, v245 op_sel_hi:[0,0,0]
	v_mfma_scale_f32_16x16x128_f8f6f4 v[112:115], v[28:35], v[216:223], v[112:115], v245, v245 op_sel_hi:[0,0,0]
	v_mfma_scale_f32_16x16x128_f8f6f4 v[108:111], v[20:27], v[216:223], v[108:111], v245, v245 op_sel_hi:[0,0,0]
	s_setprio 0
	s_setprio 1
	v_mfma_scale_f32_16x16x128_f8f6f4 v[152:155], v[12:19], v[174:181], v[152:155], v245, v245 op_sel_hi:[0,0,0]
	v_mfma_scale_f32_16x16x128_f8f6f4 v[148:151], v[4:11], v[174:181], v[148:151], v245, v245 op_sel_hi:[0,0,0]
	v_mfma_scale_f32_16x16x128_f8f6f4 v[136:139], v[12:19], v[186:193], v[136:139], v245, v245 op_sel_hi:[0,0,0]
	v_mfma_scale_f32_16x16x128_f8f6f4 v[132:135], v[4:11], v[186:193], v[132:135], v245, v245 op_sel_hi:[0,0,0]
	v_mfma_scale_f32_16x16x128_f8f6f4 v[120:123], v[12:19], v[208:215], v[120:123], v245, v245 op_sel_hi:[0,0,0]
	v_mfma_scale_f32_16x16x128_f8f6f4 v[116:119], v[4:11], v[208:215], v[116:119], v245, v245 op_sel_hi:[0,0,0]
	v_mfma_scale_f32_16x16x128_f8f6f4 v[104:107], v[12:19], v[216:223], v[104:107], v245, v245 op_sel_hi:[0,0,0]
	v_mfma_scale_f32_16x16x128_f8f6f4 v[100:103], v[4:11], v[216:223], v[100:103], v245, v245 op_sel_hi:[0,0,0]
	s_setprio 0
	s_barrier
	s_add_i32 s72, s72, s17
	v_lshl_add_u64 v[174:175], s[58:59], 0, v[2:3]
	s_mov_b32 m0, s72
	ds_read_b128 v[186:189], v184 offset:16384
	ds_read_b128 v[190:193], v184 offset:17408
	ds_read_b128 v[208:211], v184 offset:18432
	ds_read_b128 v[212:215], v184 offset:19456
	ds_read_b128 v[216:219], v184 offset:20480
	ds_read_b128 v[220:223], v184 offset:21504
	ds_read_b128 v[228:231], v184 offset:22528
	ds_read_b128 v[232:235], v184 offset:23552
	global_load_lds_dwordx4 v2, s[58:59]
	s_add_i32 m0, s72, 0x2000
	s_add_u32 s74, s58, 0x20000
	v_lshl_add_u64 v[176:177], s[58:59], 0, v[164:165]
	s_addc_u32 s75, s59, 0
	s_add_i32 s72, s73, s17
	global_load_lds_dwordx4 v164, s[58:59]
	s_mov_b32 m0, s72
	v_lshl_add_u64 v[180:181], s[60:61], 0, v[166:167]
	global_load_lds_dwordx4 v2, s[74:75]
	s_add_i32 m0, s72, 0x2000
	s_nop 0
	global_load_lds_dwordx4 v164, s[74:75]
	v_lshl_add_u64 v[178:179], s[60:61], 0, v[168:169]
	s_mov_b32 m0, s18
	s_nop 0
	global_load_lds_dwordx4 v168, s[60:61]
	s_mov_b32 m0, s19
	s_nop 0
	global_load_lds_dwordx4 v166, s[60:61]
	s_cmp_eq_u32 s71, 0
	s_cbranch_scc1 .Lpg8skip15
	s_waitcnt vmcnt(8)
.Lpg8skip15:
	s_waitcnt lgkmcnt(0)
	s_barrier
	s_setprio 1
	s_waitcnt lgkmcnt(0)
	v_mfma_scale_f32_16x16x128_f8f6f4 v[96:99], v[28:35], v[186:193], v[96:99], v245, v245 op_sel_hi:[0,0,0]
	v_mfma_scale_f32_16x16x128_f8f6f4 v[92:95], v[20:27], v[186:193], v[92:95], v245, v245 op_sel_hi:[0,0,0]
	v_mfma_scale_f32_16x16x128_f8f6f4 v[80:83], v[28:35], v[208:215], v[80:83], v245, v245 op_sel_hi:[0,0,0]
	v_mfma_scale_f32_16x16x128_f8f6f4 v[76:79], v[20:27], v[208:215], v[76:79], v245, v245 op_sel_hi:[0,0,0]
	v_mfma_scale_f32_16x16x128_f8f6f4 v[64:67], v[28:35], v[216:223], v[64:67], v245, v245 op_sel_hi:[0,0,0]
	v_mfma_scale_f32_16x16x128_f8f6f4 v[60:63], v[20:27], v[216:223], v[60:63], v245, v245 op_sel_hi:[0,0,0]
	v_mfma_scale_f32_16x16x128_f8f6f4 v[48:51], v[28:35], v[228:235], v[48:51], v245, v245 op_sel_hi:[0,0,0]
	v_mfma_scale_f32_16x16x128_f8f6f4 v[44:47], v[20:27], v[228:235], v[44:47], v245, v245 op_sel_hi:[0,0,0]
	s_setprio 0
	s_setprio 1
	v_mfma_scale_f32_16x16x128_f8f6f4 v[88:91], v[12:19], v[186:193], v[88:91], v245, v245 op_sel_hi:[0,0,0]
	v_mfma_scale_f32_16x16x128_f8f6f4 v[84:87], v[4:11], v[186:193], v[84:87], v245, v245 op_sel_hi:[0,0,0]
	v_mfma_scale_f32_16x16x128_f8f6f4 v[72:75], v[12:19], v[208:215], v[72:75], v245, v245 op_sel_hi:[0,0,0]
	v_mfma_scale_f32_16x16x128_f8f6f4 v[68:71], v[4:11], v[208:215], v[68:71], v245, v245 op_sel_hi:[0,0,0]
	v_mfma_scale_f32_16x16x128_f8f6f4 v[56:59], v[12:19], v[216:223], v[56:59], v245, v245 op_sel_hi:[0,0,0]
	v_mfma_scale_f32_16x16x128_f8f6f4 v[52:55], v[4:11], v[216:223], v[52:55], v245, v245 op_sel_hi:[0,0,0]
	v_mfma_scale_f32_16x16x128_f8f6f4 v[40:43], v[12:19], v[228:235], v[40:43], v245, v245 op_sel_hi:[0,0,0]
	v_mfma_scale_f32_16x16x128_f8f6f4 v[36:39], v[4:11], v[228:235], v[36:39], v245, v245 op_sel_hi:[0,0,0]
	s_setprio 0
	s_barrier
; #define PG8_WAIT_V(n) asm volatile("s_waitcnt vmcnt(" #n ")" ::: "memory")
; #define PG8_WAIT_L(n) asm volatile("s_waitcnt lgkmcnt(" #n ")" ::: "memory")
; template <class Epi, class Sched, bool ALIGN_EPI = false, bool SP2 = false, bool FP8 = false, bool ABLK = false>
; __device__ __forceinline__ void gemm_phase(PG8_LAS unsigned char* lds, const Gemm g, const Sched& S, const Epi& E) {
;     ...
;             PG8_LDB(B0, 1, 0); PG8_LDB(B1, 1, 1); PG8_SCHED; PG8_LDA(At, 1, 0); PG8_STAGE(PG8_SA(0, 1), a2 + hstepA, voffA);
;             PG8_WAIT_V(8); PG8_WAIT_L(0); PG8_BAR; PG8_MMA(0, 0, At, B0); PG8_MMA(0, 1, At, B1); PG8_BAR; PG8_SCHED;
;             PG8_LDA(At, 1, 1); PG8_STAGE(PG8_SB(1, 0), b3, voffB); PG8_STAGE(PG8_SB(1, 1), b3 + hstep, voffB); PG8_STAGE(PG8_SA(1, 0), a3, voffA);
;             PG8_WAIT_V(8); PG8_WAIT_L(0); PG8_BAR; PG8_MMA(1, 0, At, B0); PG8_MMA(1, 1, At, B1); PG8_BAR; PG8_SCHED;
;             } else {
;             PG8_LDB(B0, 0, 0); PG8_SCHED; PG8_LDA(At, 0, 0); PG8_STAGE(PG8_SA(1, 1), a1 + hstepA, voffA);
;             PG8_WAIT_L(8); PG8_BAR; PG8_WAIT_L(0); PG8_MMA(0, 0, At, B0); PG8_BAR; PG8_SCHED;
;             PG8_LDB(B1, 0, 1); PG8_STAGE(PG8_SB(0, 0), b2, voffB);
;             PG8_BAR; PG8_WAIT_L(0); PG8_MMA(0, 1, At, B1); PG8_BAR;
;             PG8_LDA(At, 0, 1); PG8_STAGE(PG8_SA(0, 0), a2, voffA);
;             PG8_BAR; PG8_WAIT_L(0); PG8_MMA(1, 0, At, B0); PG8_BAR; PG8_SCHED;
;             PG8_STAGE(PG8_SB(0, 1), b2 + hstep, voffB);
;             PG8_WAIT_V(6); PG8_BAR; PG8_MMA(1, 1, At, B1); PG8_BAR;
;             PG8_LDB(B0, 1, 0); PG8_SCHED; PG8_LDA(At, 1, 0); PG8_STAGE(PG8_SA(0, 1), a2 + hstepA, voffA);
;             PG8_WAIT_L(8); PG8_BAR; PG8_WAIT_L(0); PG8_MMA(0, 0, At, B0); PG8_BAR; PG8_SCHED;
;             PG8_LDB(B1, 1, 1); PG8_STAGE(PG8_SB(1, 0), b3, voffB);
;             PG8_BAR; PG8_WAIT_L(0); PG8_MMA(0, 1, At, B1); PG8_BAR;
;             PG8_LDA(At, 1, 1); PG8_STAGE(PG8_SA(1, 0), a3, voffA);
;             PG8_BAR; PG8_WAIT_L(0); PG8_MMA(1, 0, At, B0); PG8_BAR; PG8_SCHED;
;             PG8_STAGE(PG8_SB(1, 1), b3 + hstep, voffB);
;             PG8_WAIT_V(6); PG8_BAR; PG8_MMA(1, 1, At, B1); PG8_BAR;
;             }
;         }
;         if constexpr (SP2) PG8_WAIT_V(0);
;         if constexpr (FP8) asm volatile("s_nop 15\n\ts_nop 15" ::: "memory");
;         if constexpr (ALIGN_EPI) { if (wr == 0) PG8_BAR; }
	s_add_i32 s72, 0, 0x18000
	s_add_i32 s73, 0, 0x1c000
	v_add_u32_e32 v16, s72, v183
	v_add_u32_e32 v32, s73, v183
	ds_read_b128 v[4:7], v16
	ds_read_b128 v[8:11], v16 offset:1024
	ds_read_b128 v[12:15], v16 offset:2048
	ds_read_b128 v[16:19], v16 offset:3072
	ds_read_b128 v[20:23], v32
	ds_read_b128 v[24:27], v32 offset:1024
	ds_read_b128 v[28:31], v32 offset:2048
	ds_read_b128 v[32:35], v32 offset:3072
	s_add_u32 s60, s60, 0x20000
	s_addc_u32 s61, s61, 0
	s_mov_b32 m0, s20
	ds_read_b128 v[186:189], v184 offset:32768
	ds_read_b128 v[190:193], v184 offset:33792
	ds_read_b128 v[208:211], v184 offset:34816
	ds_read_b128 v[212:215], v184 offset:35840
	ds_read_b128 v[216:219], v184 offset:36864
	ds_read_b128 v[220:223], v184 offset:37888
	ds_read_b128 v[228:231], v184 offset:38912
	ds_read_b128 v[232:235], v184 offset:39936
	global_load_lds_dwordx4 v168, s[60:61]
	s_mov_b32 m0, s21
	s_nop 0
	global_load_lds_dwordx4 v166, s[60:61]
	s_waitcnt vmcnt(8)
	s_waitcnt lgkmcnt(0)
	s_barrier
	s_setprio 1
	s_waitcnt lgkmcnt(0)
	v_mfma_scale_f32_16x16x128_f8f6f4 v[160:163], v[4:11], v[186:193], v[160:163], v245, v245 op_sel_hi:[0,0,0]
	v_mfma_scale_f32_16x16x128_f8f6f4 v[156:159], v[12:19], v[186:193], v[156:159], v245, v245 op_sel_hi:[0,0,0]
	v_mfma_scale_f32_16x16x128_f8f6f4 v[144:147], v[4:11], v[208:215], v[144:147], v245, v245 op_sel_hi:[0,0,0]
	v_mfma_scale_f32_16x16x128_f8f6f4 v[140:143], v[12:19], v[208:215], v[140:143], v245, v245 op_sel_hi:[0,0,0]
	v_mfma_scale_f32_16x16x128_f8f6f4 v[128:131], v[4:11], v[216:223], v[128:131], v245, v245 op_sel_hi:[0,0,0]
	v_mfma_scale_f32_16x16x128_f8f6f4 v[124:127], v[12:19], v[216:223], v[124:127], v245, v245 op_sel_hi:[0,0,0]
	v_mfma_scale_f32_16x16x128_f8f6f4 v[112:115], v[4:11], v[228:235], v[112:115], v245, v245 op_sel_hi:[0,0,0]
	v_mfma_scale_f32_16x16x128_f8f6f4 v[108:111], v[12:19], v[228:235], v[108:111], v245, v245 op_sel_hi:[0,0,0]
	s_setprio 0
	s_setprio 1
	v_mfma_scale_f32_16x16x128_f8f6f4 v[152:155], v[20:27], v[186:193], v[152:155], v245, v245 op_sel_hi:[0,0,0]
	v_mfma_scale_f32_16x16x128_f8f6f4 v[148:151], v[28:35], v[186:193], v[148:151], v245, v245 op_sel_hi:[0,0,0]
	v_mfma_scale_f32_16x16x128_f8f6f4 v[136:139], v[20:27], v[208:215], v[136:139], v245, v245 op_sel_hi:[0,0,0]
	v_mfma_scale_f32_16x16x128_f8f6f4 v[132:135], v[28:35], v[208:215], v[132:135], v245, v245 op_sel_hi:[0,0,0]
	v_mfma_scale_f32_16x16x128_f8f6f4 v[120:123], v[20:27], v[216:223], v[120:123], v245, v245 op_sel_hi:[0,0,0]
	v_mfma_scale_f32_16x16x128_f8f6f4 v[116:119], v[28:35], v[216:223], v[116:119], v245, v245 op_sel_hi:[0,0,0]
	v_mfma_scale_f32_16x16x128_f8f6f4 v[104:107], v[20:27], v[228:235], v[104:107], v245, v245 op_sel_hi:[0,0,0]
	v_mfma_scale_f32_16x16x128_f8f6f4 v[100:103], v[28:35], v[228:235], v[100:103], v245, v245 op_sel_hi:[0,0,0]
	s_setprio 0
	s_barrier
	s_add_i32 s60, s72, s17
	v_lshl_add_u64 v[174:175], v[174:175], 0, s[34:35]
	s_mov_b32 m0, s60
	ds_read_b128 v[186:189], v184 offset:49152
	ds_read_b128 v[190:193], v184 offset:50176
	ds_read_b128 v[208:211], v184 offset:51200
	ds_read_b128 v[212:215], v184 offset:52224
	ds_read_b128 v[216:219], v184 offset:53248
	ds_read_b128 v[220:223], v184 offset:54272
	ds_read_b128 v[228:231], v184 offset:55296
	ds_read_b128 v[232:235], v184 offset:56320
	global_load_lds_dwordx4 v[174:175], off
	s_add_i32 m0, s60, 0x2000
	s_add_u32 s58, s58, 0x20080
	v_lshl_add_u64 v[174:175], v[176:177], 0, s[34:35]
	s_addc_u32 s59, s59, 0
	s_add_i32 s60, s73, s17
	global_load_lds_dwordx4 v[174:175], off
	s_mov_b32 m0, s60
	s_nop 0
	global_load_lds_dwordx4 v2, s[58:59]
	s_add_i32 m0, s60, 0x2000
	s_nop 0
	global_load_lds_dwordx4 v164, s[58:59]
	v_lshl_add_u64 v[174:175], v[178:179], 0, s[34:35]
	s_mov_b32 m0, s63
	s_nop 0
	global_load_lds_dwordx4 v[174:175], off
	v_lshl_add_u64 v[174:175], v[180:181], 0, s[34:35]
	s_mov_b32 m0, s64
	s_nop 0
	global_load_lds_dwordx4 v[174:175], off
	s_waitcnt vmcnt(8)
	s_waitcnt lgkmcnt(0)
	s_barrier
	s_setprio 1
	s_waitcnt lgkmcnt(0)
	v_mfma_scale_f32_16x16x128_f8f6f4 v[96:99], v[4:11], v[186:193], v[96:99], v245, v245 op_sel_hi:[0,0,0]
	v_mfma_scale_f32_16x16x128_f8f6f4 v[92:95], v[12:19], v[186:193], v[92:95], v245, v245 op_sel_hi:[0,0,0]
	v_mfma_scale_f32_16x16x128_f8f6f4 v[80:83], v[4:11], v[208:215], v[80:83], v245, v245 op_sel_hi:[0,0,0]
	v_mfma_scale_f32_16x16x128_f8f6f4 v[76:79], v[12:19], v[208:215], v[76:79], v245, v245 op_sel_hi:[0,0,0]
	v_mfma_scale_f32_16x16x128_f8f6f4 v[64:67], v[4:11], v[216:223], v[64:67], v245, v245 op_sel_hi:[0,0,0]
	v_mfma_scale_f32_16x16x128_f8f6f4 v[60:63], v[12:19], v[216:223], v[60:63], v245, v245 op_sel_hi:[0,0,0]
	v_mfma_scale_f32_16x16x128_f8f6f4 v[48:51], v[4:11], v[228:235], v[48:51], v245, v245 op_sel_hi:[0,0,0]
	v_mfma_scale_f32_16x16x128_f8f6f4 v[44:47], v[12:19], v[228:235], v[44:47], v245, v245 op_sel_hi:[0,0,0]
	s_setprio 0
	s_setprio 1
	v_mfma_scale_f32_16x16x128_f8f6f4 v[88:91], v[20:27], v[186:193], v[88:91], v245, v245 op_sel_hi:[0,0,0]
	v_mfma_scale_f32_16x16x128_f8f6f4 v[84:87], v[28:35], v[186:193], v[84:87], v245, v245 op_sel_hi:[0,0,0]
	v_mfma_scale_f32_16x16x128_f8f6f4 v[72:75], v[20:27], v[208:215], v[72:75], v245, v245 op_sel_hi:[0,0,0]
	v_mfma_scale_f32_16x16x128_f8f6f4 v[68:71], v[28:35], v[208:215], v[68:71], v245, v245 op_sel_hi:[0,0,0]
	v_mfma_scale_f32_16x16x128_f8f6f4 v[56:59], v[20:27], v[216:223], v[56:59], v245, v245 op_sel_hi:[0,0,0]
	v_mfma_scale_f32_16x16x128_f8f6f4 v[52:55], v[28:35], v[216:223], v[52:55], v245, v245 op_sel_hi:[0,0,0]
	v_mfma_scale_f32_16x16x128_f8f6f4 v[40:43], v[20:27], v[228:235], v[40:43], v245, v245 op_sel_hi:[0,0,0]
	v_mfma_scale_f32_16x16x128_f8f6f4 v[36:39], v[28:35], v[228:235], v[36:39], v245, v245 op_sel_hi:[0,0,0]
	s_setprio 0
	s_barrier
	s_add_u32 s56, s56, 0x100
	s_addc_u32 s57, s57, 0
	s_add_u32 s69, s69, 0x100
	s_addc_u32 s70, s70, 0
	s_cmp_gt_u32 s71, 5
	s_mov_b32 s58, s71
	s_cbranch_scc0 .LBB0_1689
	s_waitcnt vmcnt(0)
	s_nop 15
	s_nop 15
	s_and_b64 vcc, exec, s[46:47]
	s_cbranch_vccz .LBB0_1692
	s_barrier

; #define PG8_STAGE(bufoff, gbase, voff) do { _Pragma("unroll") for (int _i = 0; _i < 2; ++_i) \
;         __builtin_amdgcn_global_load_lds((const unsigned*)((const char*)(gbase) + (voff)[_i]), (PG8_LAS unsigned*)(lds + (bufoff) + ldsw + _i * 8192), 16, 0, 0); } while (0)
; #define PG8_WAIT_V(n) asm volatile("s_waitcnt vmcnt(" #n ")" ::: "memory")
; #define PG8_BAR __builtin_amdgcn_s_barrier()
;   __device__ __forceinline__ bool next(int i,AttnUnit&u)const{ const int v=vcu+(i>>2)*grid; if(v>=256)return false; const int k=i&3,s=v&7; u.bh=v>>3; u.qb=(k==0)?s:(k==1)?15-s:(k==2)?16+s:31-s; return true; }
; template <class Epi, class Sched, bool ALIGN_EPI = false, bool SP2 = false, bool FP8 = false, bool ABLK = false>
; __device__ __forceinline__ void gemm_phase(PG8_LAS unsigned char* lds, const Gemm g, const Sched& S, const Epi& E) {
;     ...
;     const char* cA = (const char*)g.A + (size_t)cur.pm * tstep; const char* cB = (const char*)g.Bt + (size_t)cur.pn * tstep;
;     S.a_ready(cur);
;     if constexpr (SP2) {
;         PG8_STAGE(PG8_SB(0, 0), cB, voffB); PG8_STAGE(PG8_SB(0, 1), cB + hstep, voffB); PG8_STAGE(PG8_SA(0, 0), cA, voffA); PG8_STAGE(PG8_SA(0, 1), cA + hstepA, voffA);
;         if (wr == 1) PG8_BAR;
;         PG8_WAIT_V(2); PG8_BAR;
;         PG8_STAGE(PG8_SB(1, 0), cB + kstep, voffB); PG8_STAGE(PG8_SA(1, 0), cA + kstepA, voffA); PG8_STAGE(PG8_SB(1, 1), cB + hstep + kstep, voffB);
;         PG8_WAIT_V(0); PG8_BAR;
;     } else {
;         PG8_STAGE(PG8_SB(0, 0), cB, voffB); PG8_STAGE(PG8_SA(0, 0), cA, voffA); PG8_STAGE(PG8_SB(0, 1), cB + hstep, voffB); PG8_STAGE(PG8_SA(0, 1), cA + hstepA, voffA);
;         if (wr == 1) PG8_BAR;
;         PG8_WAIT_V(4); PG8_BAR;
;         PG8_STAGE(PG8_SB(1, 0), cB + kstep, voffB); PG8_STAGE(PG8_SA(1, 0), cA + kstepA, voffA); PG8_STAGE(PG8_SB(1, 1), cB + hstep + kstep, voffB);
;         PG8_WAIT_V(6); PG8_BAR;
;     }
;     for (;;) {
;         const bool has_next = S.next(ui + 1, nxt);
;         const char* nA = has_next ? (const char*)g.A + (size_t)nxt.pm * tstep : cA; const char* nB = has_next ? (const char*)g.Bt + (size_t)nxt.pn * tstep : cB;
.LBB0_1699:
	v_bfe_u32 v168, v10, 4, 2
	v_and_b32_e32 v1, 15, v10
	v_lshlrev_b32_e32 v11, 4, v168
	v_lshlrev_b32_e32 v10, 2, v10
	s_and_b32 s50, s40, 3
	v_lshl_or_b32 v11, v1, 6, v11
	s_lshl_b32 s40, s5, 13
	v_and_b32_e32 v10, 32, v10
	v_lshl_add_u64 v[12:13], s[60:61], 0, v[2:3]
	v_mov_b32_e32 v157, v3
	v_bitop3_b32 v20, v11, s40, v10 bitop3:0xde
	s_lshl_b32 s40, s50, 12
	v_lshl_add_u64 v[14:15], s[60:61], 0, v[156:157]
	v_mov_b32_e32 v161, v3
	v_bitop3_b32 v169, v11, s40, v10 bitop3:0xde
	s_add_i32 m0, s20, 0x18000
	v_lshl_add_u64 v[10:11], v[12:13], 0, s[34:35]
	v_lshl_add_u64 v[16:17], s[58:59], 0, v[160:161]
	v_mov_b32_e32 v159, v3
	s_lshl_b32 s64, s5, 6
	s_waitcnt vmcnt(2)
	s_barrier
	global_load_lds_dwordx4 v[10:11], off
	v_lshl_add_u64 v[10:11], v[14:15], 0, s[34:35]
	s_add_i32 m0, s20, 0x1a000
	s_add_i32 s65, s20, 0x8000
	s_add_i32 s66, s20, 0xa000
	v_lshl_add_u64 v[18:19], s[58:59], 0, v[158:159]
	global_load_lds_dwordx4 v[10:11], off
	v_lshl_add_u64 v[10:11], v[16:17], 0, s[34:35]
	s_mov_b32 m0, s65
	s_add_u32 s40, s60, 0x40080
	global_load_lds_dwordx4 v[10:11], off
	v_lshl_add_u64 v[10:11], v[18:19], 0, s[34:35]
	s_mov_b32 m0, s66
	s_addc_u32 s41, s61, 0
	global_load_lds_dwordx4 v[10:11], off
	s_add_i32 m0, s20, 0x1c000
	s_nop 0
	global_load_lds_dwordx4 v2, s[40:41]
	s_add_i32 m0, s20, 0x1e000
	s_cmpk_lt_u32 s4, 0x100
	global_load_lds_dwordx4 v156, s[40:41]
	v_lshlrev_b32_e32 v10, 14, v8
	v_and_b32_e32 v10, 0xffff8000, v10
	v_lshl_add_u32 v7, v7, 11, v10
	v_and_b32_e32 v8, 1, v8
	v_lshl_or_b32 v7, v8, 6, v7
	v_lshl_add_u32 v162, v9, 1, v7
	v_lshlrev_b32_e32 v7, 14, v4
	v_and_b32_e32 v7, 0xffff8000, v7
	s_waitcnt vmcnt(0)
	s_cselect_b64 s[48:49], -1, 0
	s_lshl_b32 s4, s5, 11
	s_lshl_b32 s5, s50, 9
	v_lshl_add_u32 v5, v5, 11, v7
	v_and_b32_e32 v4, 1, v4
	s_or_b32 s67, s5, s4
	v_lshl_or_b32 v4, v4, 6, v5
	v_readlane_b32 s4, v252, 8
	v_mov_b32_e32 v163, v3
	v_lshl_add_u32 v164, v6, 1, v4
	v_mov_b32_e32 v165, v3
	s_mov_b32 s68, 0
	v_add_u32_e32 v170, 0, v20
	v_readlane_b32 s69, v254, 58
	s_mov_b32 s70, s4
	s_barrier
	v_readlane_b32 s5, v252, 9
	s_branch .LBB0_1702

; #define PG8_STAGE(bufoff, gbase, voff) do { _Pragma("unroll") for (int _i = 0; _i < 2; ++_i) \
;         __builtin_amdgcn_global_load_lds((const unsigned*)((const char*)(gbase) + (voff)[_i]), (PG8_LAS unsigned*)(lds + (bufoff) + ldsw + _i * 8192), 16, 0, 0); } while (0)
; #define PG8_LDA(dst, b, h) do { _Pragma("unroll") for (int m = 0; m < 4; ++m) _Pragma("unroll") for (int k = 0; k < 2; ++k) dst[m][k] = *(const PG8_LAS bf16x8*)(lds + PG8_SA(b, h) + aoff + m * 2048 + k * 1024); } while (0)
; #define PG8_WAIT_V(n) asm volatile("s_waitcnt vmcnt(" #n ")" ::: "memory")
; #define PG8_WAIT_L(n) asm volatile("s_waitcnt lgkmcnt(" #n ")" ::: "memory")
; #define PG8_BAR __builtin_amdgcn_s_barrier()
; template <class Epi, class Sched, bool ALIGN_EPI = false, bool SP2 = false, bool FP8 = false, bool ABLK = false>
; __device__ __forceinline__ void gemm_phase(PG8_LAS unsigned char* lds, const Gemm g, const Sched& S, const Epi& E) {
;     ...
;             const bool last = (t == nt - 2);
;             const char* a1 = cA + (size_t)(t + 1) * kstepA;
;             const char* a2 = last ? nA : cA + (size_t)(t + 2) * kstepA; const char* b2 = last ? nB : cB + (size_t)(t + 2) * kstep;
;             const char* a3 = a2 + kstepA; const char* b3 = b2 + kstep;
;             if (last && has_next) S.a_ready(nxt);
;             if constexpr (SP2) {
;             PG8_LDB(B0, 0, 0); PG8_LDB(B1, 0, 1); PG8_SCHED; PG8_LDA(At, 0, 0); PG8_STAGE(PG8_SA(1, 1), a1 + hstepA, voffA);
;             PG8_WAIT_V8_UNLESS_FIRST(t); PG8_WAIT_L(0); PG8_BAR; PG8_MMA(0, 0, At, B0); PG8_MMA(0, 1, At, B1); PG8_BAR; PG8_SCHED;
;             PG8_LDA(At, 0, 1); PG8_STAGE(PG8_SB(0, 0), b2, voffB); PG8_STAGE(PG8_SB(0, 1), b2 + hstep, voffB); PG8_STAGE(PG8_SA(0, 0), a2, voffA);
;             PG8_WAIT_V8_UNLESS_FIRST(t); PG8_WAIT_L(0); PG8_BAR; PG8_MMA(1, 0, At, B0); PG8_MMA(1, 1, At, B1); PG8_BAR; PG8_SCHED;
;             PG8_LDB(B0, 1, 0); PG8_LDB(B1, 1, 1); PG8_SCHED; PG8_LDA(At, 1, 0); PG8_STAGE(PG8_SA(0, 1), a2 + hstepA, voffA);
;             PG8_WAIT_V(8); PG8_WAIT_L(0); PG8_BAR; PG8_MMA(0, 0, At, B0); PG8_MMA(0, 1, At, B1); PG8_BAR; PG8_SCHED;
;             PG8_LDA(At, 1, 1); PG8_STAGE(PG8_SB(1, 0), b3, voffB); PG8_STAGE(PG8_SB(1, 1), b3 + hstep, voffB); PG8_STAGE(PG8_SA(1, 0), a3, voffA);
;             PG8_WAIT_V(8); PG8_WAIT_L(0); PG8_BAR; PG8_MMA(1, 0, At, B0); PG8_MMA(1, 1, At, B1); PG8_BAR; PG8_SCHED;
.LBB0_1709:
	s_add_i32 s73, s60, 2
	s_add_u32 s61, s58, 0xfffc0080
	s_addc_u32 s62, s59, -1
	s_add_i32 s74, 0, 0x10000
	s_cmp_eq_u32 s60, 12
	s_cselect_b32 s63, s4, s62
	s_cselect_b32 s62, s5, s61
	s_cselect_b32 s61, s51, s72
	s_cselect_b32 s60, s53, s71
	s_add_i32 s76, 0, 0x14000
	v_add_u32_e32 v144, s74, v169
	v_add_u32_e32 v166, s76, v169
	ds_read_b128 v[124:127], v144
	ds_read_b128 v[136:139], v144 offset:1024
	ds_read_b128 v[140:143], v144 offset:2048
	ds_read_b128 v[144:147], v144 offset:3072
	ds_read_b128 v[148:151], v166
	ds_read_b128 v[152:155], v166 offset:1024
	ds_read_b128 v[172:175], v166 offset:2048
	ds_read_b128 v[176:179], v166 offset:3072
	s_add_i32 m0, s20, 0xc000
	ds_read_b128 v[180:183], v170
	ds_read_b128 v[184:187], v170 offset:1024
	ds_read_b128 v[188:191], v170 offset:2048
	ds_read_b128 v[192:195], v170 offset:3072
	ds_read_b128 v[208:211], v170 offset:4096
	ds_read_b128 v[212:215], v170 offset:5120
	ds_read_b128 v[216:219], v170 offset:6144
	ds_read_b128 v[220:223], v170 offset:7168
	global_load_lds_dwordx4 v162, s[58:59]
	s_add_i32 m0, s20, 0xe000
	s_nop 0
	global_load_lds_dwordx4 v164, s[58:59]
	s_cmp_eq_u32 s73, 0
	s_cbranch_scc1 .Lpg8skip16
	s_waitcnt vmcnt(8)
.Lpg8skip16:
	s_waitcnt lgkmcnt(0)
	s_barrier
	s_setprio 1
	s_waitcnt lgkmcnt(0)
	v_mfma_f32_16x16x32_bf16 v[132:135], v[124:127], v[180:183], v[132:135]
	v_mfma_f32_16x16x32_bf16 v[128:131], v[140:143], v[180:183], v[128:131]
	v_mfma_f32_16x16x32_bf16 v[112:115], v[124:127], v[188:191], v[112:115]
	v_mfma_f32_16x16x32_bf16 v[104:107], v[140:143], v[188:191], v[104:107]
	v_mfma_f32_16x16x32_bf16 v[96:99], v[124:127], v[208:211], v[96:99]
	v_mfma_f32_16x16x32_bf16 v[88:91], v[140:143], v[208:211], v[88:91]
	v_mfma_f32_16x16x32_bf16 v[80:83], v[124:127], v[216:219], v[80:83]
	v_mfma_f32_16x16x32_bf16 v[72:75], v[140:143], v[216:219], v[72:75]
	v_mfma_f32_16x16x32_bf16 v[132:135], v[136:139], v[184:187], v[132:135]
	v_mfma_f32_16x16x32_bf16 v[128:131], v[144:147], v[184:187], v[128:131]
	v_mfma_f32_16x16x32_bf16 v[112:115], v[136:139], v[192:195], v[112:115]
	v_mfma_f32_16x16x32_bf16 v[104:107], v[144:147], v[192:195], v[104:107]
	v_mfma_f32_16x16x32_bf16 v[96:99], v[136:139], v[212:215], v[96:99]
	v_mfma_f32_16x16x32_bf16 v[88:91], v[144:147], v[212:215], v[88:91]
	v_mfma_f32_16x16x32_bf16 v[80:83], v[136:139], v[220:223], v[80:83]
	v_mfma_f32_16x16x32_bf16 v[72:75], v[144:147], v[220:223], v[72:75]
	s_setprio 0
	s_setprio 1
	v_mfma_f32_16x16x32_bf16 v[120:123], v[148:151], v[180:183], v[120:123]
	v_mfma_f32_16x16x32_bf16 v[116:119], v[172:175], v[180:183], v[116:119]
	v_mfma_f32_16x16x32_bf16 v[108:111], v[148:151], v[188:191], v[108:111]
	v_mfma_f32_16x16x32_bf16 v[100:103], v[172:175], v[188:191], v[100:103]
	v_mfma_f32_16x16x32_bf16 v[92:95], v[148:151], v[208:211], v[92:95]
	v_mfma_f32_16x16x32_bf16 v[84:87], v[172:175], v[208:211], v[84:87]
	v_mfma_f32_16x16x32_bf16 v[76:79], v[148:151], v[216:219], v[76:79]
	v_mfma_f32_16x16x32_bf16 v[68:71], v[172:175], v[216:219], v[68:71]
	v_mfma_f32_16x16x32_bf16 v[120:123], v[152:155], v[184:187], v[120:123]
	v_mfma_f32_16x16x32_bf16 v[116:119], v[176:179], v[184:187], v[116:119]
	v_mfma_f32_16x16x32_bf16 v[108:111], v[152:155], v[192:195], v[108:111]
	v_mfma_f32_16x16x32_bf16 v[100:103], v[176:179], v[192:195], v[100:103]
	v_mfma_f32_16x16x32_bf16 v[92:95], v[152:155], v[212:215], v[92:95]
	v_mfma_f32_16x16x32_bf16 v[84:87], v[176:179], v[212:215], v[84:87]
	v_mfma_f32_16x16x32_bf16 v[76:79], v[152:155], v[220:223], v[76:79]
	v_mfma_f32_16x16x32_bf16 v[68:71], v[176:179], v[220:223], v[68:71]
	s_setprio 0
	s_barrier
	s_add_i32 s74, s74, s19
	v_lshl_add_u64 v[166:167], s[60:61], 0, v[2:3]
	s_mov_b32 m0, s74
	ds_read_b128 v[180:183], v170 offset:16384
	ds_read_b128 v[184:187], v170 offset:17408
	ds_read_b128 v[188:191], v170 offset:18432
	ds_read_b128 v[192:195], v170 offset:19456
	ds_read_b128 v[208:211], v170 offset:20480
	ds_read_b128 v[212:215], v170 offset:21504
	ds_read_b128 v[216:219], v170 offset:22528
	ds_read_b128 v[220:223], v170 offset:23552
	global_load_lds_dwordx4 v2, s[60:61]
	s_add_i32 m0, s74, 0x2000
	s_add_u32 s74, s60, 0x40000
	v_lshl_add_u64 v[204:205], s[60:61], 0, v[156:157]
	s_addc_u32 s75, s61, 0
	s_add_i32 s76, s76, s19
	global_load_lds_dwordx4 v156, s[60:61]
	s_mov_b32 m0, s76
	v_lshl_add_u64 v[224:225], s[62:63], 0, v[158:159]
	global_load_lds_dwordx4 v2, s[74:75]
	s_add_i32 m0, s76, 0x2000
	s_nop 0
	global_load_lds_dwordx4 v156, s[74:75]
	v_lshl_add_u64 v[206:207], s[62:63], 0, v[160:161]
	s_mov_b32 m0, s20
	s_nop 0
	global_load_lds_dwordx4 v160, s[62:63]
	s_mov_b32 m0, s21
	s_nop 0
	global_load_lds_dwordx4 v158, s[62:63]
	s_cmp_eq_u32 s73, 0
	s_cbranch_scc1 .Lpg8skip17
	s_waitcnt vmcnt(8)
; #define PG8_STAGE(bufoff, gbase, voff) do { _Pragma("unroll") for (int _i = 0; _i < 2; ++_i) \
;         __builtin_amdgcn_global_load_lds((const unsigned*)((const char*)(gbase) + (voff)[_i]), (PG8_LAS unsigned*)(lds + (bufoff) + ldsw + _i * 8192), 16, 0, 0); } while (0)
; #define PG8_LDA(dst, b, h) do { _Pragma("unroll") for (int m = 0; m < 4; ++m) _Pragma("unroll") for (int k = 0; k < 2; ++k) dst[m][k] = *(const PG8_LAS bf16x8*)(lds + PG8_SA(b, h) + aoff + m * 2048 + k * 1024); } while (0)
; #define PG8_LDB(dst, b, h) do { _Pragma("unroll") for (int n = 0; n < 2; ++n) _Pragma("unroll") for (int k = 0; k < 2; ++k) dst[n][k] = *(const PG8_LAS bf16x8*)(lds + PG8_SB(b, h) + boff + n * 2048 + k * 1024); } while (0)
; #define PG8_WAIT_V(n) asm volatile("s_waitcnt vmcnt(" #n ")" ::: "memory")
; #define PG8_WAIT_V8_UNLESS_FIRST(t) asm volatile("s_cmp_eq_u32 %0, 0\n\ts_cbranch_scc1 .Lpg8skip%=\n\ts_waitcnt vmcnt(8)\n.Lpg8skip%=:" :: "s"(t) : "scc", "memory")
; #define PG8_WAIT_L(n) asm volatile("s_waitcnt lgkmcnt(" #n ")" ::: "memory")
; #define PG8_BAR __builtin_amdgcn_s_barrier()
; template <class Epi, class Sched, bool ALIGN_EPI = false, bool SP2 = false, bool FP8 = false, bool ABLK = false>
; __device__ __forceinline__ void gemm_phase(PG8_LAS unsigned char* lds, const Gemm g, const Sched& S, const Epi& E) {
;     ...
;             PG8_LDB(B0, 0, 0); PG8_LDB(B1, 0, 1); PG8_SCHED; PG8_LDA(At, 0, 0); PG8_STAGE(PG8_SA(1, 1), a1 + hstepA, voffA);
;             PG8_WAIT_V8_UNLESS_FIRST(t); PG8_WAIT_L(0); PG8_BAR; PG8_MMA(0, 0, At, B0); PG8_MMA(0, 1, At, B1); PG8_BAR; PG8_SCHED;
;             PG8_LDA(At, 0, 1); PG8_STAGE(PG8_SB(0, 0), b2, voffB); PG8_STAGE(PG8_SB(0, 1), b2 + hstep, voffB); PG8_STAGE(PG8_SA(0, 0), a2, voffA);
;             PG8_WAIT_V8_UNLESS_FIRST(t); PG8_WAIT_L(0); PG8_BAR; PG8_MMA(1, 0, At, B0); PG8_MMA(1, 1, At, B1); PG8_BAR; PG8_SCHED;
;             PG8_LDB(B0, 1, 0); PG8_LDB(B1, 1, 1); PG8_SCHED; PG8_LDA(At, 1, 0); PG8_STAGE(PG8_SA(0, 1), a2 + hstepA, voffA);
;             PG8_WAIT_V(8); PG8_WAIT_L(0); PG8_BAR; PG8_MMA(0, 0, At, B0); PG8_MMA(0, 1, At, B1); PG8_BAR; PG8_SCHED;
;             PG8_LDA(At, 1, 1); PG8_STAGE(PG8_SB(1, 0), b3, voffB); PG8_STAGE(PG8_SB(1, 1), b3 + hstep, voffB); PG8_STAGE(PG8_SA(1, 0), a3, voffA);
;             PG8_WAIT_V(8); PG8_WAIT_L(0); PG8_BAR; PG8_MMA(1, 0, At, B0); PG8_MMA(1, 1, At, B1); PG8_BAR; PG8_SCHED;
.Lpg8skip17:
	s_waitcnt lgkmcnt(0)
	s_barrier
	s_setprio 1
	s_waitcnt lgkmcnt(0)
	v_mfma_f32_16x16x32_bf16 v[64:67], v[124:127], v[180:183], v[64:67]
	v_mfma_f32_16x16x32_bf16 v[56:59], v[140:143], v[180:183], v[56:59]
	v_mfma_f32_16x16x32_bf16 v[48:51], v[124:127], v[188:191], v[48:51]
	v_mfma_f32_16x16x32_bf16 v[40:43], v[140:143], v[188:191], v[40:43]
	v_mfma_f32_16x16x32_bf16 v[32:35], v[124:127], v[208:211], v[32:35]
	v_mfma_f32_16x16x32_bf16 v[24:27], v[140:143], v[208:211], v[24:27]
	v_mfma_f32_16x16x32_bf16 v[16:19], v[124:127], v[216:219], v[16:19]
	v_mfma_f32_16x16x32_bf16 v[8:11], v[140:143], v[216:219], v[8:11]
	v_mfma_f32_16x16x32_bf16 v[64:67], v[136:139], v[184:187], v[64:67]
	v_mfma_f32_16x16x32_bf16 v[56:59], v[144:147], v[184:187], v[56:59]
	v_mfma_f32_16x16x32_bf16 v[48:51], v[136:139], v[192:195], v[48:51]
	v_mfma_f32_16x16x32_bf16 v[40:43], v[144:147], v[192:195], v[40:43]
	v_mfma_f32_16x16x32_bf16 v[32:35], v[136:139], v[212:215], v[32:35]
	v_mfma_f32_16x16x32_bf16 v[24:27], v[144:147], v[212:215], v[24:27]
	v_mfma_f32_16x16x32_bf16 v[16:19], v[136:139], v[220:223], v[16:19]
	v_mfma_f32_16x16x32_bf16 v[8:11], v[144:147], v[220:223], v[8:11]
	s_setprio 0
	s_setprio 1
	v_mfma_f32_16x16x32_bf16 v[60:63], v[148:151], v[180:183], v[60:63]
	v_mfma_f32_16x16x32_bf16 v[52:55], v[172:175], v[180:183], v[52:55]
	v_mfma_f32_16x16x32_bf16 v[44:47], v[148:151], v[188:191], v[44:47]
	v_mfma_f32_16x16x32_bf16 v[36:39], v[172:175], v[188:191], v[36:39]
	v_mfma_f32_16x16x32_bf16 v[28:31], v[148:151], v[208:211], v[28:31]
	v_mfma_f32_16x16x32_bf16 v[20:23], v[172:175], v[208:211], v[20:23]
	v_mfma_f32_16x16x32_bf16 v[12:15], v[148:151], v[216:219], v[12:15]
	v_mfma_f32_16x16x32_bf16 v[4:7], v[172:175], v[216:219], v[4:7]
	v_mfma_f32_16x16x32_bf16 v[60:63], v[152:155], v[184:187], v[60:63]
	v_mfma_f32_16x16x32_bf16 v[52:55], v[176:179], v[184:187], v[52:55]
	v_mfma_f32_16x16x32_bf16 v[44:47], v[152:155], v[192:195], v[44:47]
	v_mfma_f32_16x16x32_bf16 v[36:39], v[176:179], v[192:195], v[36:39]
	v_mfma_f32_16x16x32_bf16 v[28:31], v[152:155], v[212:215], v[28:31]
	v_mfma_f32_16x16x32_bf16 v[20:23], v[176:179], v[212:215], v[20:23]
	v_mfma_f32_16x16x32_bf16 v[12:15], v[152:155], v[220:223], v[12:15]
	v_mfma_f32_16x16x32_bf16 v[4:7], v[176:179], v[220:223], v[4:7]
	s_setprio 0
	s_barrier
	s_add_i32 s74, 0, 0x18000
	s_add_i32 s75, 0, 0x1c000
	v_add_u32_e32 v144, s74, v169
	v_add_u32_e32 v171, s75, v169
	ds_read_b128 v[124:127], v144
	ds_read_b128 v[136:139], v144 offset:1024
	ds_read_b128 v[140:143], v144 offset:2048
	ds_read_b128 v[144:147], v144 offset:3072
	ds_read_b128 v[148:151], v171
	ds_read_b128 v[152:155], v171 offset:1024
	ds_read_b128 v[172:175], v171 offset:2048
	ds_read_b128 v[176:179], v171 offset:3072
	s_add_u32 s62, s62, 0x40000
	s_addc_u32 s63, s63, 0
	s_mov_b32 m0, s22
	ds_read_b128 v[180:183], v170 offset:32768
	ds_read_b128 v[184:187], v170 offset:33792
	ds_read_b128 v[188:191], v170 offset:34816
	ds_read_b128 v[192:195], v170 offset:35840
	ds_read_b128 v[208:211], v170 offset:36864
	ds_read_b128 v[212:215], v170 offset:37888
	ds_read_b128 v[216:219], v170 offset:38912
	ds_read_b128 v[220:223], v170 offset:39936
	global_load_lds_dwordx4 v160, s[62:63]
	s_mov_b32 m0, s23
	s_nop 0
	global_load_lds_dwordx4 v158, s[62:63]
	s_waitcnt vmcnt(8)
	s_waitcnt lgkmcnt(0)
	s_barrier
	s_setprio 1
	s_waitcnt lgkmcnt(0)
	v_mfma_f32_16x16x32_bf16 v[132:135], v[124:127], v[180:183], v[132:135]
	v_mfma_f32_16x16x32_bf16 v[128:131], v[140:143], v[180:183], v[128:131]
	v_mfma_f32_16x16x32_bf16 v[112:115], v[124:127], v[188:191], v[112:115]
	v_mfma_f32_16x16x32_bf16 v[104:107], v[140:143], v[188:191], v[104:107]
	v_mfma_f32_16x16x32_bf16 v[96:99], v[124:127], v[208:211], v[96:99]
	v_mfma_f32_16x16x32_bf16 v[88:91], v[140:143], v[208:211], v[88:91]
	v_mfma_f32_16x16x32_bf16 v[80:83], v[124:127], v[216:219], v[80:83]
	v_mfma_f32_16x16x32_bf16 v[72:75], v[140:143], v[216:219], v[72:75]
	v_mfma_f32_16x16x32_bf16 v[132:135], v[136:139], v[184:187], v[132:135]
	v_mfma_f32_16x16x32_bf16 v[128:131], v[144:147], v[184:187], v[128:131]
	v_mfma_f32_16x16x32_bf16 v[112:115], v[136:139], v[192:195], v[112:115]
	v_mfma_f32_16x16x32_bf16 v[104:107], v[144:147], v[192:195], v[104:107]
	v_mfma_f32_16x16x32_bf16 v[96:99], v[136:139], v[212:215], v[96:99]
	v_mfma_f32_16x16x32_bf16 v[88:91], v[144:147], v[212:215], v[88:91]
	v_mfma_f32_16x16x32_bf16 v[80:83], v[136:139], v[220:223], v[80:83]
	v_mfma_f32_16x16x32_bf16 v[72:75], v[144:147], v[220:223], v[72:75]
	s_setprio 0
	s_setprio 1
	v_mfma_f32_16x16x32_bf16 v[120:123], v[148:151], v[180:183], v[120:123]
	v_mfma_f32_16x16x32_bf16 v[116:119], v[172:175], v[180:183], v[116:119]
	v_mfma_f32_16x16x32_bf16 v[108:111], v[148:151], v[188:191], v[108:111]
	v_mfma_f32_16x16x32_bf16 v[100:103], v[172:175], v[188:191], v[100:103]
	v_mfma_f32_16x16x32_bf16 v[92:95], v[148:151], v[208:211], v[92:95]
	v_mfma_f32_16x16x32_bf16 v[84:87], v[172:175], v[208:211], v[84:87]
	v_mfma_f32_16x16x32_bf16 v[76:79], v[148:151], v[216:219], v[76:79]
	v_mfma_f32_16x16x32_bf16 v[68:71], v[172:175], v[216:219], v[68:71]
	v_mfma_f32_16x16x32_bf16 v[120:123], v[152:155], v[184:187], v[120:123]
	v_mfma_f32_16x16x32_bf16 v[116:119], v[176:179], v[184:187], v[116:119]
	v_mfma_f32_16x16x32_bf16 v[108:111], v[152:155], v[192:195], v[108:111]
	v_mfma_f32_16x16x32_bf16 v[100:103], v[176:179], v[192:195], v[100:103]
	v_mfma_f32_16x16x32_bf16 v[92:95], v[152:155], v[212:215], v[92:95]
	v_mfma_f32_16x16x32_bf16 v[84:87], v[176:179], v[212:215], v[84:87]
	v_mfma_f32_16x16x32_bf16 v[76:79], v[152:155], v[220:223], v[76:79]
	v_mfma_f32_16x16x32_bf16 v[68:71], v[176:179], v[220:223], v[68:71]
	s_setprio 0
	s_barrier
; #define PG8_BAR __builtin_amdgcn_s_barrier()
; template <class Epi, class Sched, bool ALIGN_EPI = false, bool SP2 = false, bool FP8 = false, bool ABLK = false>
; __device__ __forceinline__ void gemm_phase(PG8_LAS unsigned char* lds, const Gemm g, const Sched& S, const Epi& E) {
;     ...
;             PG8_LDB(B0, 0, 0); PG8_LDB(B1, 0, 1); PG8_SCHED; PG8_LDA(At, 0, 0); PG8_STAGE(PG8_SA(1, 1), a1 + hstepA, voffA);
;             PG8_WAIT_V8_UNLESS_FIRST(t); PG8_WAIT_L(0); PG8_BAR; PG8_MMA(0, 0, At, B0); PG8_MMA(0, 1, At, B1); PG8_BAR; PG8_SCHED;
;             PG8_LDA(At, 0, 1); PG8_STAGE(PG8_SB(0, 0), b2, voffB); PG8_STAGE(PG8_SB(0, 1), b2 + hstep, voffB); PG8_STAGE(PG8_SA(0, 0), a2, voffA);
;             PG8_WAIT_V8_UNLESS_FIRST(t); PG8_WAIT_L(0); PG8_BAR; PG8_MMA(1, 0, At, B0); PG8_MMA(1, 1, At, B1); PG8_BAR; PG8_SCHED;
;             PG8_LDB(B0, 1, 0); PG8_LDB(B1, 1, 1); PG8_SCHED; PG8_LDA(At, 1, 0); PG8_STAGE(PG8_SA(0, 1), a2 + hstepA, voffA);
;             PG8_WAIT_V(8); PG8_WAIT_L(0); PG8_BAR; PG8_MMA(0, 0, At, B0); PG8_MMA(0, 1, At, B1); PG8_BAR; PG8_SCHED;
;             PG8_LDA(At, 1, 1); PG8_STAGE(PG8_SB(1, 0), b3, voffB); PG8_STAGE(PG8_SB(1, 1), b3 + hstep, voffB); PG8_STAGE(PG8_SA(1, 0), a3, voffA);
;             PG8_WAIT_V(8); PG8_WAIT_L(0); PG8_BAR; PG8_MMA(1, 0, At, B0); PG8_MMA(1, 1, At, B1); PG8_BAR; PG8_SCHED;
;             } else {
;             PG8_LDB(B0, 0, 0); PG8_SCHED; PG8_LDA(At, 0, 0); PG8_STAGE(PG8_SA(1, 1), a1 + hstepA, voffA);
;             PG8_WAIT_L(8); PG8_BAR; PG8_WAIT_L(0); PG8_MMA(0, 0, At, B0); PG8_BAR; PG8_SCHED;
;             PG8_LDB(B1, 0, 1); PG8_STAGE(PG8_SB(0, 0), b2, voffB);
;             PG8_BAR; PG8_WAIT_L(0); PG8_MMA(0, 1, At, B1); PG8_BAR;
;             PG8_LDA(At, 0, 1); PG8_STAGE(PG8_SA(0, 0), a2, voffA);
;             PG8_BAR; PG8_WAIT_L(0); PG8_MMA(1, 0, At, B0); PG8_BAR; PG8_SCHED;
;             PG8_STAGE(PG8_SB(0, 1), b2 + hstep, voffB);
;             PG8_WAIT_V(6); PG8_BAR; PG8_MMA(1, 1, At, B1); PG8_BAR;
;             PG8_LDB(B0, 1, 0); PG8_SCHED; PG8_LDA(At, 1, 0); PG8_STAGE(PG8_SA(0, 1), a2 + hstepA, voffA);
;             PG8_WAIT_L(8); PG8_BAR; PG8_WAIT_L(0); PG8_MMA(0, 0, At, B0); PG8_BAR; PG8_SCHED;
;             PG8_LDB(B1, 1, 1); PG8_STAGE(PG8_SB(1, 0), b3, voffB);
;             PG8_BAR; PG8_WAIT_L(0); PG8_MMA(0, 1, At, B1); PG8_BAR;
;             PG8_LDA(At, 1, 1); PG8_STAGE(PG8_SA(1, 0), a3, voffA);
	s_add_i32 s62, s74, s19
	v_lshl_add_u64 v[166:167], v[166:167], 0, s[34:35]
	s_mov_b32 m0, s62
	ds_read_b128 v[180:183], v170 offset:49152
	ds_read_b128 v[184:187], v170 offset:50176
	ds_read_b128 v[188:191], v170 offset:51200
	ds_read_b128 v[192:195], v170 offset:52224
	ds_read_b128 v[208:211], v170 offset:53248
	ds_read_b128 v[212:215], v170 offset:54272
	ds_read_b128 v[216:219], v170 offset:55296
	ds_read_b128 v[220:223], v170 offset:56320
	global_load_lds_dwordx4 v[166:167], off
	s_add_i32 m0, s62, 0x2000
	s_add_u32 s60, s60, 0x40080
	v_lshl_add_u64 v[166:167], v[204:205], 0, s[34:35]
	s_addc_u32 s61, s61, 0
	s_add_i32 s62, s75, s19
	global_load_lds_dwordx4 v[166:167], off
	s_mov_b32 m0, s62
	s_nop 0
	global_load_lds_dwordx4 v2, s[60:61]
	s_add_i32 m0, s62, 0x2000
	s_nop 0
	global_load_lds_dwordx4 v156, s[60:61]
	v_lshl_add_u64 v[166:167], v[206:207], 0, s[34:35]
	s_mov_b32 m0, s65
	s_nop 0
	global_load_lds_dwordx4 v[166:167], off
	v_lshl_add_u64 v[166:167], v[224:225], 0, s[34:35]
	s_mov_b32 m0, s66
	s_nop 0
	global_load_lds_dwordx4 v[166:167], off
	s_waitcnt vmcnt(8)
	s_waitcnt lgkmcnt(0)
	s_barrier
	s_setprio 1
	s_waitcnt lgkmcnt(0)
	v_mfma_f32_16x16x32_bf16 v[64:67], v[124:127], v[180:183], v[64:67]
	v_mfma_f32_16x16x32_bf16 v[56:59], v[140:143], v[180:183], v[56:59]
	v_mfma_f32_16x16x32_bf16 v[48:51], v[124:127], v[188:191], v[48:51]
	v_mfma_f32_16x16x32_bf16 v[40:43], v[140:143], v[188:191], v[40:43]
	v_mfma_f32_16x16x32_bf16 v[32:35], v[124:127], v[208:211], v[32:35]
	v_mfma_f32_16x16x32_bf16 v[24:27], v[140:143], v[208:211], v[24:27]
	v_mfma_f32_16x16x32_bf16 v[16:19], v[124:127], v[216:219], v[16:19]
	v_mfma_f32_16x16x32_bf16 v[8:11], v[140:143], v[216:219], v[8:11]
	v_mfma_f32_16x16x32_bf16 v[64:67], v[136:139], v[184:187], v[64:67]
	v_mfma_f32_16x16x32_bf16 v[56:59], v[144:147], v[184:187], v[56:59]
	v_mfma_f32_16x16x32_bf16 v[48:51], v[136:139], v[192:195], v[48:51]
	v_mfma_f32_16x16x32_bf16 v[40:43], v[144:147], v[192:195], v[40:43]
	v_mfma_f32_16x16x32_bf16 v[32:35], v[136:139], v[212:215], v[32:35]
	v_mfma_f32_16x16x32_bf16 v[24:27], v[144:147], v[212:215], v[24:27]
	v_mfma_f32_16x16x32_bf16 v[16:19], v[136:139], v[220:223], v[16:19]
	v_mfma_f32_16x16x32_bf16 v[8:11], v[144:147], v[220:223], v[8:11]
	s_setprio 0
	s_setprio 1
	v_mfma_f32_16x16x32_bf16 v[60:63], v[148:151], v[180:183], v[60:63]
	v_mfma_f32_16x16x32_bf16 v[52:55], v[172:175], v[180:183], v[52:55]
	v_mfma_f32_16x16x32_bf16 v[44:47], v[148:151], v[188:191], v[44:47]
	v_mfma_f32_16x16x32_bf16 v[36:39], v[172:175], v[188:191], v[36:39]
	v_mfma_f32_16x16x32_bf16 v[28:31], v[148:151], v[208:211], v[28:31]
	v_mfma_f32_16x16x32_bf16 v[20:23], v[172:175], v[208:211], v[20:23]
	v_mfma_f32_16x16x32_bf16 v[12:15], v[148:151], v[216:219], v[12:15]
	v_mfma_f32_16x16x32_bf16 v[4:7], v[172:175], v[216:219], v[4:7]
	v_mfma_f32_16x16x32_bf16 v[60:63], v[152:155], v[184:187], v[60:63]
	v_mfma_f32_16x16x32_bf16 v[52:55], v[176:179], v[184:187], v[52:55]
	v_mfma_f32_16x16x32_bf16 v[44:47], v[152:155], v[192:195], v[44:47]
	v_mfma_f32_16x16x32_bf16 v[36:39], v[176:179], v[192:195], v[36:39]
	v_mfma_f32_16x16x32_bf16 v[28:31], v[152:155], v[212:215], v[28:31]
	v_mfma_f32_16x16x32_bf16 v[20:23], v[176:179], v[212:215], v[20:23]
	v_mfma_f32_16x16x32_bf16 v[12:15], v[152:155], v[220:223], v[12:15]
	v_mfma_f32_16x16x32_bf16 v[4:7], v[176:179], v[220:223], v[4:7]
	s_setprio 0
	s_barrier
	s_add_u32 s58, s58, 0x100
	s_addc_u32 s59, s59, 0
	s_add_u32 s71, s71, 0x100
	s_addc_u32 s72, s72, 0
	s_cmp_gt_u32 s73, 13
	s_mov_b32 s60, s73
	s_cbranch_scc0 .LBB0_1709
	s_waitcnt vmcnt(0)
	s_and_b64 vcc, exec, s[48:49]
	s_cbranch_vccz .LBB0_1712
	s_barrier

; #define PG8_STAGE(bufoff, gbase, voff) do { _Pragma("unroll") for (int _i = 0; _i < 2; ++_i) \
;         __builtin_amdgcn_global_load_lds((const unsigned*)((const char*)(gbase) + (voff)[_i]), (PG8_LAS unsigned*)(lds + (bufoff) + ldsw + _i * 8192), 16, 0, 0); } while (0)
; #define PG8_WAIT_V(n) asm volatile("s_waitcnt vmcnt(" #n ")" ::: "memory")
; #define PG8_BAR __builtin_amdgcn_s_barrier()
; template <class Epi, class Sched, bool ALIGN_EPI = false, bool SP2 = false, bool FP8 = false, bool ABLK = false>
; __device__ __forceinline__ void gemm_phase(PG8_LAS unsigned char* lds, const Gemm g, const Sched& S, const Epi& E) {
;     ...
;     const unsigned ldsw = (unsigned)wid * 1024u;
;     const int aoff = lds_byte(wr * 64 + fr, fq * 8), boff = lds_byte(wc * 32 + fr, fq * 8);
;     ...
;         PG8_STAGE(PG8_SB(0, 0), cB, voffB); PG8_STAGE(PG8_SB(0, 1), cB + hstep, voffB); PG8_STAGE(PG8_SA(0, 0), cA, voffA); PG8_STAGE(PG8_SA(0, 1), cA + hstepA, voffA);
;         if (wr == 1) PG8_BAR;
;         PG8_WAIT_V(2); PG8_BAR;
;         PG8_STAGE(PG8_SB(1, 0), cB + kstep, voffB); PG8_STAGE(PG8_SA(1, 0), cA + kstepA, voffA); PG8_STAGE(PG8_SB(1, 1), cB + hstep + kstep, voffB);
;         PG8_WAIT_V(0); PG8_BAR;
.LBB0_1817:
	s_add_u32 s44, s38, 0x7a00000
	s_addc_u32 s45, s39, 0
	v_bfe_u32 v182, v13, 4, 2
	s_add_u32 s46, s38, 0x1c000000
	v_and_b32_e32 v1, 15, v13
	v_lshlrev_b32_e32 v19, 4, v182
	v_lshlrev_b32_e32 v13, 2, v13
	s_addc_u32 s47, s39, 0
	s_and_b32 s22, s5, 3
	s_lshl_b32 s23, s4, 6
	v_lshl_or_b32 v19, v1, 6, v19
	s_lshl_b32 s4, s4, 13
	v_and_b32_e32 v13, 32, v13
	s_add_i32 m0, s18, 0x18000
	v_lshl_add_u64 v[4:5], v[4:5], 0, s[34:35]
	v_bitop3_b32 v20, v19, s4, v13 bitop3:0xde
	s_lshl_b32 s62, s22, 5
	s_lshl_b32 s4, s22, 12
	s_waitcnt vmcnt(2)
	s_barrier
	global_load_lds_dwordx4 v[4:5], off
	s_add_i32 m0, s18, 0x1a000
	v_bitop3_b32 v183, v19, s4, v13 bitop3:0xde
	s_add_u32 s4, s52, 0x8000
	v_lshl_add_u64 v[4:5], v[6:7], 0, s[34:35]
	s_addc_u32 s5, s53, 0
	s_add_i32 s63, s18, 0x8000
	global_load_lds_dwordx4 v[4:5], off
	s_mov_b32 m0, s63
	s_add_i32 s64, s18, 0xa000
	global_load_lds_dwordx4 v168, s[4:5]
	v_lshl_add_u64 v[4:5], s[4:5], 0, v[166:167]
	s_add_u32 s4, s54, 0x58080
	s_mov_b32 m0, s64
	s_addc_u32 s5, s55, 0
	global_load_lds_dwordx4 v[4:5], off
	s_add_i32 m0, s18, 0x1c000
	s_nop 0
	global_load_lds_dwordx4 v2, s[4:5]
	s_add_i32 m0, s18, 0x1e000
	s_cmpk_lt_u32 s40, 0x100
	global_load_lds_dwordx4 v164, s[4:5]
	v_lshlrev_b32_e32 v4, 8, v14
	v_and_b32_e32 v4, 0xffffc000, v4
	v_lshl_add_u32 v4, v15, 12, v4
	v_or_b32_e32 v4, v4, v16
	v_add3_u32 v170, v4, v17, v18
	v_lshlrev_b32_e32 v4, 8, v8
	v_and_b32_e32 v4, 0xffffc000, v4
	s_waitcnt vmcnt(0)
	v_lshl_add_u32 v4, v9, 12, v4
	v_or_b32_e32 v4, v4, v10
	v_readlane_b32 s4, v252, 8
	s_cselect_b64 s[48:49], -1, 0
	v_mov_b32_e32 v171, v3
	v_add3_u32 v172, v4, v11, v12
	v_mov_b32_e32 v173, v3
	s_mov_b32 s65, 0
	v_add_u32_e32 v184, 0, v20
	v_readlane_b32 s68, v254, 58
	s_mov_b32 s69, s4
	s_barrier
	v_readlane_b32 s5, v252, 9
	s_branch .LBB0_1820

; #define PG8_STAGE(bufoff, gbase, voff) do { _Pragma("unroll") for (int _i = 0; _i < 2; ++_i) \
;         __builtin_amdgcn_global_load_lds((const unsigned*)((const char*)(gbase) + (voff)[_i]), (PG8_LAS unsigned*)(lds + (bufoff) + ldsw + _i * 8192), 16, 0, 0); } while (0)
; #define PG8_LDA(dst, b, h) do { _Pragma("unroll") for (int m = 0; m < 4; ++m) _Pragma("unroll") for (int k = 0; k < 2; ++k) dst[m][k] = *(const PG8_LAS bf16x8*)(lds + PG8_SA(b, h) + aoff + m * 2048 + k * 1024); } while (0)
; #define PG8_LDB(dst, b, h) do { _Pragma("unroll") for (int n = 0; n < 2; ++n) _Pragma("unroll") for (int k = 0; k < 2; ++k) dst[n][k] = *(const PG8_LAS bf16x8*)(lds + PG8_SB(b, h) + boff + n * 2048 + k * 1024); } while (0)
; #define PG8_WAIT_V(n) asm volatile("s_waitcnt vmcnt(" #n ")" ::: "memory")
; #define PG8_WAIT_V8_UNLESS_FIRST(t) asm volatile("s_cmp_eq_u32 %0, 0\n\ts_cbranch_scc1 .Lpg8skip%=\n\ts_waitcnt vmcnt(8)\n.Lpg8skip%=:" :: "s"(t) : "scc", "memory")
; #define PG8_WAIT_L(n) asm volatile("s_waitcnt lgkmcnt(" #n ")" ::: "memory")
; #define PG8_BAR __builtin_amdgcn_s_barrier()
; template <class Epi, class Sched, bool ALIGN_EPI = false, bool SP2 = false, bool FP8 = false, bool ABLK = false>
; __device__ __forceinline__ void gemm_phase(PG8_LAS unsigned char* lds, const Gemm g, const Sched& S, const Epi& E) {
;     ...
;             PG8_LDB(B0, 0, 0); PG8_LDB(B1, 0, 1); PG8_SCHED; PG8_LDA(At, 0, 0); PG8_STAGE(PG8_SA(1, 1), a1 + hstepA, voffA);
;             PG8_WAIT_V8_UNLESS_FIRST(t); PG8_WAIT_L(0); PG8_BAR; PG8_MMA(0, 0, At, B0); PG8_MMA(0, 1, At, B1); PG8_BAR; PG8_SCHED;
;             PG8_LDA(At, 0, 1); PG8_STAGE(PG8_SB(0, 0), b2, voffB); PG8_STAGE(PG8_SB(0, 1), b2 + hstep, voffB); PG8_STAGE(PG8_SA(0, 0), a2, voffA);
;             PG8_WAIT_V8_UNLESS_FIRST(t); PG8_WAIT_L(0); PG8_BAR; PG8_MMA(1, 0, At, B0); PG8_MMA(1, 1, At, B1); PG8_BAR; PG8_SCHED;
;             PG8_LDB(B0, 1, 0); PG8_LDB(B1, 1, 1); PG8_SCHED; PG8_LDA(At, 1, 0); PG8_STAGE(PG8_SA(0, 1), a2 + hstepA, voffA);
;             PG8_WAIT_V(8); PG8_WAIT_L(0); PG8_BAR; PG8_MMA(0, 0, At, B0); PG8_MMA(0, 1, At, B1); PG8_BAR; PG8_SCHED;
;             PG8_LDA(At, 1, 1); PG8_STAGE(PG8_SB(1, 0), b3, voffB); PG8_STAGE(PG8_SB(1, 1), b3 + hstep, voffB); PG8_STAGE(PG8_SA(1, 0), a3, voffA);
;             PG8_WAIT_V(8); PG8_WAIT_L(0); PG8_BAR; PG8_MMA(1, 0, At, B0); PG8_MMA(1, 1, At, B1); PG8_BAR; PG8_SCHED;
.Lpg8skip18:
	s_waitcnt lgkmcnt(0)
	s_barrier
	s_setprio 1
	s_waitcnt lgkmcnt(0)
	v_mfma_scale_f32_16x16x128_f8f6f4 v[160:163], v[28:35], v[186:193], v[160:163], v245, v245 op_sel_hi:[0,0,0]
	v_mfma_scale_f32_16x16x128_f8f6f4 v[156:159], v[20:27], v[186:193], v[156:159], v245, v245 op_sel_hi:[0,0,0]
	v_mfma_scale_f32_16x16x128_f8f6f4 v[144:147], v[28:35], v[208:215], v[144:147], v245, v245 op_sel_hi:[0,0,0]
	v_mfma_scale_f32_16x16x128_f8f6f4 v[140:143], v[20:27], v[208:215], v[140:143], v245, v245 op_sel_hi:[0,0,0]
	v_mfma_scale_f32_16x16x128_f8f6f4 v[128:131], v[28:35], v[216:223], v[128:131], v245, v245 op_sel_hi:[0,0,0]
	v_mfma_scale_f32_16x16x128_f8f6f4 v[124:127], v[20:27], v[216:223], v[124:127], v245, v245 op_sel_hi:[0,0,0]
	v_mfma_scale_f32_16x16x128_f8f6f4 v[112:115], v[28:35], v[228:235], v[112:115], v245, v245 op_sel_hi:[0,0,0]
	v_mfma_scale_f32_16x16x128_f8f6f4 v[108:111], v[20:27], v[228:235], v[108:111], v245, v245 op_sel_hi:[0,0,0]
	s_setprio 0
	s_setprio 1
	v_mfma_scale_f32_16x16x128_f8f6f4 v[152:155], v[12:19], v[186:193], v[152:155], v245, v245 op_sel_hi:[0,0,0]
	v_mfma_scale_f32_16x16x128_f8f6f4 v[148:151], v[4:11], v[186:193], v[148:151], v245, v245 op_sel_hi:[0,0,0]
	v_mfma_scale_f32_16x16x128_f8f6f4 v[136:139], v[12:19], v[208:215], v[136:139], v245, v245 op_sel_hi:[0,0,0]
	v_mfma_scale_f32_16x16x128_f8f6f4 v[132:135], v[4:11], v[208:215], v[132:135], v245, v245 op_sel_hi:[0,0,0]
	v_mfma_scale_f32_16x16x128_f8f6f4 v[120:123], v[12:19], v[216:223], v[120:123], v245, v245 op_sel_hi:[0,0,0]
	v_mfma_scale_f32_16x16x128_f8f6f4 v[116:119], v[4:11], v[216:223], v[116:119], v245, v245 op_sel_hi:[0,0,0]
	v_mfma_scale_f32_16x16x128_f8f6f4 v[104:107], v[12:19], v[228:235], v[104:107], v245, v245 op_sel_hi:[0,0,0]
	v_mfma_scale_f32_16x16x128_f8f6f4 v[100:103], v[4:11], v[228:235], v[100:103], v245, v245 op_sel_hi:[0,0,0]
	s_setprio 0
	s_barrier
	s_add_i32 s72, s72, s17
	v_lshl_add_u64 v[178:179], s[58:59], 0, v[2:3]
	s_mov_b32 m0, s72
	ds_read_b128 v[186:189], v184 offset:16384
	ds_read_b128 v[190:193], v184 offset:17408
	ds_read_b128 v[208:211], v184 offset:18432
	ds_read_b128 v[212:215], v184 offset:19456
	ds_read_b128 v[216:219], v184 offset:20480
	ds_read_b128 v[220:223], v184 offset:21504
	ds_read_b128 v[228:231], v184 offset:22528
	ds_read_b128 v[232:235], v184 offset:23552
	global_load_lds_dwordx4 v2, s[58:59]
	s_add_i32 m0, s72, 0x2000
	s_add_u32 s72, s58, 0x58000
	v_lshl_add_u64 v[180:181], s[58:59], 0, v[164:165]
	s_addc_u32 s73, s59, 0
	s_add_i32 s71, s71, s17
	global_load_lds_dwordx4 v164, s[58:59]
	s_mov_b32 m0, s71
	v_lshl_add_u64 v[204:205], s[60:61], 0, v[166:167]
	global_load_lds_dwordx4 v2, s[72:73]
	s_add_i32 m0, s71, 0x2000
	s_nop 0
	global_load_lds_dwordx4 v164, s[72:73]
	v_lshl_add_u64 v[194:195], s[60:61], 0, v[168:169]
	s_mov_b32 m0, s18
	s_nop 0
	global_load_lds_dwordx4 v168, s[60:61]
	s_mov_b32 m0, s19
	s_nop 0
	global_load_lds_dwordx4 v166, s[60:61]
	s_cmp_eq_u32 s70, 0
	s_cbranch_scc1 .Lpg8skip19
	s_waitcnt vmcnt(8)
.Lpg8skip19:
	s_waitcnt lgkmcnt(0)
	s_barrier
	s_setprio 1
	s_waitcnt lgkmcnt(0)
	v_mfma_scale_f32_16x16x128_f8f6f4 v[96:99], v[28:35], v[186:193], v[96:99], v245, v245 op_sel_hi:[0,0,0]
	v_mfma_scale_f32_16x16x128_f8f6f4 v[92:95], v[20:27], v[186:193], v[92:95], v245, v245 op_sel_hi:[0,0,0]
	v_mfma_scale_f32_16x16x128_f8f6f4 v[80:83], v[28:35], v[208:215], v[80:83], v245, v245 op_sel_hi:[0,0,0]
	v_mfma_scale_f32_16x16x128_f8f6f4 v[76:79], v[20:27], v[208:215], v[76:79], v245, v245 op_sel_hi:[0,0,0]
	v_mfma_scale_f32_16x16x128_f8f6f4 v[64:67], v[28:35], v[216:223], v[64:67], v245, v245 op_sel_hi:[0,0,0]
	v_mfma_scale_f32_16x16x128_f8f6f4 v[60:63], v[20:27], v[216:223], v[60:63], v245, v245 op_sel_hi:[0,0,0]
	v_mfma_scale_f32_16x16x128_f8f6f4 v[48:51], v[28:35], v[228:235], v[48:51], v245, v245 op_sel_hi:[0,0,0]
	v_mfma_scale_f32_16x16x128_f8f6f4 v[44:47], v[20:27], v[228:235], v[44:47], v245, v245 op_sel_hi:[0,0,0]
	s_setprio 0
	s_setprio 1
	v_mfma_scale_f32_16x16x128_f8f6f4 v[88:91], v[12:19], v[186:193], v[88:91], v245, v245 op_sel_hi:[0,0,0]
	v_mfma_scale_f32_16x16x128_f8f6f4 v[84:87], v[4:11], v[186:193], v[84:87], v245, v245 op_sel_hi:[0,0,0]
	v_mfma_scale_f32_16x16x128_f8f6f4 v[72:75], v[12:19], v[208:215], v[72:75], v245, v245 op_sel_hi:[0,0,0]
	v_mfma_scale_f32_16x16x128_f8f6f4 v[68:71], v[4:11], v[208:215], v[68:71], v245, v245 op_sel_hi:[0,0,0]
	v_mfma_scale_f32_16x16x128_f8f6f4 v[56:59], v[12:19], v[216:223], v[56:59], v245, v245 op_sel_hi:[0,0,0]
	v_mfma_scale_f32_16x16x128_f8f6f4 v[52:55], v[4:11], v[216:223], v[52:55], v245, v245 op_sel_hi:[0,0,0]
	v_mfma_scale_f32_16x16x128_f8f6f4 v[40:43], v[12:19], v[228:235], v[40:43], v245, v245 op_sel_hi:[0,0,0]
	v_mfma_scale_f32_16x16x128_f8f6f4 v[36:39], v[4:11], v[228:235], v[36:39], v245, v245 op_sel_hi:[0,0,0]
	s_setprio 0
	s_barrier
	s_add_i32 s60, 0, 0x18000
	s_add_i32 s61, 0, 0x1c000
	v_add_u32_e32 v16, s60, v183
	v_add_u32_e32 v32, s61, v183
	ds_read_b128 v[4:7], v16
	ds_read_b128 v[8:11], v16 offset:1024
	ds_read_b128 v[12:15], v16 offset:2048
	ds_read_b128 v[16:19], v16 offset:3072
	ds_read_b128 v[20:23], v32
	ds_read_b128 v[24:27], v32 offset:1024
	ds_read_b128 v[28:31], v32 offset:2048
	ds_read_b128 v[32:35], v32 offset:3072
	s_mov_b32 m0, s20
	v_lshl_add_u64 v[194:195], v[194:195], 0, s[24:25]
	ds_read_b128 v[186:189], v184 offset:32768
	ds_read_b128 v[190:193], v184 offset:33792
	ds_read_b128 v[208:211], v184 offset:34816
	ds_read_b128 v[212:215], v184 offset:35840
	ds_read_b128 v[216:219], v184 offset:36864
	ds_read_b128 v[220:223], v184 offset:37888
	ds_read_b128 v[228:231], v184 offset:38912
	ds_read_b128 v[232:235], v184 offset:39936
	global_load_lds_dwordx4 v[194:195], off
	v_lshl_add_u64 v[194:195], v[204:205], 0, s[24:25]
	s_mov_b32 m0, s21
	s_nop 0
	global_load_lds_dwordx4 v[194:195], off
	s_waitcnt vmcnt(8)
	s_waitcnt lgkmcnt(0)
	s_barrier
; #define PG8_BAR __builtin_amdgcn_s_barrier()
; template <class Epi, class Sched, bool ALIGN_EPI = false, bool SP2 = false, bool FP8 = false, bool ABLK = false>
; __device__ __forceinline__ void gemm_phase(PG8_LAS unsigned char* lds, const Gemm g, const Sched& S, const Epi& E) {
;     ...
;             PG8_LDB(B0, 0, 0); PG8_LDB(B1, 0, 1); PG8_SCHED; PG8_LDA(At, 0, 0); PG8_STAGE(PG8_SA(1, 1), a1 + hstepA, voffA);
;             PG8_WAIT_V8_UNLESS_FIRST(t); PG8_WAIT_L(0); PG8_BAR; PG8_MMA(0, 0, At, B0); PG8_MMA(0, 1, At, B1); PG8_BAR; PG8_SCHED;
;             PG8_LDA(At, 0, 1); PG8_STAGE(PG8_SB(0, 0), b2, voffB); PG8_STAGE(PG8_SB(0, 1), b2 + hstep, voffB); PG8_STAGE(PG8_SA(0, 0), a2, voffA);
;             PG8_WAIT_V8_UNLESS_FIRST(t); PG8_WAIT_L(0); PG8_BAR; PG8_MMA(1, 0, At, B0); PG8_MMA(1, 1, At, B1); PG8_BAR; PG8_SCHED;
;             PG8_LDB(B0, 1, 0); PG8_LDB(B1, 1, 1); PG8_SCHED; PG8_LDA(At, 1, 0); PG8_STAGE(PG8_SA(0, 1), a2 + hstepA, voffA);
;             PG8_WAIT_V(8); PG8_WAIT_L(0); PG8_BAR; PG8_MMA(0, 0, At, B0); PG8_MMA(0, 1, At, B1); PG8_BAR; PG8_SCHED;
;             PG8_LDA(At, 1, 1); PG8_STAGE(PG8_SB(1, 0), b3, voffB); PG8_STAGE(PG8_SB(1, 1), b3 + hstep, voffB); PG8_STAGE(PG8_SA(1, 0), a3, voffA);
;             PG8_WAIT_V(8); PG8_WAIT_L(0); PG8_BAR; PG8_MMA(1, 0, At, B0); PG8_MMA(1, 1, At, B1); PG8_BAR; PG8_SCHED;
;             } else {
;             PG8_LDB(B0, 0, 0); PG8_SCHED; PG8_LDA(At, 0, 0); PG8_STAGE(PG8_SA(1, 1), a1 + hstepA, voffA);
;             PG8_WAIT_L(8); PG8_BAR; PG8_WAIT_L(0); PG8_MMA(0, 0, At, B0); PG8_BAR; PG8_SCHED;
;             PG8_LDB(B1, 0, 1); PG8_STAGE(PG8_SB(0, 0), b2, voffB);
;             PG8_BAR; PG8_WAIT_L(0); PG8_MMA(0, 1, At, B1); PG8_BAR;
;             PG8_LDA(At, 0, 1); PG8_STAGE(PG8_SA(0, 0), a2, voffA);
;             PG8_BAR; PG8_WAIT_L(0); PG8_MMA(1, 0, At, B0); PG8_BAR; PG8_SCHED;
;             PG8_STAGE(PG8_SB(0, 1), b2 + hstep, voffB);
;             PG8_WAIT_V(6); PG8_BAR; PG8_MMA(1, 1, At, B1); PG8_BAR;
;             PG8_LDB(B0, 1, 0); PG8_SCHED; PG8_LDA(At, 1, 0); PG8_STAGE(PG8_SA(0, 1), a2 + hstepA, voffA);
;             PG8_WAIT_L(8); PG8_BAR; PG8_WAIT_L(0); PG8_MMA(0, 0, At, B0); PG8_BAR; PG8_SCHED;
;             PG8_LDB(B1, 1, 1); PG8_STAGE(PG8_SB(1, 0), b3, voffB);
;             PG8_BAR; PG8_WAIT_L(0); PG8_MMA(0, 1, At, B1); PG8_BAR;
;             PG8_LDA(At, 1, 1); PG8_STAGE(PG8_SA(1, 0), a3, voffA);
	s_setprio 1
	s_waitcnt lgkmcnt(0)
	v_mfma_scale_f32_16x16x128_f8f6f4 v[160:163], v[4:11], v[186:193], v[160:163], v245, v245 op_sel_hi:[0,0,0]
	v_mfma_scale_f32_16x16x128_f8f6f4 v[156:159], v[12:19], v[186:193], v[156:159], v245, v245 op_sel_hi:[0,0,0]
	v_mfma_scale_f32_16x16x128_f8f6f4 v[144:147], v[4:11], v[208:215], v[144:147], v245, v245 op_sel_hi:[0,0,0]
	v_mfma_scale_f32_16x16x128_f8f6f4 v[140:143], v[12:19], v[208:215], v[140:143], v245, v245 op_sel_hi:[0,0,0]
	v_mfma_scale_f32_16x16x128_f8f6f4 v[128:131], v[4:11], v[216:223], v[128:131], v245, v245 op_sel_hi:[0,0,0]
	v_mfma_scale_f32_16x16x128_f8f6f4 v[124:127], v[12:19], v[216:223], v[124:127], v245, v245 op_sel_hi:[0,0,0]
	v_mfma_scale_f32_16x16x128_f8f6f4 v[112:115], v[4:11], v[228:235], v[112:115], v245, v245 op_sel_hi:[0,0,0]
	v_mfma_scale_f32_16x16x128_f8f6f4 v[108:111], v[12:19], v[228:235], v[108:111], v245, v245 op_sel_hi:[0,0,0]
	s_setprio 0
	s_setprio 1
	v_mfma_scale_f32_16x16x128_f8f6f4 v[152:155], v[20:27], v[186:193], v[152:155], v245, v245 op_sel_hi:[0,0,0]
	v_mfma_scale_f32_16x16x128_f8f6f4 v[148:151], v[28:35], v[186:193], v[148:151], v245, v245 op_sel_hi:[0,0,0]
	v_mfma_scale_f32_16x16x128_f8f6f4 v[136:139], v[20:27], v[208:215], v[136:139], v245, v245 op_sel_hi:[0,0,0]
	v_mfma_scale_f32_16x16x128_f8f6f4 v[132:135], v[28:35], v[208:215], v[132:135], v245, v245 op_sel_hi:[0,0,0]
	v_mfma_scale_f32_16x16x128_f8f6f4 v[120:123], v[20:27], v[216:223], v[120:123], v245, v245 op_sel_hi:[0,0,0]
	v_mfma_scale_f32_16x16x128_f8f6f4 v[116:119], v[28:35], v[216:223], v[116:119], v245, v245 op_sel_hi:[0,0,0]
	v_mfma_scale_f32_16x16x128_f8f6f4 v[104:107], v[20:27], v[228:235], v[104:107], v245, v245 op_sel_hi:[0,0,0]
	v_mfma_scale_f32_16x16x128_f8f6f4 v[100:103], v[28:35], v[228:235], v[100:103], v245, v245 op_sel_hi:[0,0,0]
	s_setprio 0
	s_barrier
	s_add_i32 s60, s60, s17
	v_lshl_add_u64 v[178:179], v[178:179], 0, s[34:35]
	s_mov_b32 m0, s60
	ds_read_b128 v[186:189], v184 offset:49152
	ds_read_b128 v[190:193], v184 offset:50176
	ds_read_b128 v[208:211], v184 offset:51200
	ds_read_b128 v[212:215], v184 offset:52224
	ds_read_b128 v[216:219], v184 offset:53248
	ds_read_b128 v[220:223], v184 offset:54272
	ds_read_b128 v[228:231], v184 offset:55296
	ds_read_b128 v[232:235], v184 offset:56320
	global_load_lds_dwordx4 v[178:179], off
	s_add_i32 m0, s60, 0x2000
	s_add_u32 s58, s58, 0x58080
	v_lshl_add_u64 v[178:179], v[180:181], 0, s[34:35]
	s_addc_u32 s59, s59, 0
	s_add_i32 s60, s61, s17
	global_load_lds_dwordx4 v[178:179], off
	s_mov_b32 m0, s60
	s_nop 0
	global_load_lds_dwordx4 v2, s[58:59]
	s_add_i32 m0, s60, 0x2000
	s_nop 0
	global_load_lds_dwordx4 v164, s[58:59]
	s_mov_b32 m0, s63
	s_nop 0
	global_load_lds_dwordx4 v168, s[56:57]
	s_mov_b32 m0, s64
	s_nop 0
	global_load_lds_dwordx4 v166, s[56:57]
	s_waitcnt vmcnt(8)
	s_waitcnt lgkmcnt(0)
	s_barrier
	s_setprio 1
	s_waitcnt lgkmcnt(0)
	v_mfma_scale_f32_16x16x128_f8f6f4 v[96:99], v[4:11], v[186:193], v[96:99], v245, v245 op_sel_hi:[0,0,0]
	v_mfma_scale_f32_16x16x128_f8f6f4 v[92:95], v[12:19], v[186:193], v[92:95], v245, v245 op_sel_hi:[0,0,0]
	v_mfma_scale_f32_16x16x128_f8f6f4 v[80:83], v[4:11], v[208:215], v[80:83], v245, v245 op_sel_hi:[0,0,0]
	v_mfma_scale_f32_16x16x128_f8f6f4 v[76:79], v[12:19], v[208:215], v[76:79], v245, v245 op_sel_hi:[0,0,0]
	v_mfma_scale_f32_16x16x128_f8f6f4 v[64:67], v[4:11], v[216:223], v[64:67], v245, v245 op_sel_hi:[0,0,0]
	v_mfma_scale_f32_16x16x128_f8f6f4 v[60:63], v[12:19], v[216:223], v[60:63], v245, v245 op_sel_hi:[0,0,0]
	v_mfma_scale_f32_16x16x128_f8f6f4 v[48:51], v[4:11], v[228:235], v[48:51], v245, v245 op_sel_hi:[0,0,0]
	v_mfma_scale_f32_16x16x128_f8f6f4 v[44:47], v[12:19], v[228:235], v[44:47], v245, v245 op_sel_hi:[0,0,0]
	s_setprio 0
	s_setprio 1
	v_mfma_scale_f32_16x16x128_f8f6f4 v[88:91], v[20:27], v[186:193], v[88:91], v245, v245 op_sel_hi:[0,0,0]
	v_mfma_scale_f32_16x16x128_f8f6f4 v[84:87], v[28:35], v[186:193], v[84:87], v245, v245 op_sel_hi:[0,0,0]
	v_mfma_scale_f32_16x16x128_f8f6f4 v[72:75], v[20:27], v[208:215], v[72:75], v245, v245 op_sel_hi:[0,0,0]
	v_mfma_scale_f32_16x16x128_f8f6f4 v[68:71], v[28:35], v[208:215], v[68:71], v245, v245 op_sel_hi:[0,0,0]
	v_mfma_scale_f32_16x16x128_f8f6f4 v[56:59], v[20:27], v[216:223], v[56:59], v245, v245 op_sel_hi:[0,0,0]
	v_mfma_scale_f32_16x16x128_f8f6f4 v[52:55], v[28:35], v[216:223], v[52:55], v245, v245 op_sel_hi:[0,0,0]
	v_mfma_scale_f32_16x16x128_f8f6f4 v[40:43], v[20:27], v[228:235], v[40:43], v245, v245 op_sel_hi:[0,0,0]
	v_mfma_scale_f32_16x16x128_f8f6f4 v[36:39], v[28:35], v[228:235], v[36:39], v245, v245 op_sel_hi:[0,0,0]
	s_setprio 0
	s_barrier
	s_add_u32 s4, s4, 0x100
	s_addc_u32 s5, s5, 0
	s_add_u32 s54, s54, 0x10000
	s_addc_u32 s55, s55, 0
	s_cmp_gt_u32 s70, 19
	s_cbranch_scc0 .LBB0_1831
	s_waitcnt vmcnt(0)
	s_nop 15
	s_nop 15
	s_and_b64 vcc, exec, s[48:49]
	s_cbranch_vccz .LBB0_1834
	s_barrier
